# K-loop LDS-DMA addressing: uniform k-offset added to the 64-bit scalar base (SALU) instead of per-lane VALU add, in 9 GEMM phases
# speedup vs baseline: 1.0053x; 1.0053x over previous
.LBB0_296:
	ds_read_b128 v[160:163], v144
	ds_read_b128 v[164:167], v145
	ds_read_b128 v[168:171], v140
	ds_read_b128 v[172:175], v141
	ds_read_b128 v[176:179], v146
	ds_read_b128 v[180:183], v147
	ds_read_b128 v[184:187], v148
	ds_read_b128 v[188:191], v149
	s_add_i32 s72, s14, 0x80
	s_cmp_eq_u32 s54, s71
	s_cselect_b32 s73, s13, s70
	s_cselect_b32 s72, s15, s72
	s_add_u32 s98, s4, s14
	s_addc_u32 s99, s5, 0
	s_add_i32 m0, s22, 0xc000
	ds_read_b128 v[192:195], v158
	ds_read_b128 v[196:199], v158 offset:1024
	ds_read_b128 v[200:203], v158 offset:2048
	ds_read_b128 v[204:207], v158 offset:3072
	ds_read_b128 v[214:217], v158 offset:4096
	ds_read_b128 v[218:221], v158 offset:5120
	ds_read_b128 v[222:225], v158 offset:6144
	ds_read_b128 v[226:229], v158 offset:7168
	global_load_lds_dwordx4 v157, s[98:99]
	s_add_u32 s100, s4, s14
	s_addc_u32 s101, s5, 0
	s_add_i32 m0, s22, 0xe000
	s_nop 0
	global_load_lds_dwordx4 v156, s[100:101]
	s_waitcnt vmcnt(8)
	s_waitcnt lgkmcnt(0)
	s_barrier
	s_setprio 1
	s_waitcnt lgkmcnt(0)
	v_mfma_f32_16x16x32_bf16 v[122:125], v[168:171], v[192:195], v[122:125]
	v_mfma_f32_16x16x32_bf16 v[126:129], v[164:167], v[192:195], v[126:129]
	v_mfma_f32_16x16x32_bf16 v[110:113], v[168:171], v[200:203], v[110:113]
	v_mfma_f32_16x16x32_bf16 v[106:109], v[164:167], v[200:203], v[106:109]
	v_mfma_f32_16x16x32_bf16 v[94:97], v[168:171], v[214:217], v[94:97]
	v_mfma_f32_16x16x32_bf16 v[90:93], v[164:167], v[214:217], v[90:93]
	v_mfma_f32_16x16x32_bf16 v[78:81], v[168:171], v[222:225], v[78:81]
	v_mfma_f32_16x16x32_bf16 v[74:77], v[164:167], v[222:225], v[74:77]
	v_mfma_f32_16x16x32_bf16 v[122:125], v[160:163], v[196:199], v[122:125]
	v_mfma_f32_16x16x32_bf16 v[126:129], v[176:179], v[196:199], v[126:129]
	v_mfma_f32_16x16x32_bf16 v[110:113], v[160:163], v[204:207], v[110:113]
	v_mfma_f32_16x16x32_bf16 v[106:109], v[176:179], v[204:207], v[106:109]
	v_mfma_f32_16x16x32_bf16 v[94:97], v[160:163], v[218:221], v[94:97]
	v_mfma_f32_16x16x32_bf16 v[90:93], v[176:179], v[218:221], v[90:93]
	v_mfma_f32_16x16x32_bf16 v[78:81], v[160:163], v[226:229], v[78:81]
	v_mfma_f32_16x16x32_bf16 v[74:77], v[176:179], v[226:229], v[74:77]
	s_setprio 0
	s_setprio 1
	v_mfma_f32_16x16x32_bf16 v[118:121], v[172:175], v[192:195], v[118:121]
	v_mfma_f32_16x16x32_bf16 v[114:117], v[184:187], v[192:195], v[114:117]
	v_mfma_f32_16x16x32_bf16 v[102:105], v[172:175], v[200:203], v[102:105]
	v_mfma_f32_16x16x32_bf16 v[98:101], v[184:187], v[200:203], v[98:101]
	v_mfma_f32_16x16x32_bf16 v[86:89], v[172:175], v[214:217], v[86:89]
	v_mfma_f32_16x16x32_bf16 v[82:85], v[184:187], v[214:217], v[82:85]
	v_mfma_f32_16x16x32_bf16 v[70:73], v[172:175], v[222:225], v[70:73]
	v_mfma_f32_16x16x32_bf16 v[66:69], v[184:187], v[222:225], v[66:69]
	v_mfma_f32_16x16x32_bf16 v[118:121], v[180:183], v[196:199], v[118:121]
	v_mfma_f32_16x16x32_bf16 v[114:117], v[188:191], v[196:199], v[114:117]
	v_mfma_f32_16x16x32_bf16 v[102:105], v[180:183], v[204:207], v[102:105]
	v_mfma_f32_16x16x32_bf16 v[98:101], v[188:191], v[204:207], v[98:101]
	v_mfma_f32_16x16x32_bf16 v[86:89], v[180:183], v[218:221], v[86:89]
	v_mfma_f32_16x16x32_bf16 v[82:85], v[188:191], v[218:221], v[82:85]
	v_mfma_f32_16x16x32_bf16 v[70:73], v[180:183], v[226:229], v[70:73]
	v_mfma_f32_16x16x32_bf16 v[66:69], v[188:191], v[226:229], v[66:69]
	s_setprio 0
	s_barrier
	s_mov_b32 m0, s23
	s_add_u32 s98, s20, s73
	s_addc_u32 s99, s21, 0
	ds_read_b128 v[192:195], v158 offset:16384
	ds_read_b128 v[196:199], v158 offset:17408
	ds_read_b128 v[200:203], v158 offset:18432
	ds_read_b128 v[204:207], v158 offset:19456
	ds_read_b128 v[214:217], v158 offset:20480
	ds_read_b128 v[218:221], v158 offset:21504
	ds_read_b128 v[222:225], v158 offset:22528
	ds_read_b128 v[226:229], v158 offset:23552
	global_load_lds_dwordx4 v134, s[98:99]
	s_add_u32 s100, s98, s17
	s_addc_u32 s101, s99, 0
	s_mov_b32 m0, s28
	s_nop 0
	global_load_lds_dwordx4 v134, s[100:101]
	s_add_u32 s98, s20, s73
	s_addc_u32 s99, s21, 0
	s_mov_b32 m0, s29
	s_nop 0
	global_load_lds_dwordx4 v135, s[98:99]
	s_add_u32 s100, s98, s17
	s_addc_u32 s101, s99, 0
	s_mov_b32 m0, s30
	s_nop 0
	global_load_lds_dwordx4 v135, s[100:101]
	s_add_u32 s98, s4, s72
	s_addc_u32 s99, s5, 0
	s_mov_b32 m0, s22
	s_nop 0
	global_load_lds_dwordx4 v1, s[98:99]
	s_add_u32 s100, s98, s16
	s_addc_u32 s101, s99, 0
	s_mov_b32 m0, s31
	s_nop 0
	global_load_lds_dwordx4 v1, s[100:101]
	s_waitcnt vmcnt(8)
	s_waitcnt lgkmcnt(0)
	s_barrier
	s_setprio 1
	s_waitcnt lgkmcnt(0)
	v_mfma_f32_16x16x32_bf16 v[62:65], v[168:171], v[192:195], v[62:65]
	v_mfma_f32_16x16x32_bf16 v[58:61], v[164:167], v[192:195], v[58:61]
	v_mfma_f32_16x16x32_bf16 v[46:49], v[168:171], v[200:203], v[46:49]
	v_mfma_f32_16x16x32_bf16 v[42:45], v[164:167], v[200:203], v[42:45]
	v_mfma_f32_16x16x32_bf16 v[30:33], v[168:171], v[214:217], v[30:33]
	v_mfma_f32_16x16x32_bf16 v[26:29], v[164:167], v[214:217], v[26:29]
	v_mfma_f32_16x16x32_bf16 v[14:17], v[168:171], v[222:225], v[14:17]
	v_mfma_f32_16x16x32_bf16 v[10:13], v[164:167], v[222:225], v[10:13]
	v_mfma_f32_16x16x32_bf16 v[62:65], v[160:163], v[196:199], v[62:65]
	v_mfma_f32_16x16x32_bf16 v[58:61], v[176:179], v[196:199], v[58:61]
	v_mfma_f32_16x16x32_bf16 v[46:49], v[160:163], v[204:207], v[46:49]
	v_mfma_f32_16x16x32_bf16 v[42:45], v[176:179], v[204:207], v[42:45]
	v_mfma_f32_16x16x32_bf16 v[30:33], v[160:163], v[218:221], v[30:33]
	v_mfma_f32_16x16x32_bf16 v[26:29], v[176:179], v[218:221], v[26:29]
	v_mfma_f32_16x16x32_bf16 v[14:17], v[160:163], v[226:229], v[14:17]
	v_mfma_f32_16x16x32_bf16 v[10:13], v[176:179], v[226:229], v[10:13]
	s_setprio 0
	s_setprio 1
	v_mfma_f32_16x16x32_bf16 v[54:57], v[172:175], v[192:195], v[54:57]
	v_mfma_f32_16x16x32_bf16 v[50:53], v[184:187], v[192:195], v[50:53]
	v_mfma_f32_16x16x32_bf16 v[38:41], v[172:175], v[200:203], v[38:41]
	v_mfma_f32_16x16x32_bf16 v[34:37], v[184:187], v[200:203], v[34:37]
	v_mfma_f32_16x16x32_bf16 v[22:25], v[172:175], v[214:217], v[22:25]
	v_mfma_f32_16x16x32_bf16 v[18:21], v[184:187], v[214:217], v[18:21]
	v_mfma_f32_16x16x32_bf16 v[6:9], v[172:175], v[222:225], v[6:9]
	v_mfma_f32_16x16x32_bf16 v[2:5], v[184:187], v[222:225], v[2:5]
	v_mfma_f32_16x16x32_bf16 v[54:57], v[180:183], v[196:199], v[54:57]
	v_mfma_f32_16x16x32_bf16 v[50:53], v[188:191], v[196:199], v[50:53]
	v_mfma_f32_16x16x32_bf16 v[38:41], v[180:183], v[204:207], v[38:41]
	v_mfma_f32_16x16x32_bf16 v[34:37], v[188:191], v[204:207], v[34:37]
	v_mfma_f32_16x16x32_bf16 v[22:25], v[180:183], v[218:221], v[22:25]
	v_mfma_f32_16x16x32_bf16 v[18:21], v[188:191], v[218:221], v[18:21]
	v_mfma_f32_16x16x32_bf16 v[6:9], v[180:183], v[226:229], v[6:9]
	v_mfma_f32_16x16x32_bf16 v[2:5], v[188:191], v[226:229], v[2:5]
	s_setprio 0
	s_barrier
	ds_read_b128 v[160:163], v150
	ds_read_b128 v[164:167], v151
	ds_read_b128 v[168:171], v142
	ds_read_b128 v[172:175], v143
	ds_read_b128 v[176:179], v152
	ds_read_b128 v[180:183], v153
	ds_read_b128 v[184:187], v154
	ds_read_b128 v[188:191], v155
	s_mov_b32 m0, s35
	s_add_u32 s98, s4, s72
	s_addc_u32 s99, s5, 0
	ds_read_b128 v[192:195], v158 offset:32768
	ds_read_b128 v[196:199], v158 offset:33792
	ds_read_b128 v[200:203], v158 offset:34816
	ds_read_b128 v[204:207], v158 offset:35840
	ds_read_b128 v[214:217], v158 offset:36864
	ds_read_b128 v[218:221], v158 offset:37888
	ds_read_b128 v[222:225], v158 offset:38912
	ds_read_b128 v[226:229], v158 offset:39936
	global_load_lds_dwordx4 v136, s[98:99]
	s_add_u32 s100, s98, s16
	s_addc_u32 s101, s99, 0
	s_mov_b32 m0, s44
	s_nop 0
	global_load_lds_dwordx4 v136, s[100:101]
	s_waitcnt vmcnt(8)
	s_waitcnt lgkmcnt(0)
	s_barrier
	s_setprio 1
	s_waitcnt lgkmcnt(0)
	v_mfma_f32_16x16x32_bf16 v[122:125], v[168:171], v[192:195], v[122:125]
	v_mfma_f32_16x16x32_bf16 v[126:129], v[164:167], v[192:195], v[126:129]
	v_mfma_f32_16x16x32_bf16 v[110:113], v[168:171], v[200:203], v[110:113]
	v_mfma_f32_16x16x32_bf16 v[106:109], v[164:167], v[200:203], v[106:109]
	v_mfma_f32_16x16x32_bf16 v[94:97], v[168:171], v[214:217], v[94:97]
	v_mfma_f32_16x16x32_bf16 v[90:93], v[164:167], v[214:217], v[90:93]
	v_mfma_f32_16x16x32_bf16 v[78:81], v[168:171], v[222:225], v[78:81]
	v_mfma_f32_16x16x32_bf16 v[74:77], v[164:167], v[222:225], v[74:77]
	v_mfma_f32_16x16x32_bf16 v[122:125], v[160:163], v[196:199], v[122:125]
	v_mfma_f32_16x16x32_bf16 v[126:129], v[176:179], v[196:199], v[126:129]
	v_mfma_f32_16x16x32_bf16 v[110:113], v[160:163], v[204:207], v[110:113]
	v_mfma_f32_16x16x32_bf16 v[106:109], v[176:179], v[204:207], v[106:109]
	v_mfma_f32_16x16x32_bf16 v[94:97], v[160:163], v[218:221], v[94:97]
	v_mfma_f32_16x16x32_bf16 v[90:93], v[176:179], v[218:221], v[90:93]
	v_mfma_f32_16x16x32_bf16 v[78:81], v[160:163], v[226:229], v[78:81]
	v_mfma_f32_16x16x32_bf16 v[74:77], v[176:179], v[226:229], v[74:77]
	s_setprio 0
	s_setprio 1
	v_mfma_f32_16x16x32_bf16 v[118:121], v[172:175], v[192:195], v[118:121]
	v_mfma_f32_16x16x32_bf16 v[114:117], v[184:187], v[192:195], v[114:117]
	v_mfma_f32_16x16x32_bf16 v[102:105], v[172:175], v[200:203], v[102:105]
	v_mfma_f32_16x16x32_bf16 v[98:101], v[184:187], v[200:203], v[98:101]
	v_mfma_f32_16x16x32_bf16 v[86:89], v[172:175], v[214:217], v[86:89]
	v_mfma_f32_16x16x32_bf16 v[82:85], v[184:187], v[214:217], v[82:85]
	v_mfma_f32_16x16x32_bf16 v[70:73], v[172:175], v[222:225], v[70:73]
	v_mfma_f32_16x16x32_bf16 v[66:69], v[184:187], v[222:225], v[66:69]
	v_mfma_f32_16x16x32_bf16 v[118:121], v[180:183], v[196:199], v[118:121]
	v_mfma_f32_16x16x32_bf16 v[114:117], v[188:191], v[196:199], v[114:117]
	v_mfma_f32_16x16x32_bf16 v[102:105], v[180:183], v[204:207], v[102:105]
	v_mfma_f32_16x16x32_bf16 v[98:101], v[188:191], v[204:207], v[98:101]
	v_mfma_f32_16x16x32_bf16 v[86:89], v[180:183], v[218:221], v[86:89]
	v_mfma_f32_16x16x32_bf16 v[82:85], v[188:191], v[218:221], v[82:85]
	v_mfma_f32_16x16x32_bf16 v[70:73], v[180:183], v[226:229], v[70:73]
	v_mfma_f32_16x16x32_bf16 v[66:69], v[188:191], v[226:229], v[66:69]
	s_setprio 0
	s_barrier
	s_addk_i32 s73, 0x80
	s_mov_b32 m0, s46
	s_add_u32 s98, s20, s73
	s_addc_u32 s99, s21, 0
	ds_read_b128 v[192:195], v158 offset:49152
	ds_read_b128 v[196:199], v158 offset:50176
	ds_read_b128 v[200:203], v158 offset:51200
	ds_read_b128 v[204:207], v158 offset:52224
	ds_read_b128 v[214:217], v158 offset:53248
	ds_read_b128 v[218:221], v158 offset:54272
	ds_read_b128 v[222:225], v158 offset:55296
	ds_read_b128 v[226:229], v158 offset:56320
	global_load_lds_dwordx4 v134, s[98:99]
	s_add_u32 s100, s98, s17
	s_addc_u32 s101, s99, 0
	s_mov_b32 m0, s47
	s_nop 0
	global_load_lds_dwordx4 v134, s[100:101]
	s_add_u32 s98, s20, s73
	s_addc_u32 s99, s21, 0
	s_mov_b32 m0, s50
	s_nop 0
	global_load_lds_dwordx4 v135, s[98:99]
	s_add_u32 s100, s98, s17
	s_addc_u32 s101, s99, 0
	s_mov_b32 m0, s51
	s_nop 0
	global_load_lds_dwordx4 v135, s[100:101]
	s_add_u32 s98, s4, s72
	s_addc_u32 s99, s5, 0
	s_mov_b32 m0, s48
	s_nop 0
	global_load_lds_dwordx4 v137, s[98:99]
	s_add_u32 s100, s98, s16
	s_addc_u32 s101, s99, 0
	s_mov_b32 m0, s49
	s_nop 0
	global_load_lds_dwordx4 v137, s[100:101]
	s_waitcnt vmcnt(8)
	s_waitcnt lgkmcnt(0)
	s_barrier
	s_setprio 1
	s_waitcnt lgkmcnt(0)
	v_mfma_f32_16x16x32_bf16 v[62:65], v[168:171], v[192:195], v[62:65]
	v_mfma_f32_16x16x32_bf16 v[58:61], v[164:167], v[192:195], v[58:61]
	v_mfma_f32_16x16x32_bf16 v[46:49], v[168:171], v[200:203], v[46:49]
	v_mfma_f32_16x16x32_bf16 v[42:45], v[164:167], v[200:203], v[42:45]
	v_mfma_f32_16x16x32_bf16 v[30:33], v[168:171], v[214:217], v[30:33]
	v_mfma_f32_16x16x32_bf16 v[26:29], v[164:167], v[214:217], v[26:29]
	v_mfma_f32_16x16x32_bf16 v[14:17], v[168:171], v[222:225], v[14:17]
	v_mfma_f32_16x16x32_bf16 v[10:13], v[164:167], v[222:225], v[10:13]
	v_mfma_f32_16x16x32_bf16 v[62:65], v[160:163], v[196:199], v[62:65]
	v_mfma_f32_16x16x32_bf16 v[58:61], v[176:179], v[196:199], v[58:61]
	v_mfma_f32_16x16x32_bf16 v[46:49], v[160:163], v[204:207], v[46:49]
	v_mfma_f32_16x16x32_bf16 v[42:45], v[176:179], v[204:207], v[42:45]
	v_mfma_f32_16x16x32_bf16 v[30:33], v[160:163], v[218:221], v[30:33]
	v_mfma_f32_16x16x32_bf16 v[26:29], v[176:179], v[218:221], v[26:29]
	v_mfma_f32_16x16x32_bf16 v[14:17], v[160:163], v[226:229], v[14:17]
	v_mfma_f32_16x16x32_bf16 v[10:13], v[176:179], v[226:229], v[10:13]
	s_setprio 0
	s_setprio 1
	v_mfma_f32_16x16x32_bf16 v[54:57], v[172:175], v[192:195], v[54:57]
	v_mfma_f32_16x16x32_bf16 v[50:53], v[184:187], v[192:195], v[50:53]
	v_mfma_f32_16x16x32_bf16 v[38:41], v[172:175], v[200:203], v[38:41]
	v_mfma_f32_16x16x32_bf16 v[34:37], v[184:187], v[200:203], v[34:37]
	v_mfma_f32_16x16x32_bf16 v[22:25], v[172:175], v[214:217], v[22:25]
	v_mfma_f32_16x16x32_bf16 v[18:21], v[184:187], v[214:217], v[18:21]
	v_mfma_f32_16x16x32_bf16 v[6:9], v[172:175], v[222:225], v[6:9]
	v_mfma_f32_16x16x32_bf16 v[2:5], v[184:187], v[222:225], v[2:5]
	v_mfma_f32_16x16x32_bf16 v[54:57], v[180:183], v[196:199], v[54:57]
	v_mfma_f32_16x16x32_bf16 v[50:53], v[188:191], v[196:199], v[50:53]
	v_mfma_f32_16x16x32_bf16 v[38:41], v[180:183], v[204:207], v[38:41]
	v_mfma_f32_16x16x32_bf16 v[34:37], v[188:191], v[204:207], v[34:37]
	v_mfma_f32_16x16x32_bf16 v[22:25], v[180:183], v[218:221], v[22:25]
	v_mfma_f32_16x16x32_bf16 v[18:21], v[188:191], v[218:221], v[18:21]
	v_mfma_f32_16x16x32_bf16 v[6:9], v[180:183], v[226:229], v[6:9]
	v_mfma_f32_16x16x32_bf16 v[2:5], v[188:191], v[226:229], v[2:5]
	s_setprio 0
	s_barrier
	s_add_i32 s71, s71, 2
	s_addk_i32 s14, 0x100
	s_addk_i32 s70, 0x100
	s_cmp_ge_i32 s71, s52
	s_cbranch_scc0 .LBB0_296

.LBB0_584:
	ds_read_b128 v[54:57], v46
	ds_read_b128 v[58:61], v48
	s_add_i32 s67, s22, 0x80
	s_cmp_eq_u32 s58, s66
	s_cselect_b32 s68, s23, s65
	s_cselect_b32 s67, s21, s67
	s_add_u32 s98, s4, s22
	s_addc_u32 s99, s5, 0
	s_add_i32 m0, s29, 0xc000
	ds_read_b128 v[62:65], v52
	ds_read_b128 v[66:69], v52 offset:1024
	ds_read_b128 v[70:73], v52 offset:2048
	ds_read_b128 v[74:77], v52 offset:3072
	ds_read_b128 v[78:81], v52 offset:4096
	ds_read_b128 v[82:85], v52 offset:5120
	ds_read_b128 v[86:89], v52 offset:6144
	ds_read_b128 v[90:93], v52 offset:7168
	global_load_lds_dwordx4 v51, s[98:99]
	s_add_u32 s100, s4, s22
	s_addc_u32 s101, s5, 0
	s_add_i32 m0, s29, 0xe000
	s_nop 0
	global_load_lds_dwordx4 v50, s[100:101]
	s_waitcnt vmcnt(8)
	s_waitcnt lgkmcnt(0)
	s_barrier
	s_setprio 1
	s_waitcnt lgkmcnt(0)
	v_mfma_f32_16x16x32_bf16 v[26:29], v[54:57], v[62:65], v[26:29]
	v_mfma_f32_16x16x32_bf16 v[30:33], v[54:57], v[70:73], v[30:33]
	v_mfma_f32_16x16x32_bf16 v[22:25], v[54:57], v[78:81], v[22:25]
	v_mfma_f32_16x16x32_bf16 v[18:21], v[54:57], v[86:89], v[18:21]
	v_mfma_f32_16x16x32_bf16 v[26:29], v[58:61], v[66:69], v[26:29]
	v_mfma_f32_16x16x32_bf16 v[30:33], v[58:61], v[74:77], v[30:33]
	v_mfma_f32_16x16x32_bf16 v[22:25], v[58:61], v[82:85], v[22:25]
	v_mfma_f32_16x16x32_bf16 v[18:21], v[58:61], v[90:93], v[18:21]
	s_setprio 0
	s_setprio 1
	s_setprio 0
	s_barrier
	s_mov_b32 m0, s30
	s_add_u32 s98, s6, s68
	s_addc_u32 s99, s7, 0
	ds_read_b128 v[62:65], v52 offset:16384
	ds_read_b128 v[66:69], v52 offset:17408
	ds_read_b128 v[70:73], v52 offset:18432
	ds_read_b128 v[74:77], v52 offset:19456
	ds_read_b128 v[78:81], v52 offset:20480
	ds_read_b128 v[82:85], v52 offset:21504
	ds_read_b128 v[86:89], v52 offset:22528
	ds_read_b128 v[90:93], v52 offset:23552
	global_load_lds_dwordx4 v40, s[98:99]
	s_add_u32 s100, s98, s28
	s_addc_u32 s101, s99, 0
	s_mov_b32 m0, s31
	s_nop 0
	global_load_lds_dwordx4 v40, s[100:101]
	s_add_u32 s98, s6, s68
	s_addc_u32 s99, s7, 0
	s_mov_b32 m0, s35
	s_nop 0
	global_load_lds_dwordx4 v41, s[98:99]
	s_add_u32 s100, s98, s28
	s_addc_u32 s101, s99, 0
	s_mov_b32 m0, s44
	s_nop 0
	global_load_lds_dwordx4 v41, s[100:101]
	s_add_u32 s98, s4, s67
	s_addc_u32 s99, s5, 0
	s_mov_b32 m0, s29
	s_nop 0
	global_load_lds_dwordx4 v1, s[98:99]
	s_add_u32 s100, s98, s25
	s_addc_u32 s101, s99, 0
	s_mov_b32 m0, s45
	s_nop 0
	global_load_lds_dwordx4 v1, s[100:101]
	s_waitcnt vmcnt(8)
	s_waitcnt lgkmcnt(0)
	s_barrier
	s_setprio 1
	s_waitcnt lgkmcnt(0)
	v_mfma_f32_16x16x32_bf16 v[14:17], v[54:57], v[62:65], v[14:17]
	v_mfma_f32_16x16x32_bf16 v[10:13], v[54:57], v[70:73], v[10:13]
	v_mfma_f32_16x16x32_bf16 v[6:9], v[54:57], v[78:81], v[6:9]
	v_mfma_f32_16x16x32_bf16 v[2:5], v[54:57], v[86:89], v[2:5]
	v_mfma_f32_16x16x32_bf16 v[14:17], v[58:61], v[66:69], v[14:17]
	v_mfma_f32_16x16x32_bf16 v[10:13], v[58:61], v[74:77], v[10:13]
	v_mfma_f32_16x16x32_bf16 v[6:9], v[58:61], v[82:85], v[6:9]
	v_mfma_f32_16x16x32_bf16 v[2:5], v[58:61], v[90:93], v[2:5]
	s_setprio 0
	s_setprio 1
	s_setprio 0
	s_barrier
	ds_read_b128 v[54:57], v47
	ds_read_b128 v[58:61], v49
	s_mov_b32 m0, s46
	s_add_u32 s98, s4, s67
	s_addc_u32 s99, s5, 0
	ds_read_b128 v[62:65], v52 offset:32768
	ds_read_b128 v[66:69], v52 offset:33792
	ds_read_b128 v[70:73], v52 offset:34816
	ds_read_b128 v[74:77], v52 offset:35840
	ds_read_b128 v[78:81], v52 offset:36864
	ds_read_b128 v[82:85], v52 offset:37888
	ds_read_b128 v[86:89], v52 offset:38912
	ds_read_b128 v[90:93], v52 offset:39936
	global_load_lds_dwordx4 v42, s[98:99]
	s_add_u32 s100, s98, s25
	s_addc_u32 s101, s99, 0
	s_mov_b32 m0, s47
	s_nop 0
	global_load_lds_dwordx4 v42, s[100:101]
	s_waitcnt vmcnt(8)
	s_waitcnt lgkmcnt(0)
	s_barrier
	s_setprio 1
	s_waitcnt lgkmcnt(0)
	v_mfma_f32_16x16x32_bf16 v[26:29], v[54:57], v[62:65], v[26:29]
	v_mfma_f32_16x16x32_bf16 v[30:33], v[54:57], v[70:73], v[30:33]
	v_mfma_f32_16x16x32_bf16 v[22:25], v[54:57], v[78:81], v[22:25]
	v_mfma_f32_16x16x32_bf16 v[18:21], v[54:57], v[86:89], v[18:21]
	v_mfma_f32_16x16x32_bf16 v[26:29], v[58:61], v[66:69], v[26:29]
	v_mfma_f32_16x16x32_bf16 v[30:33], v[58:61], v[74:77], v[30:33]
	v_mfma_f32_16x16x32_bf16 v[22:25], v[58:61], v[82:85], v[22:25]
	v_mfma_f32_16x16x32_bf16 v[18:21], v[58:61], v[90:93], v[18:21]
	s_setprio 0
	s_setprio 1
	s_setprio 0
	s_barrier
	s_addk_i32 s68, 0x80
	s_mov_b32 m0, s50
	s_add_u32 s98, s6, s68
	s_addc_u32 s99, s7, 0
	ds_read_b128 v[62:65], v52 offset:49152
	ds_read_b128 v[66:69], v52 offset:50176
	ds_read_b128 v[70:73], v52 offset:51200
	ds_read_b128 v[74:77], v52 offset:52224
	ds_read_b128 v[78:81], v52 offset:53248
	ds_read_b128 v[82:85], v52 offset:54272
	ds_read_b128 v[86:89], v52 offset:55296
	ds_read_b128 v[90:93], v52 offset:56320
	global_load_lds_dwordx4 v40, s[98:99]
	s_add_u32 s100, s98, s28
	s_addc_u32 s101, s99, 0
	s_mov_b32 m0, s51
	s_nop 0
	global_load_lds_dwordx4 v40, s[100:101]
	s_add_u32 s98, s6, s68
	s_addc_u32 s99, s7, 0
	s_mov_b32 m0, s54
	s_nop 0
	global_load_lds_dwordx4 v41, s[98:99]
	s_add_u32 s100, s98, s28
	s_addc_u32 s101, s99, 0
	s_mov_b32 m0, s55
	s_nop 0
	global_load_lds_dwordx4 v41, s[100:101]
	s_add_u32 s98, s4, s67
	s_addc_u32 s99, s5, 0
	s_mov_b32 m0, s52
	s_nop 0
	global_load_lds_dwordx4 v43, s[98:99]
	s_add_u32 s100, s98, s25
	s_addc_u32 s101, s99, 0
	s_mov_b32 m0, s53
	s_nop 0
	global_load_lds_dwordx4 v43, s[100:101]
	s_waitcnt vmcnt(8)
	s_waitcnt lgkmcnt(0)
	s_barrier
	s_setprio 1
	s_waitcnt lgkmcnt(0)
	v_mfma_f32_16x16x32_bf16 v[14:17], v[54:57], v[62:65], v[14:17]
	v_mfma_f32_16x16x32_bf16 v[10:13], v[54:57], v[70:73], v[10:13]
	v_mfma_f32_16x16x32_bf16 v[6:9], v[54:57], v[78:81], v[6:9]
	v_mfma_f32_16x16x32_bf16 v[2:5], v[54:57], v[86:89], v[2:5]
	v_mfma_f32_16x16x32_bf16 v[14:17], v[58:61], v[66:69], v[14:17]
	v_mfma_f32_16x16x32_bf16 v[10:13], v[58:61], v[74:77], v[10:13]
	v_mfma_f32_16x16x32_bf16 v[6:9], v[58:61], v[82:85], v[6:9]
	v_mfma_f32_16x16x32_bf16 v[2:5], v[58:61], v[90:93], v[2:5]
	s_setprio 0
	s_setprio 1
	s_setprio 0
	s_barrier
	s_add_i32 s66, s66, 2
	s_addk_i32 s22, 0x100
	s_addk_i32 s65, 0x100
	s_cmp_ge_i32 s66, s56
	s_cbranch_scc0 .LBB0_584

.LBB0_603:
	ds_read_b128 v[164:167], v147
	ds_read_b128 v[168:171], v148
	ds_read_b128 v[172:175], v143
	ds_read_b128 v[176:179], v144
	ds_read_b128 v[180:183], v149
	ds_read_b128 v[184:187], v150
	ds_read_b128 v[188:191], v151
	ds_read_b128 v[192:195], v152
	s_add_i32 s75, s16, 0x80
	s_cmp_eq_u32 s59, s74
	s_cselect_b32 s76, s17, s73
	s_cselect_b32 s75, s72, s75
	s_add_u32 s98, s4, s16
	s_addc_u32 s99, s5, 0
	s_add_i32 m0, s28, 0xc000
	ds_read_b128 v[196:199], v161
	ds_read_b128 v[200:203], v161 offset:1024
	ds_read_b128 v[204:207], v161 offset:2048
	ds_read_b128 v[214:217], v161 offset:3072
	ds_read_b128 v[218:221], v161 offset:4096
	ds_read_b128 v[222:225], v161 offset:5120
	ds_read_b128 v[226:229], v161 offset:6144
	ds_read_b128 v[230:233], v161 offset:7168
	global_load_lds_dwordx4 v160, s[98:99]
	s_add_u32 s100, s4, s16
	s_addc_u32 s101, s5, 0
	s_add_i32 m0, s28, 0xe000
	s_nop 0
	global_load_lds_dwordx4 v159, s[100:101]
	s_waitcnt vmcnt(8)
	s_waitcnt lgkmcnt(0)
	s_barrier
	s_setprio 1
	s_waitcnt lgkmcnt(0)
	v_mfma_f32_16x16x32_bf16 v[126:129], v[172:175], v[196:199], v[126:129]
	v_mfma_f32_16x16x32_bf16 v[122:125], v[168:171], v[196:199], v[122:125]
	v_mfma_f32_16x16x32_bf16 v[110:113], v[172:175], v[204:207], v[110:113]
	v_mfma_f32_16x16x32_bf16 v[106:109], v[168:171], v[204:207], v[106:109]
	v_mfma_f32_16x16x32_bf16 v[94:97], v[172:175], v[218:221], v[94:97]
	v_mfma_f32_16x16x32_bf16 v[90:93], v[168:171], v[218:221], v[90:93]
	v_mfma_f32_16x16x32_bf16 v[78:81], v[172:175], v[226:229], v[78:81]
	v_mfma_f32_16x16x32_bf16 v[74:77], v[168:171], v[226:229], v[74:77]
	v_mfma_f32_16x16x32_bf16 v[126:129], v[164:167], v[200:203], v[126:129]
	v_mfma_f32_16x16x32_bf16 v[122:125], v[180:183], v[200:203], v[122:125]
	v_mfma_f32_16x16x32_bf16 v[110:113], v[164:167], v[214:217], v[110:113]
	v_mfma_f32_16x16x32_bf16 v[106:109], v[180:183], v[214:217], v[106:109]
	v_mfma_f32_16x16x32_bf16 v[94:97], v[164:167], v[222:225], v[94:97]
	v_mfma_f32_16x16x32_bf16 v[90:93], v[180:183], v[222:225], v[90:93]
	v_mfma_f32_16x16x32_bf16 v[78:81], v[164:167], v[230:233], v[78:81]
	v_mfma_f32_16x16x32_bf16 v[74:77], v[180:183], v[230:233], v[74:77]
	s_setprio 0
	s_setprio 1
	v_mfma_f32_16x16x32_bf16 v[118:121], v[176:179], v[196:199], v[118:121]
	v_mfma_f32_16x16x32_bf16 v[114:117], v[188:191], v[196:199], v[114:117]
	v_mfma_f32_16x16x32_bf16 v[102:105], v[176:179], v[204:207], v[102:105]
	v_mfma_f32_16x16x32_bf16 v[98:101], v[188:191], v[204:207], v[98:101]
	v_mfma_f32_16x16x32_bf16 v[86:89], v[176:179], v[218:221], v[86:89]
	v_mfma_f32_16x16x32_bf16 v[82:85], v[188:191], v[218:221], v[82:85]
	v_mfma_f32_16x16x32_bf16 v[70:73], v[176:179], v[226:229], v[70:73]
	v_mfma_f32_16x16x32_bf16 v[66:69], v[188:191], v[226:229], v[66:69]
	v_mfma_f32_16x16x32_bf16 v[118:121], v[184:187], v[200:203], v[118:121]
	v_mfma_f32_16x16x32_bf16 v[114:117], v[192:195], v[200:203], v[114:117]
	v_mfma_f32_16x16x32_bf16 v[102:105], v[184:187], v[214:217], v[102:105]
	v_mfma_f32_16x16x32_bf16 v[98:101], v[192:195], v[214:217], v[98:101]
	v_mfma_f32_16x16x32_bf16 v[86:89], v[184:187], v[222:225], v[86:89]
	v_mfma_f32_16x16x32_bf16 v[82:85], v[192:195], v[222:225], v[82:85]
	v_mfma_f32_16x16x32_bf16 v[70:73], v[184:187], v[230:233], v[70:73]
	v_mfma_f32_16x16x32_bf16 v[66:69], v[192:195], v[230:233], v[66:69]
	s_setprio 0
	s_barrier
	s_mov_b32 m0, s29
	s_add_u32 s98, s6, s76
	s_addc_u32 s99, s7, 0
	ds_read_b128 v[196:199], v161 offset:16384
	ds_read_b128 v[200:203], v161 offset:17408
	ds_read_b128 v[204:207], v161 offset:18432
	ds_read_b128 v[214:217], v161 offset:19456
	ds_read_b128 v[218:221], v161 offset:20480
	ds_read_b128 v[222:225], v161 offset:21504
	ds_read_b128 v[226:229], v161 offset:22528
	ds_read_b128 v[230:233], v161 offset:23552
	global_load_lds_dwordx4 v135, s[98:99]
	s_add_u32 s100, s98, s23
	s_addc_u32 s101, s99, 0
	s_mov_b32 m0, s30
	s_nop 0
	global_load_lds_dwordx4 v135, s[100:101]
	s_add_u32 s98, s6, s76
	s_addc_u32 s99, s7, 0
	s_mov_b32 m0, s31
	s_nop 0
	global_load_lds_dwordx4 v138, s[98:99]
	s_add_u32 s100, s98, s23
	s_addc_u32 s101, s99, 0
	s_mov_b32 m0, s35
	s_nop 0
	global_load_lds_dwordx4 v138, s[100:101]
	s_add_u32 s98, s4, s75
	s_addc_u32 s99, s5, 0
	s_mov_b32 m0, s28
	s_nop 0
	global_load_lds_dwordx4 v1, s[98:99]
	s_add_u32 s100, s98, s22
	s_addc_u32 s101, s99, 0
	s_mov_b32 m0, s44
	s_nop 0
	global_load_lds_dwordx4 v1, s[100:101]
	s_waitcnt vmcnt(8)
	s_waitcnt lgkmcnt(0)
	s_barrier
	s_setprio 1
	s_waitcnt lgkmcnt(0)
	v_mfma_f32_16x16x32_bf16 v[62:65], v[172:175], v[196:199], v[62:65]
	v_mfma_f32_16x16x32_bf16 v[58:61], v[168:171], v[196:199], v[58:61]
	v_mfma_f32_16x16x32_bf16 v[46:49], v[172:175], v[204:207], v[46:49]
	v_mfma_f32_16x16x32_bf16 v[42:45], v[168:171], v[204:207], v[42:45]
	v_mfma_f32_16x16x32_bf16 v[30:33], v[172:175], v[218:221], v[30:33]
	v_mfma_f32_16x16x32_bf16 v[26:29], v[168:171], v[218:221], v[26:29]
	v_mfma_f32_16x16x32_bf16 v[14:17], v[172:175], v[226:229], v[14:17]
	v_mfma_f32_16x16x32_bf16 v[10:13], v[168:171], v[226:229], v[10:13]
	v_mfma_f32_16x16x32_bf16 v[62:65], v[164:167], v[200:203], v[62:65]
	v_mfma_f32_16x16x32_bf16 v[58:61], v[180:183], v[200:203], v[58:61]
	v_mfma_f32_16x16x32_bf16 v[46:49], v[164:167], v[214:217], v[46:49]
	v_mfma_f32_16x16x32_bf16 v[42:45], v[180:183], v[214:217], v[42:45]
	v_mfma_f32_16x16x32_bf16 v[30:33], v[164:167], v[222:225], v[30:33]
	v_mfma_f32_16x16x32_bf16 v[26:29], v[180:183], v[222:225], v[26:29]
	v_mfma_f32_16x16x32_bf16 v[14:17], v[164:167], v[230:233], v[14:17]
	v_mfma_f32_16x16x32_bf16 v[10:13], v[180:183], v[230:233], v[10:13]
	s_setprio 0
	s_setprio 1
	v_mfma_f32_16x16x32_bf16 v[54:57], v[176:179], v[196:199], v[54:57]
	v_mfma_f32_16x16x32_bf16 v[50:53], v[188:191], v[196:199], v[50:53]
	v_mfma_f32_16x16x32_bf16 v[38:41], v[176:179], v[204:207], v[38:41]
	v_mfma_f32_16x16x32_bf16 v[34:37], v[188:191], v[204:207], v[34:37]
	v_mfma_f32_16x16x32_bf16 v[22:25], v[176:179], v[218:221], v[22:25]
	v_mfma_f32_16x16x32_bf16 v[18:21], v[188:191], v[218:221], v[18:21]
	v_mfma_f32_16x16x32_bf16 v[6:9], v[176:179], v[226:229], v[6:9]
	v_mfma_f32_16x16x32_bf16 v[2:5], v[188:191], v[226:229], v[2:5]
	v_mfma_f32_16x16x32_bf16 v[54:57], v[184:187], v[200:203], v[54:57]
	v_mfma_f32_16x16x32_bf16 v[50:53], v[192:195], v[200:203], v[50:53]
	v_mfma_f32_16x16x32_bf16 v[38:41], v[184:187], v[214:217], v[38:41]
	v_mfma_f32_16x16x32_bf16 v[34:37], v[192:195], v[214:217], v[34:37]
	v_mfma_f32_16x16x32_bf16 v[22:25], v[184:187], v[222:225], v[22:25]
	v_mfma_f32_16x16x32_bf16 v[18:21], v[192:195], v[222:225], v[18:21]
	v_mfma_f32_16x16x32_bf16 v[6:9], v[184:187], v[230:233], v[6:9]
	v_mfma_f32_16x16x32_bf16 v[2:5], v[192:195], v[230:233], v[2:5]
	s_setprio 0
	s_barrier
	ds_read_b128 v[164:167], v153
	ds_read_b128 v[168:171], v154
	ds_read_b128 v[172:175], v145
	ds_read_b128 v[176:179], v146
	ds_read_b128 v[180:183], v155
	ds_read_b128 v[184:187], v156
	ds_read_b128 v[188:191], v157
	ds_read_b128 v[192:195], v158
	s_mov_b32 m0, s45
	s_add_u32 s98, s4, s75
	s_addc_u32 s99, s5, 0
	ds_read_b128 v[196:199], v161 offset:32768
	ds_read_b128 v[200:203], v161 offset:33792
	ds_read_b128 v[204:207], v161 offset:34816
	ds_read_b128 v[214:217], v161 offset:35840
	ds_read_b128 v[218:221], v161 offset:36864
	ds_read_b128 v[222:225], v161 offset:37888
	ds_read_b128 v[226:229], v161 offset:38912
	ds_read_b128 v[230:233], v161 offset:39936
	global_load_lds_dwordx4 v139, s[98:99]
	s_add_u32 s100, s98, s22
	s_addc_u32 s101, s99, 0
	s_mov_b32 m0, s46
	s_nop 0
	global_load_lds_dwordx4 v139, s[100:101]
	s_waitcnt vmcnt(8)
	s_waitcnt lgkmcnt(0)
	s_barrier
	s_setprio 1
	s_waitcnt lgkmcnt(0)
	v_mfma_f32_16x16x32_bf16 v[126:129], v[172:175], v[196:199], v[126:129]
	v_mfma_f32_16x16x32_bf16 v[122:125], v[168:171], v[196:199], v[122:125]
	v_mfma_f32_16x16x32_bf16 v[110:113], v[172:175], v[204:207], v[110:113]
	v_mfma_f32_16x16x32_bf16 v[106:109], v[168:171], v[204:207], v[106:109]
	v_mfma_f32_16x16x32_bf16 v[94:97], v[172:175], v[218:221], v[94:97]
	v_mfma_f32_16x16x32_bf16 v[90:93], v[168:171], v[218:221], v[90:93]
	v_mfma_f32_16x16x32_bf16 v[78:81], v[172:175], v[226:229], v[78:81]
	v_mfma_f32_16x16x32_bf16 v[74:77], v[168:171], v[226:229], v[74:77]
	v_mfma_f32_16x16x32_bf16 v[126:129], v[164:167], v[200:203], v[126:129]
	v_mfma_f32_16x16x32_bf16 v[122:125], v[180:183], v[200:203], v[122:125]
	v_mfma_f32_16x16x32_bf16 v[110:113], v[164:167], v[214:217], v[110:113]
	v_mfma_f32_16x16x32_bf16 v[106:109], v[180:183], v[214:217], v[106:109]
	v_mfma_f32_16x16x32_bf16 v[94:97], v[164:167], v[222:225], v[94:97]
	v_mfma_f32_16x16x32_bf16 v[90:93], v[180:183], v[222:225], v[90:93]
	v_mfma_f32_16x16x32_bf16 v[78:81], v[164:167], v[230:233], v[78:81]
	v_mfma_f32_16x16x32_bf16 v[74:77], v[180:183], v[230:233], v[74:77]
	s_setprio 0
	s_setprio 1
	v_mfma_f32_16x16x32_bf16 v[118:121], v[176:179], v[196:199], v[118:121]
	v_mfma_f32_16x16x32_bf16 v[114:117], v[188:191], v[196:199], v[114:117]
	v_mfma_f32_16x16x32_bf16 v[102:105], v[176:179], v[204:207], v[102:105]
	v_mfma_f32_16x16x32_bf16 v[98:101], v[188:191], v[204:207], v[98:101]
	v_mfma_f32_16x16x32_bf16 v[86:89], v[176:179], v[218:221], v[86:89]
	v_mfma_f32_16x16x32_bf16 v[82:85], v[188:191], v[218:221], v[82:85]
	v_mfma_f32_16x16x32_bf16 v[70:73], v[176:179], v[226:229], v[70:73]
	v_mfma_f32_16x16x32_bf16 v[66:69], v[188:191], v[226:229], v[66:69]
	v_mfma_f32_16x16x32_bf16 v[118:121], v[184:187], v[200:203], v[118:121]
	v_mfma_f32_16x16x32_bf16 v[114:117], v[192:195], v[200:203], v[114:117]
	v_mfma_f32_16x16x32_bf16 v[102:105], v[184:187], v[214:217], v[102:105]
	v_mfma_f32_16x16x32_bf16 v[98:101], v[192:195], v[214:217], v[98:101]
	v_mfma_f32_16x16x32_bf16 v[86:89], v[184:187], v[222:225], v[86:89]
	v_mfma_f32_16x16x32_bf16 v[82:85], v[192:195], v[222:225], v[82:85]
	v_mfma_f32_16x16x32_bf16 v[70:73], v[184:187], v[230:233], v[70:73]
	v_mfma_f32_16x16x32_bf16 v[66:69], v[192:195], v[230:233], v[66:69]
	s_setprio 0
	s_barrier
	s_addk_i32 s76, 0x80
	s_mov_b32 m0, s48
	s_add_u32 s98, s6, s76
	s_addc_u32 s99, s7, 0
	ds_read_b128 v[196:199], v161 offset:49152
	ds_read_b128 v[200:203], v161 offset:50176
	ds_read_b128 v[204:207], v161 offset:51200
	ds_read_b128 v[214:217], v161 offset:52224
	ds_read_b128 v[218:221], v161 offset:53248
	ds_read_b128 v[222:225], v161 offset:54272
	ds_read_b128 v[226:229], v161 offset:55296
	ds_read_b128 v[230:233], v161 offset:56320
	global_load_lds_dwordx4 v135, s[98:99]
	s_add_u32 s100, s98, s23
	s_addc_u32 s101, s99, 0
	s_mov_b32 m0, s49
	s_nop 0
	global_load_lds_dwordx4 v135, s[100:101]
	s_add_u32 s98, s6, s76
	s_addc_u32 s99, s7, 0
	s_mov_b32 m0, s52
	s_nop 0
	global_load_lds_dwordx4 v138, s[98:99]
	s_add_u32 s100, s98, s23
	s_addc_u32 s101, s99, 0
	s_mov_b32 m0, s53
	s_nop 0
	global_load_lds_dwordx4 v138, s[100:101]
	s_add_u32 s98, s4, s75
	s_addc_u32 s99, s5, 0
	s_mov_b32 m0, s50
	s_nop 0
	global_load_lds_dwordx4 v140, s[98:99]
	s_add_u32 s100, s98, s22
	s_addc_u32 s101, s99, 0
	s_mov_b32 m0, s51
	s_nop 0
	global_load_lds_dwordx4 v140, s[100:101]
	s_waitcnt vmcnt(8)
	s_waitcnt lgkmcnt(0)
	s_barrier
	s_setprio 1
	s_waitcnt lgkmcnt(0)
	v_mfma_f32_16x16x32_bf16 v[62:65], v[172:175], v[196:199], v[62:65]
	v_mfma_f32_16x16x32_bf16 v[58:61], v[168:171], v[196:199], v[58:61]
	v_mfma_f32_16x16x32_bf16 v[46:49], v[172:175], v[204:207], v[46:49]
	v_mfma_f32_16x16x32_bf16 v[42:45], v[168:171], v[204:207], v[42:45]
	v_mfma_f32_16x16x32_bf16 v[30:33], v[172:175], v[218:221], v[30:33]
	v_mfma_f32_16x16x32_bf16 v[26:29], v[168:171], v[218:221], v[26:29]
	v_mfma_f32_16x16x32_bf16 v[14:17], v[172:175], v[226:229], v[14:17]
	v_mfma_f32_16x16x32_bf16 v[10:13], v[168:171], v[226:229], v[10:13]
	v_mfma_f32_16x16x32_bf16 v[62:65], v[164:167], v[200:203], v[62:65]
	v_mfma_f32_16x16x32_bf16 v[58:61], v[180:183], v[200:203], v[58:61]
	v_mfma_f32_16x16x32_bf16 v[46:49], v[164:167], v[214:217], v[46:49]
	v_mfma_f32_16x16x32_bf16 v[42:45], v[180:183], v[214:217], v[42:45]
	v_mfma_f32_16x16x32_bf16 v[30:33], v[164:167], v[222:225], v[30:33]
	v_mfma_f32_16x16x32_bf16 v[26:29], v[180:183], v[222:225], v[26:29]
	v_mfma_f32_16x16x32_bf16 v[14:17], v[164:167], v[230:233], v[14:17]
	v_mfma_f32_16x16x32_bf16 v[10:13], v[180:183], v[230:233], v[10:13]
	s_setprio 0
	s_setprio 1
	v_mfma_f32_16x16x32_bf16 v[54:57], v[176:179], v[196:199], v[54:57]
	v_mfma_f32_16x16x32_bf16 v[50:53], v[188:191], v[196:199], v[50:53]
	v_mfma_f32_16x16x32_bf16 v[38:41], v[176:179], v[204:207], v[38:41]
	v_mfma_f32_16x16x32_bf16 v[34:37], v[188:191], v[204:207], v[34:37]
	v_mfma_f32_16x16x32_bf16 v[22:25], v[176:179], v[218:221], v[22:25]
	v_mfma_f32_16x16x32_bf16 v[18:21], v[188:191], v[218:221], v[18:21]
	v_mfma_f32_16x16x32_bf16 v[6:9], v[176:179], v[226:229], v[6:9]
	v_mfma_f32_16x16x32_bf16 v[2:5], v[188:191], v[226:229], v[2:5]
	v_mfma_f32_16x16x32_bf16 v[54:57], v[184:187], v[200:203], v[54:57]
	v_mfma_f32_16x16x32_bf16 v[50:53], v[192:195], v[200:203], v[50:53]
	v_mfma_f32_16x16x32_bf16 v[38:41], v[184:187], v[214:217], v[38:41]
	v_mfma_f32_16x16x32_bf16 v[34:37], v[192:195], v[214:217], v[34:37]
	v_mfma_f32_16x16x32_bf16 v[22:25], v[184:187], v[222:225], v[22:25]
	v_mfma_f32_16x16x32_bf16 v[18:21], v[192:195], v[222:225], v[18:21]
	v_mfma_f32_16x16x32_bf16 v[6:9], v[184:187], v[230:233], v[6:9]
	v_mfma_f32_16x16x32_bf16 v[2:5], v[192:195], v[230:233], v[2:5]
	s_setprio 0
	s_barrier
	s_add_i32 s74, s74, 2
	s_addk_i32 s16, 0x100
	s_addk_i32 s73, 0x100
	s_cmp_ge_i32 s74, s54
	s_cbranch_scc0 .LBB0_603

.LBB0_620:
	ds_read_b128 v[160:163], v144
	ds_read_b128 v[164:167], v145
	ds_read_b128 v[168:171], v140
	ds_read_b128 v[172:175], v141
	ds_read_b128 v[176:179], v146
	ds_read_b128 v[180:183], v147
	ds_read_b128 v[184:187], v148
	ds_read_b128 v[188:191], v149
	s_add_i32 s73, s16, 0x80
	s_cmp_eq_u32 s20, s72
	s_cselect_b32 s74, s15, s71
	s_cselect_b32 s73, s17, s73
	s_add_u32 s98, s4, s16
	s_addc_u32 s99, s5, 0
	s_add_i32 m0, s28, 0xc000
	ds_read_b128 v[192:195], v158
	ds_read_b128 v[196:199], v158 offset:1024
	ds_read_b128 v[200:203], v158 offset:2048
	ds_read_b128 v[204:207], v158 offset:3072
	ds_read_b128 v[214:217], v158 offset:4096
	ds_read_b128 v[218:221], v158 offset:5120
	ds_read_b128 v[222:225], v158 offset:6144
	ds_read_b128 v[226:229], v158 offset:7168
	global_load_lds_dwordx4 v157, s[98:99]
	s_add_u32 s100, s4, s16
	s_addc_u32 s101, s5, 0
	s_add_i32 m0, s28, 0xe000
	s_nop 0
	global_load_lds_dwordx4 v156, s[100:101]
	s_waitcnt vmcnt(8)
	s_waitcnt lgkmcnt(0)
	s_barrier
	s_setprio 1
	s_waitcnt lgkmcnt(0)
	v_mfma_f32_16x16x32_bf16 v[122:125], v[168:171], v[192:195], v[122:125]
	v_mfma_f32_16x16x32_bf16 v[126:129], v[164:167], v[192:195], v[126:129]
	v_mfma_f32_16x16x32_bf16 v[110:113], v[168:171], v[200:203], v[110:113]
	v_mfma_f32_16x16x32_bf16 v[106:109], v[164:167], v[200:203], v[106:109]
	v_mfma_f32_16x16x32_bf16 v[94:97], v[168:171], v[214:217], v[94:97]
	v_mfma_f32_16x16x32_bf16 v[90:93], v[164:167], v[214:217], v[90:93]
	v_mfma_f32_16x16x32_bf16 v[78:81], v[168:171], v[222:225], v[78:81]
	v_mfma_f32_16x16x32_bf16 v[74:77], v[164:167], v[222:225], v[74:77]
	v_mfma_f32_16x16x32_bf16 v[122:125], v[160:163], v[196:199], v[122:125]
	v_mfma_f32_16x16x32_bf16 v[126:129], v[176:179], v[196:199], v[126:129]
	v_mfma_f32_16x16x32_bf16 v[110:113], v[160:163], v[204:207], v[110:113]
	v_mfma_f32_16x16x32_bf16 v[106:109], v[176:179], v[204:207], v[106:109]
	v_mfma_f32_16x16x32_bf16 v[94:97], v[160:163], v[218:221], v[94:97]
	v_mfma_f32_16x16x32_bf16 v[90:93], v[176:179], v[218:221], v[90:93]
	v_mfma_f32_16x16x32_bf16 v[78:81], v[160:163], v[226:229], v[78:81]
	v_mfma_f32_16x16x32_bf16 v[74:77], v[176:179], v[226:229], v[74:77]
	s_setprio 0
	s_setprio 1
	v_mfma_f32_16x16x32_bf16 v[118:121], v[172:175], v[192:195], v[118:121]
	v_mfma_f32_16x16x32_bf16 v[114:117], v[184:187], v[192:195], v[114:117]
	v_mfma_f32_16x16x32_bf16 v[102:105], v[172:175], v[200:203], v[102:105]
	v_mfma_f32_16x16x32_bf16 v[98:101], v[184:187], v[200:203], v[98:101]
	v_mfma_f32_16x16x32_bf16 v[86:89], v[172:175], v[214:217], v[86:89]
	v_mfma_f32_16x16x32_bf16 v[82:85], v[184:187], v[214:217], v[82:85]
	v_mfma_f32_16x16x32_bf16 v[70:73], v[172:175], v[222:225], v[70:73]
	v_mfma_f32_16x16x32_bf16 v[66:69], v[184:187], v[222:225], v[66:69]
	v_mfma_f32_16x16x32_bf16 v[118:121], v[180:183], v[196:199], v[118:121]
	v_mfma_f32_16x16x32_bf16 v[114:117], v[188:191], v[196:199], v[114:117]
	v_mfma_f32_16x16x32_bf16 v[102:105], v[180:183], v[204:207], v[102:105]
	v_mfma_f32_16x16x32_bf16 v[98:101], v[188:191], v[204:207], v[98:101]
	v_mfma_f32_16x16x32_bf16 v[86:89], v[180:183], v[218:221], v[86:89]
	v_mfma_f32_16x16x32_bf16 v[82:85], v[188:191], v[218:221], v[82:85]
	v_mfma_f32_16x16x32_bf16 v[70:73], v[180:183], v[226:229], v[70:73]
	v_mfma_f32_16x16x32_bf16 v[66:69], v[188:191], v[226:229], v[66:69]
	s_setprio 0
	s_barrier
	s_mov_b32 m0, s29
	s_add_u32 s98, s6, s74
	s_addc_u32 s99, s7, 0
	ds_read_b128 v[192:195], v158 offset:16384
	ds_read_b128 v[196:199], v158 offset:17408
	ds_read_b128 v[200:203], v158 offset:18432
	ds_read_b128 v[204:207], v158 offset:19456
	ds_read_b128 v[214:217], v158 offset:20480
	ds_read_b128 v[218:221], v158 offset:21504
	ds_read_b128 v[222:225], v158 offset:22528
	ds_read_b128 v[226:229], v158 offset:23552
	global_load_lds_dwordx4 v134, s[98:99]
	s_add_u32 s100, s98, s23
	s_addc_u32 s101, s99, 0
	s_mov_b32 m0, s30
	s_nop 0
	global_load_lds_dwordx4 v134, s[100:101]
	s_add_u32 s98, s6, s74
	s_addc_u32 s99, s7, 0
	s_mov_b32 m0, s31
	s_nop 0
	global_load_lds_dwordx4 v135, s[98:99]
	s_add_u32 s100, s98, s23
	s_addc_u32 s101, s99, 0
	s_mov_b32 m0, s35
	s_nop 0
	global_load_lds_dwordx4 v135, s[100:101]
	s_add_u32 s98, s4, s73
	s_addc_u32 s99, s5, 0
	s_mov_b32 m0, s28
	s_nop 0
	global_load_lds_dwordx4 v1, s[98:99]
	s_add_u32 s100, s98, s22
	s_addc_u32 s101, s99, 0
	s_mov_b32 m0, s44
	s_nop 0
	global_load_lds_dwordx4 v1, s[100:101]
	s_waitcnt vmcnt(8)
	s_waitcnt lgkmcnt(0)
	s_barrier
	s_setprio 1
	s_waitcnt lgkmcnt(0)
	v_mfma_f32_16x16x32_bf16 v[62:65], v[168:171], v[192:195], v[62:65]
	v_mfma_f32_16x16x32_bf16 v[58:61], v[164:167], v[192:195], v[58:61]
	v_mfma_f32_16x16x32_bf16 v[46:49], v[168:171], v[200:203], v[46:49]
	v_mfma_f32_16x16x32_bf16 v[42:45], v[164:167], v[200:203], v[42:45]
	v_mfma_f32_16x16x32_bf16 v[30:33], v[168:171], v[214:217], v[30:33]
	v_mfma_f32_16x16x32_bf16 v[26:29], v[164:167], v[214:217], v[26:29]
	v_mfma_f32_16x16x32_bf16 v[14:17], v[168:171], v[222:225], v[14:17]
	v_mfma_f32_16x16x32_bf16 v[10:13], v[164:167], v[222:225], v[10:13]
	v_mfma_f32_16x16x32_bf16 v[62:65], v[160:163], v[196:199], v[62:65]
	v_mfma_f32_16x16x32_bf16 v[58:61], v[176:179], v[196:199], v[58:61]
	v_mfma_f32_16x16x32_bf16 v[46:49], v[160:163], v[204:207], v[46:49]
	v_mfma_f32_16x16x32_bf16 v[42:45], v[176:179], v[204:207], v[42:45]
	v_mfma_f32_16x16x32_bf16 v[30:33], v[160:163], v[218:221], v[30:33]
	v_mfma_f32_16x16x32_bf16 v[26:29], v[176:179], v[218:221], v[26:29]
	v_mfma_f32_16x16x32_bf16 v[14:17], v[160:163], v[226:229], v[14:17]
	v_mfma_f32_16x16x32_bf16 v[10:13], v[176:179], v[226:229], v[10:13]
	s_setprio 0
	s_setprio 1
	v_mfma_f32_16x16x32_bf16 v[54:57], v[172:175], v[192:195], v[54:57]
	v_mfma_f32_16x16x32_bf16 v[50:53], v[184:187], v[192:195], v[50:53]
	v_mfma_f32_16x16x32_bf16 v[38:41], v[172:175], v[200:203], v[38:41]
	v_mfma_f32_16x16x32_bf16 v[34:37], v[184:187], v[200:203], v[34:37]
	v_mfma_f32_16x16x32_bf16 v[22:25], v[172:175], v[214:217], v[22:25]
	v_mfma_f32_16x16x32_bf16 v[18:21], v[184:187], v[214:217], v[18:21]
	v_mfma_f32_16x16x32_bf16 v[6:9], v[172:175], v[222:225], v[6:9]
	v_mfma_f32_16x16x32_bf16 v[2:5], v[184:187], v[222:225], v[2:5]
	v_mfma_f32_16x16x32_bf16 v[54:57], v[180:183], v[196:199], v[54:57]
	v_mfma_f32_16x16x32_bf16 v[50:53], v[188:191], v[196:199], v[50:53]
	v_mfma_f32_16x16x32_bf16 v[38:41], v[180:183], v[204:207], v[38:41]
	v_mfma_f32_16x16x32_bf16 v[34:37], v[188:191], v[204:207], v[34:37]
	v_mfma_f32_16x16x32_bf16 v[22:25], v[180:183], v[218:221], v[22:25]
	v_mfma_f32_16x16x32_bf16 v[18:21], v[188:191], v[218:221], v[18:21]
	v_mfma_f32_16x16x32_bf16 v[6:9], v[180:183], v[226:229], v[6:9]
	v_mfma_f32_16x16x32_bf16 v[2:5], v[188:191], v[226:229], v[2:5]
	s_setprio 0
	s_barrier
	ds_read_b128 v[160:163], v150
	ds_read_b128 v[164:167], v151
	ds_read_b128 v[168:171], v142
	ds_read_b128 v[172:175], v143
	ds_read_b128 v[176:179], v152
	ds_read_b128 v[180:183], v153
	ds_read_b128 v[184:187], v154
	ds_read_b128 v[188:191], v155
	s_mov_b32 m0, s45
	s_add_u32 s98, s4, s73
	s_addc_u32 s99, s5, 0
	ds_read_b128 v[192:195], v158 offset:32768
	ds_read_b128 v[196:199], v158 offset:33792
	ds_read_b128 v[200:203], v158 offset:34816
	ds_read_b128 v[204:207], v158 offset:35840
	ds_read_b128 v[214:217], v158 offset:36864
	ds_read_b128 v[218:221], v158 offset:37888
	ds_read_b128 v[222:225], v158 offset:38912
	ds_read_b128 v[226:229], v158 offset:39936
	global_load_lds_dwordx4 v136, s[98:99]
	s_add_u32 s100, s98, s22
	s_addc_u32 s101, s99, 0
	s_mov_b32 m0, s46
	s_nop 0
	global_load_lds_dwordx4 v136, s[100:101]
	s_waitcnt vmcnt(8)
	s_waitcnt lgkmcnt(0)
	s_barrier
	s_setprio 1
	s_waitcnt lgkmcnt(0)
	v_mfma_f32_16x16x32_bf16 v[122:125], v[168:171], v[192:195], v[122:125]
	v_mfma_f32_16x16x32_bf16 v[126:129], v[164:167], v[192:195], v[126:129]
	v_mfma_f32_16x16x32_bf16 v[110:113], v[168:171], v[200:203], v[110:113]
	v_mfma_f32_16x16x32_bf16 v[106:109], v[164:167], v[200:203], v[106:109]
	v_mfma_f32_16x16x32_bf16 v[94:97], v[168:171], v[214:217], v[94:97]
	v_mfma_f32_16x16x32_bf16 v[90:93], v[164:167], v[214:217], v[90:93]
	v_mfma_f32_16x16x32_bf16 v[78:81], v[168:171], v[222:225], v[78:81]
	v_mfma_f32_16x16x32_bf16 v[74:77], v[164:167], v[222:225], v[74:77]
	v_mfma_f32_16x16x32_bf16 v[122:125], v[160:163], v[196:199], v[122:125]
	v_mfma_f32_16x16x32_bf16 v[126:129], v[176:179], v[196:199], v[126:129]
	v_mfma_f32_16x16x32_bf16 v[110:113], v[160:163], v[204:207], v[110:113]
	v_mfma_f32_16x16x32_bf16 v[106:109], v[176:179], v[204:207], v[106:109]
	v_mfma_f32_16x16x32_bf16 v[94:97], v[160:163], v[218:221], v[94:97]
	v_mfma_f32_16x16x32_bf16 v[90:93], v[176:179], v[218:221], v[90:93]
	v_mfma_f32_16x16x32_bf16 v[78:81], v[160:163], v[226:229], v[78:81]
	v_mfma_f32_16x16x32_bf16 v[74:77], v[176:179], v[226:229], v[74:77]
	s_setprio 0
	s_setprio 1
	v_mfma_f32_16x16x32_bf16 v[118:121], v[172:175], v[192:195], v[118:121]
	v_mfma_f32_16x16x32_bf16 v[114:117], v[184:187], v[192:195], v[114:117]
	v_mfma_f32_16x16x32_bf16 v[102:105], v[172:175], v[200:203], v[102:105]
	v_mfma_f32_16x16x32_bf16 v[98:101], v[184:187], v[200:203], v[98:101]
	v_mfma_f32_16x16x32_bf16 v[86:89], v[172:175], v[214:217], v[86:89]
	v_mfma_f32_16x16x32_bf16 v[82:85], v[184:187], v[214:217], v[82:85]
	v_mfma_f32_16x16x32_bf16 v[70:73], v[172:175], v[222:225], v[70:73]
	v_mfma_f32_16x16x32_bf16 v[66:69], v[184:187], v[222:225], v[66:69]
	v_mfma_f32_16x16x32_bf16 v[118:121], v[180:183], v[196:199], v[118:121]
	v_mfma_f32_16x16x32_bf16 v[114:117], v[188:191], v[196:199], v[114:117]
	v_mfma_f32_16x16x32_bf16 v[102:105], v[180:183], v[204:207], v[102:105]
	v_mfma_f32_16x16x32_bf16 v[98:101], v[188:191], v[204:207], v[98:101]
	v_mfma_f32_16x16x32_bf16 v[86:89], v[180:183], v[218:221], v[86:89]
	v_mfma_f32_16x16x32_bf16 v[82:85], v[188:191], v[218:221], v[82:85]
	v_mfma_f32_16x16x32_bf16 v[70:73], v[180:183], v[226:229], v[70:73]
	v_mfma_f32_16x16x32_bf16 v[66:69], v[188:191], v[226:229], v[66:69]
	s_setprio 0
	s_barrier
	s_addk_i32 s74, 0x80
	s_mov_b32 m0, s49
	s_add_u32 s98, s6, s74
	s_addc_u32 s99, s7, 0
	ds_read_b128 v[192:195], v158 offset:49152
	ds_read_b128 v[196:199], v158 offset:50176
	ds_read_b128 v[200:203], v158 offset:51200
	ds_read_b128 v[204:207], v158 offset:52224
	ds_read_b128 v[214:217], v158 offset:53248
	ds_read_b128 v[218:221], v158 offset:54272
	ds_read_b128 v[222:225], v158 offset:55296
	ds_read_b128 v[226:229], v158 offset:56320
	global_load_lds_dwordx4 v134, s[98:99]
	s_add_u32 s100, s98, s23
	s_addc_u32 s101, s99, 0
	s_mov_b32 m0, s50
	s_nop 0
	global_load_lds_dwordx4 v134, s[100:101]
	s_add_u32 s98, s6, s74
	s_addc_u32 s99, s7, 0
	s_mov_b32 m0, s53
	s_nop 0
	global_load_lds_dwordx4 v135, s[98:99]
	s_add_u32 s100, s98, s23
	s_addc_u32 s101, s99, 0
	s_mov_b32 m0, s54
	s_nop 0
	global_load_lds_dwordx4 v135, s[100:101]
	s_add_u32 s98, s4, s73
	s_addc_u32 s99, s5, 0
	s_mov_b32 m0, s51
	s_nop 0
	global_load_lds_dwordx4 v137, s[98:99]
	s_add_u32 s100, s98, s22
	s_addc_u32 s101, s99, 0
	s_mov_b32 m0, s52
	s_nop 0
	global_load_lds_dwordx4 v137, s[100:101]
	s_waitcnt vmcnt(8)
	s_waitcnt lgkmcnt(0)
	s_barrier
	s_setprio 1
	s_waitcnt lgkmcnt(0)
	v_mfma_f32_16x16x32_bf16 v[62:65], v[168:171], v[192:195], v[62:65]
	v_mfma_f32_16x16x32_bf16 v[58:61], v[164:167], v[192:195], v[58:61]
	v_mfma_f32_16x16x32_bf16 v[46:49], v[168:171], v[200:203], v[46:49]
	v_mfma_f32_16x16x32_bf16 v[42:45], v[164:167], v[200:203], v[42:45]
	v_mfma_f32_16x16x32_bf16 v[30:33], v[168:171], v[214:217], v[30:33]
	v_mfma_f32_16x16x32_bf16 v[26:29], v[164:167], v[214:217], v[26:29]
	v_mfma_f32_16x16x32_bf16 v[14:17], v[168:171], v[222:225], v[14:17]
	v_mfma_f32_16x16x32_bf16 v[10:13], v[164:167], v[222:225], v[10:13]
	v_mfma_f32_16x16x32_bf16 v[62:65], v[160:163], v[196:199], v[62:65]
	v_mfma_f32_16x16x32_bf16 v[58:61], v[176:179], v[196:199], v[58:61]
	v_mfma_f32_16x16x32_bf16 v[46:49], v[160:163], v[204:207], v[46:49]
	v_mfma_f32_16x16x32_bf16 v[42:45], v[176:179], v[204:207], v[42:45]
	v_mfma_f32_16x16x32_bf16 v[30:33], v[160:163], v[218:221], v[30:33]
	v_mfma_f32_16x16x32_bf16 v[26:29], v[176:179], v[218:221], v[26:29]
	v_mfma_f32_16x16x32_bf16 v[14:17], v[160:163], v[226:229], v[14:17]
	v_mfma_f32_16x16x32_bf16 v[10:13], v[176:179], v[226:229], v[10:13]
	s_setprio 0
	s_setprio 1
	v_mfma_f32_16x16x32_bf16 v[54:57], v[172:175], v[192:195], v[54:57]
	v_mfma_f32_16x16x32_bf16 v[50:53], v[184:187], v[192:195], v[50:53]
	v_mfma_f32_16x16x32_bf16 v[38:41], v[172:175], v[200:203], v[38:41]
	v_mfma_f32_16x16x32_bf16 v[34:37], v[184:187], v[200:203], v[34:37]
	v_mfma_f32_16x16x32_bf16 v[22:25], v[172:175], v[214:217], v[22:25]
	v_mfma_f32_16x16x32_bf16 v[18:21], v[184:187], v[214:217], v[18:21]
	v_mfma_f32_16x16x32_bf16 v[6:9], v[172:175], v[222:225], v[6:9]
	v_mfma_f32_16x16x32_bf16 v[2:5], v[184:187], v[222:225], v[2:5]
	v_mfma_f32_16x16x32_bf16 v[54:57], v[180:183], v[196:199], v[54:57]
	v_mfma_f32_16x16x32_bf16 v[50:53], v[188:191], v[196:199], v[50:53]
	v_mfma_f32_16x16x32_bf16 v[38:41], v[180:183], v[204:207], v[38:41]
	v_mfma_f32_16x16x32_bf16 v[34:37], v[188:191], v[204:207], v[34:37]
	v_mfma_f32_16x16x32_bf16 v[22:25], v[180:183], v[218:221], v[22:25]
	v_mfma_f32_16x16x32_bf16 v[18:21], v[188:191], v[218:221], v[18:21]
	v_mfma_f32_16x16x32_bf16 v[6:9], v[180:183], v[226:229], v[6:9]
	v_mfma_f32_16x16x32_bf16 v[2:5], v[188:191], v[226:229], v[2:5]
	s_setprio 0
	s_barrier
	s_add_i32 s72, s72, 2
	s_addk_i32 s16, 0x100
	s_addk_i32 s71, 0x100
	s_cmp_ge_i32 s72, s55
	s_cbranch_scc0 .LBB0_620

.LBB0_637:
	ds_read_b128 v[130:133], v188
	ds_read_b128 v[134:137], v189
	ds_read_b128 v[138:141], v184
	ds_read_b128 v[142:145], v185
	ds_read_b128 v[146:149], v190
	ds_read_b128 v[150:153], v191
	ds_read_b128 v[154:157], v192
	ds_read_b128 v[158:161], v193
	s_add_i32 s75, s28, 0x80
	s_cmp_eq_u32 s66, s80
	s_cselect_b32 s81, s25, s79
	s_cselect_b32 s75, s29, s75
	s_add_u32 s98, s4, s28
	s_addc_u32 s99, s5, 0
	s_add_i32 m0, s46, 0xc000
	ds_read_b128 v[162:165], v202
	ds_read_b128 v[166:169], v202 offset:1024
	ds_read_b128 v[170:173], v202 offset:2048
	ds_read_b128 v[204:207], v202 offset:3072
	ds_read_b128 v[214:217], v202 offset:4096
	ds_read_b128 v[218:221], v202 offset:5120
	ds_read_b128 v[222:225], v202 offset:6144
	ds_read_b128 v[226:229], v202 offset:7168
	global_load_lds_dwordx4 v201, s[98:99]
	s_add_u32 s100, s4, s28
	s_addc_u32 s101, s5, 0
	s_add_i32 m0, s46, 0xe000
	s_nop 0
	global_load_lds_dwordx4 v200, s[100:101]
	s_waitcnt vmcnt(8)
	s_waitcnt lgkmcnt(0)
	s_barrier
	s_setprio 1
	s_waitcnt lgkmcnt(0)
	v_mfma_f32_16x16x32_bf16 v[126:129], v[138:141], v[162:165], v[126:129]
	v_mfma_f32_16x16x32_bf16 v[118:121], v[134:137], v[162:165], v[118:121]
	v_mfma_f32_16x16x32_bf16 v[110:113], v[138:141], v[170:173], v[110:113]
	v_mfma_f32_16x16x32_bf16 v[102:105], v[134:137], v[170:173], v[102:105]
	v_mfma_f32_16x16x32_bf16 v[94:97], v[138:141], v[214:217], v[94:97]
	v_mfma_f32_16x16x32_bf16 v[86:89], v[134:137], v[214:217], v[86:89]
	v_mfma_f32_16x16x32_bf16 v[78:81], v[138:141], v[222:225], v[78:81]
	v_mfma_f32_16x16x32_bf16 v[70:73], v[134:137], v[222:225], v[70:73]
	v_mfma_f32_16x16x32_bf16 v[126:129], v[130:133], v[166:169], v[126:129]
	v_mfma_f32_16x16x32_bf16 v[118:121], v[146:149], v[166:169], v[118:121]
	v_mfma_f32_16x16x32_bf16 v[110:113], v[130:133], v[204:207], v[110:113]
	v_mfma_f32_16x16x32_bf16 v[102:105], v[146:149], v[204:207], v[102:105]
	v_mfma_f32_16x16x32_bf16 v[94:97], v[130:133], v[218:221], v[94:97]
	v_mfma_f32_16x16x32_bf16 v[86:89], v[146:149], v[218:221], v[86:89]
	v_mfma_f32_16x16x32_bf16 v[78:81], v[130:133], v[226:229], v[78:81]
	v_mfma_f32_16x16x32_bf16 v[70:73], v[146:149], v[226:229], v[70:73]
	s_setprio 0
	s_setprio 1
	v_mfma_f32_16x16x32_bf16 v[122:125], v[142:145], v[162:165], v[122:125]
	v_mfma_f32_16x16x32_bf16 v[114:117], v[154:157], v[162:165], v[114:117]
	v_mfma_f32_16x16x32_bf16 v[106:109], v[142:145], v[170:173], v[106:109]
	v_mfma_f32_16x16x32_bf16 v[98:101], v[154:157], v[170:173], v[98:101]
	v_mfma_f32_16x16x32_bf16 v[90:93], v[142:145], v[214:217], v[90:93]
	v_mfma_f32_16x16x32_bf16 v[82:85], v[154:157], v[214:217], v[82:85]
	v_mfma_f32_16x16x32_bf16 v[74:77], v[142:145], v[222:225], v[74:77]
	v_mfma_f32_16x16x32_bf16 v[66:69], v[154:157], v[222:225], v[66:69]
	v_mfma_f32_16x16x32_bf16 v[122:125], v[150:153], v[166:169], v[122:125]
	v_mfma_f32_16x16x32_bf16 v[114:117], v[158:161], v[166:169], v[114:117]
	v_mfma_f32_16x16x32_bf16 v[106:109], v[150:153], v[204:207], v[106:109]
	v_mfma_f32_16x16x32_bf16 v[98:101], v[158:161], v[204:207], v[98:101]
	v_mfma_f32_16x16x32_bf16 v[90:93], v[150:153], v[218:221], v[90:93]
	v_mfma_f32_16x16x32_bf16 v[82:85], v[158:161], v[218:221], v[82:85]
	v_mfma_f32_16x16x32_bf16 v[74:77], v[150:153], v[226:229], v[74:77]
	v_mfma_f32_16x16x32_bf16 v[66:69], v[158:161], v[226:229], v[66:69]
	s_setprio 0
	s_barrier
	s_mov_b32 m0, s47
	s_add_u32 s98, s6, s81
	s_addc_u32 s99, s7, 0
	ds_read_b128 v[162:165], v202 offset:16384
	ds_read_b128 v[166:169], v202 offset:17408
	ds_read_b128 v[170:173], v202 offset:18432
	ds_read_b128 v[204:207], v202 offset:19456
	ds_read_b128 v[214:217], v202 offset:20480
	ds_read_b128 v[218:221], v202 offset:21504
	ds_read_b128 v[222:225], v202 offset:22528
	ds_read_b128 v[226:229], v202 offset:23552
	global_load_lds_dwordx4 v178, s[98:99]
	s_add_u32 s100, s98, s35
	s_addc_u32 s101, s99, 0
	s_mov_b32 m0, s48
	s_nop 0
	global_load_lds_dwordx4 v178, s[100:101]
	s_add_u32 s98, s6, s81
	s_addc_u32 s99, s7, 0
	s_mov_b32 m0, s49
	s_nop 0
	global_load_lds_dwordx4 v179, s[98:99]
	s_add_u32 s100, s98, s35
	s_addc_u32 s101, s99, 0
	s_mov_b32 m0, s50
	s_nop 0
	global_load_lds_dwordx4 v179, s[100:101]
	s_add_u32 s98, s4, s75
	s_addc_u32 s99, s5, 0
	s_mov_b32 m0, s46
	s_nop 0
	global_load_lds_dwordx4 v1, s[98:99]
	s_add_u32 s100, s98, s31
	s_addc_u32 s101, s99, 0
	s_mov_b32 m0, s51
	s_nop 0
	global_load_lds_dwordx4 v1, s[100:101]
	s_waitcnt vmcnt(8)
	s_waitcnt lgkmcnt(0)
	s_barrier
	s_setprio 1
	s_waitcnt lgkmcnt(0)
	v_mfma_f32_16x16x32_bf16 v[62:65], v[138:141], v[162:165], v[62:65]
	v_mfma_f32_16x16x32_bf16 v[54:57], v[134:137], v[162:165], v[54:57]
	v_mfma_f32_16x16x32_bf16 v[46:49], v[138:141], v[170:173], v[46:49]
	v_mfma_f32_16x16x32_bf16 v[38:41], v[134:137], v[170:173], v[38:41]
	v_mfma_f32_16x16x32_bf16 v[30:33], v[138:141], v[214:217], v[30:33]
	v_mfma_f32_16x16x32_bf16 v[22:25], v[134:137], v[214:217], v[22:25]
	v_mfma_f32_16x16x32_bf16 v[14:17], v[138:141], v[222:225], v[14:17]
	v_mfma_f32_16x16x32_bf16 v[6:9], v[134:137], v[222:225], v[6:9]
	v_mfma_f32_16x16x32_bf16 v[62:65], v[130:133], v[166:169], v[62:65]
	v_mfma_f32_16x16x32_bf16 v[54:57], v[146:149], v[166:169], v[54:57]
	v_mfma_f32_16x16x32_bf16 v[46:49], v[130:133], v[204:207], v[46:49]
	v_mfma_f32_16x16x32_bf16 v[38:41], v[146:149], v[204:207], v[38:41]
	v_mfma_f32_16x16x32_bf16 v[30:33], v[130:133], v[218:221], v[30:33]
	v_mfma_f32_16x16x32_bf16 v[22:25], v[146:149], v[218:221], v[22:25]
	v_mfma_f32_16x16x32_bf16 v[14:17], v[130:133], v[226:229], v[14:17]
	v_mfma_f32_16x16x32_bf16 v[6:9], v[146:149], v[226:229], v[6:9]
	s_setprio 0
	s_setprio 1
	v_mfma_f32_16x16x32_bf16 v[58:61], v[142:145], v[162:165], v[58:61]
	v_mfma_f32_16x16x32_bf16 v[50:53], v[154:157], v[162:165], v[50:53]
	v_mfma_f32_16x16x32_bf16 v[42:45], v[142:145], v[170:173], v[42:45]
	v_mfma_f32_16x16x32_bf16 v[34:37], v[154:157], v[170:173], v[34:37]
	v_mfma_f32_16x16x32_bf16 v[26:29], v[142:145], v[214:217], v[26:29]
	v_mfma_f32_16x16x32_bf16 v[18:21], v[154:157], v[214:217], v[18:21]
	v_mfma_f32_16x16x32_bf16 v[10:13], v[142:145], v[222:225], v[10:13]
	v_mfma_f32_16x16x32_bf16 v[2:5], v[154:157], v[222:225], v[2:5]
	v_mfma_f32_16x16x32_bf16 v[58:61], v[150:153], v[166:169], v[58:61]
	v_mfma_f32_16x16x32_bf16 v[50:53], v[158:161], v[166:169], v[50:53]
	v_mfma_f32_16x16x32_bf16 v[42:45], v[150:153], v[204:207], v[42:45]
	v_mfma_f32_16x16x32_bf16 v[34:37], v[158:161], v[204:207], v[34:37]
	v_mfma_f32_16x16x32_bf16 v[26:29], v[150:153], v[218:221], v[26:29]
	v_mfma_f32_16x16x32_bf16 v[18:21], v[158:161], v[218:221], v[18:21]
	v_mfma_f32_16x16x32_bf16 v[10:13], v[150:153], v[226:229], v[10:13]
	v_mfma_f32_16x16x32_bf16 v[2:5], v[158:161], v[226:229], v[2:5]
	s_setprio 0
	s_barrier
	ds_read_b128 v[130:133], v194
	ds_read_b128 v[134:137], v195
	ds_read_b128 v[138:141], v186
	ds_read_b128 v[142:145], v187
	ds_read_b128 v[146:149], v196
	ds_read_b128 v[150:153], v197
	ds_read_b128 v[154:157], v198
	ds_read_b128 v[158:161], v199
	s_mov_b32 m0, s52
	s_add_u32 s98, s4, s75
	s_addc_u32 s99, s5, 0
	ds_read_b128 v[162:165], v202 offset:32768
	ds_read_b128 v[166:169], v202 offset:33792
	ds_read_b128 v[170:173], v202 offset:34816
	ds_read_b128 v[204:207], v202 offset:35840
	ds_read_b128 v[214:217], v202 offset:36864
	ds_read_b128 v[218:221], v202 offset:37888
	ds_read_b128 v[222:225], v202 offset:38912
	ds_read_b128 v[226:229], v202 offset:39936
	global_load_lds_dwordx4 v180, s[98:99]
	s_add_u32 s100, s98, s31
	s_addc_u32 s101, s99, 0
	s_mov_b32 m0, s53
	s_nop 0
	global_load_lds_dwordx4 v180, s[100:101]
	s_waitcnt vmcnt(8)
	s_waitcnt lgkmcnt(0)
	s_barrier
	s_setprio 1
	s_waitcnt lgkmcnt(0)
	v_mfma_f32_16x16x32_bf16 v[126:129], v[138:141], v[162:165], v[126:129]
	v_mfma_f32_16x16x32_bf16 v[118:121], v[134:137], v[162:165], v[118:121]
	v_mfma_f32_16x16x32_bf16 v[110:113], v[138:141], v[170:173], v[110:113]
	v_mfma_f32_16x16x32_bf16 v[102:105], v[134:137], v[170:173], v[102:105]
	v_mfma_f32_16x16x32_bf16 v[94:97], v[138:141], v[214:217], v[94:97]
	v_mfma_f32_16x16x32_bf16 v[86:89], v[134:137], v[214:217], v[86:89]
	v_mfma_f32_16x16x32_bf16 v[78:81], v[138:141], v[222:225], v[78:81]
	v_mfma_f32_16x16x32_bf16 v[70:73], v[134:137], v[222:225], v[70:73]
	v_mfma_f32_16x16x32_bf16 v[126:129], v[130:133], v[166:169], v[126:129]
	v_mfma_f32_16x16x32_bf16 v[118:121], v[146:149], v[166:169], v[118:121]
	v_mfma_f32_16x16x32_bf16 v[110:113], v[130:133], v[204:207], v[110:113]
	v_mfma_f32_16x16x32_bf16 v[102:105], v[146:149], v[204:207], v[102:105]
	v_mfma_f32_16x16x32_bf16 v[94:97], v[130:133], v[218:221], v[94:97]
	v_mfma_f32_16x16x32_bf16 v[86:89], v[146:149], v[218:221], v[86:89]
	v_mfma_f32_16x16x32_bf16 v[78:81], v[130:133], v[226:229], v[78:81]
	v_mfma_f32_16x16x32_bf16 v[70:73], v[146:149], v[226:229], v[70:73]
	s_setprio 0
	s_setprio 1
	v_mfma_f32_16x16x32_bf16 v[122:125], v[142:145], v[162:165], v[122:125]
	v_mfma_f32_16x16x32_bf16 v[114:117], v[154:157], v[162:165], v[114:117]
	v_mfma_f32_16x16x32_bf16 v[106:109], v[142:145], v[170:173], v[106:109]
	v_mfma_f32_16x16x32_bf16 v[98:101], v[154:157], v[170:173], v[98:101]
	v_mfma_f32_16x16x32_bf16 v[90:93], v[142:145], v[214:217], v[90:93]
	v_mfma_f32_16x16x32_bf16 v[82:85], v[154:157], v[214:217], v[82:85]
	v_mfma_f32_16x16x32_bf16 v[74:77], v[142:145], v[222:225], v[74:77]
	v_mfma_f32_16x16x32_bf16 v[66:69], v[154:157], v[222:225], v[66:69]
	v_mfma_f32_16x16x32_bf16 v[122:125], v[150:153], v[166:169], v[122:125]
	v_mfma_f32_16x16x32_bf16 v[114:117], v[158:161], v[166:169], v[114:117]
	v_mfma_f32_16x16x32_bf16 v[106:109], v[150:153], v[204:207], v[106:109]
	v_mfma_f32_16x16x32_bf16 v[98:101], v[158:161], v[204:207], v[98:101]
	v_mfma_f32_16x16x32_bf16 v[90:93], v[150:153], v[218:221], v[90:93]
	v_mfma_f32_16x16x32_bf16 v[82:85], v[158:161], v[218:221], v[82:85]
	v_mfma_f32_16x16x32_bf16 v[74:77], v[150:153], v[226:229], v[74:77]
	v_mfma_f32_16x16x32_bf16 v[66:69], v[158:161], v[226:229], v[66:69]
	s_setprio 0
	s_barrier
	s_addk_i32 s81, 0x80
	s_mov_b32 m0, s55
	s_add_u32 s98, s6, s81
	s_addc_u32 s99, s7, 0
	ds_read_b128 v[162:165], v202 offset:49152
	ds_read_b128 v[166:169], v202 offset:50176
	ds_read_b128 v[170:173], v202 offset:51200
	ds_read_b128 v[204:207], v202 offset:52224
	ds_read_b128 v[214:217], v202 offset:53248
	ds_read_b128 v[218:221], v202 offset:54272
	ds_read_b128 v[222:225], v202 offset:55296
	ds_read_b128 v[226:229], v202 offset:56320
	global_load_lds_dwordx4 v178, s[98:99]
	s_add_u32 s100, s98, s35
	s_addc_u32 s101, s99, 0
	s_mov_b32 m0, s56
	s_nop 0
	global_load_lds_dwordx4 v178, s[100:101]
	s_add_u32 s98, s6, s81
	s_addc_u32 s99, s7, 0
	s_mov_b32 m0, s59
	s_nop 0
	global_load_lds_dwordx4 v179, s[98:99]
	s_add_u32 s100, s98, s35
	s_addc_u32 s101, s99, 0
	s_mov_b32 m0, s60
	s_nop 0
	global_load_lds_dwordx4 v179, s[100:101]
	s_add_u32 s98, s4, s75
	s_addc_u32 s99, s5, 0
	s_mov_b32 m0, s57
	s_nop 0
	global_load_lds_dwordx4 v181, s[98:99]
	s_add_u32 s100, s98, s31
	s_addc_u32 s101, s99, 0
	s_mov_b32 m0, s58
	s_nop 0
	global_load_lds_dwordx4 v181, s[100:101]
	s_waitcnt vmcnt(8)
	s_waitcnt lgkmcnt(0)
	s_barrier
	s_setprio 1
	s_waitcnt lgkmcnt(0)
	v_mfma_f32_16x16x32_bf16 v[62:65], v[138:141], v[162:165], v[62:65]
	v_mfma_f32_16x16x32_bf16 v[54:57], v[134:137], v[162:165], v[54:57]
	v_mfma_f32_16x16x32_bf16 v[46:49], v[138:141], v[170:173], v[46:49]
	v_mfma_f32_16x16x32_bf16 v[38:41], v[134:137], v[170:173], v[38:41]
	v_mfma_f32_16x16x32_bf16 v[30:33], v[138:141], v[214:217], v[30:33]
	v_mfma_f32_16x16x32_bf16 v[22:25], v[134:137], v[214:217], v[22:25]
	v_mfma_f32_16x16x32_bf16 v[14:17], v[138:141], v[222:225], v[14:17]
	v_mfma_f32_16x16x32_bf16 v[6:9], v[134:137], v[222:225], v[6:9]
	v_mfma_f32_16x16x32_bf16 v[62:65], v[130:133], v[166:169], v[62:65]
	v_mfma_f32_16x16x32_bf16 v[54:57], v[146:149], v[166:169], v[54:57]
	v_mfma_f32_16x16x32_bf16 v[46:49], v[130:133], v[204:207], v[46:49]
	v_mfma_f32_16x16x32_bf16 v[38:41], v[146:149], v[204:207], v[38:41]
	v_mfma_f32_16x16x32_bf16 v[30:33], v[130:133], v[218:221], v[30:33]
	v_mfma_f32_16x16x32_bf16 v[22:25], v[146:149], v[218:221], v[22:25]
	v_mfma_f32_16x16x32_bf16 v[14:17], v[130:133], v[226:229], v[14:17]
	v_mfma_f32_16x16x32_bf16 v[6:9], v[146:149], v[226:229], v[6:9]
	s_setprio 0
	s_setprio 1
	v_mfma_f32_16x16x32_bf16 v[58:61], v[142:145], v[162:165], v[58:61]
	v_mfma_f32_16x16x32_bf16 v[50:53], v[154:157], v[162:165], v[50:53]
	v_mfma_f32_16x16x32_bf16 v[42:45], v[142:145], v[170:173], v[42:45]
	v_mfma_f32_16x16x32_bf16 v[34:37], v[154:157], v[170:173], v[34:37]
	v_mfma_f32_16x16x32_bf16 v[26:29], v[142:145], v[214:217], v[26:29]
	v_mfma_f32_16x16x32_bf16 v[18:21], v[154:157], v[214:217], v[18:21]
	v_mfma_f32_16x16x32_bf16 v[10:13], v[142:145], v[222:225], v[10:13]
	v_mfma_f32_16x16x32_bf16 v[2:5], v[154:157], v[222:225], v[2:5]
	v_mfma_f32_16x16x32_bf16 v[58:61], v[150:153], v[166:169], v[58:61]
	v_mfma_f32_16x16x32_bf16 v[50:53], v[158:161], v[166:169], v[50:53]
	v_mfma_f32_16x16x32_bf16 v[42:45], v[150:153], v[204:207], v[42:45]
	v_mfma_f32_16x16x32_bf16 v[34:37], v[158:161], v[204:207], v[34:37]
	v_mfma_f32_16x16x32_bf16 v[26:29], v[150:153], v[218:221], v[26:29]
	v_mfma_f32_16x16x32_bf16 v[18:21], v[158:161], v[218:221], v[18:21]
	v_mfma_f32_16x16x32_bf16 v[10:13], v[150:153], v[226:229], v[10:13]
	v_mfma_f32_16x16x32_bf16 v[2:5], v[158:161], v[226:229], v[2:5]
	s_setprio 0
	s_barrier
	s_add_i32 s80, s80, 2
	s_addk_i32 s28, 0x100
	s_addk_i32 s79, 0x100
	s_cmp_ge_i32 s80, s61
	s_cbranch_scc0 .LBB0_637

.LBB0_1183:
	ds_read_b128 v[114:117], v206
	ds_read_b128 v[118:121], v207
	ds_read_b128 v[122:125], v202
	ds_read_b128 v[126:129], v203
	ds_read_b128 v[146:149], v208
	ds_read_b128 v[150:153], v209
	ds_read_b128 v[154:157], v211
	ds_read_b128 v[158:161], v213
	s_add_i32 s60, s6, 0x80
	s_cmp_eq_u32 s90, s59
	s_cselect_b32 s61, s5, s58
	s_cselect_b32 s60, s7, s60
	s_add_u32 s98, s8, s6
	s_addc_u32 s99, s9, 0
	s_add_i32 m0, s70, 0xc000
	ds_read_b128 v[162:165], v222
	ds_read_b128 v[170:173], v222 offset:1024
	ds_read_b128 v[174:177], v222 offset:2048
	ds_read_b128 v[178:181], v222 offset:3072
	ds_read_b128 v[182:185], v222 offset:4096
	ds_read_b128 v[186:189], v222 offset:5120
	ds_read_b128 v[190:193], v222 offset:6144
	ds_read_b128 v[226:229], v222 offset:7168
	global_load_lds_dwordx4 v221, s[98:99]
	s_add_u32 s100, s8, s6
	s_addc_u32 s101, s9, 0
	s_add_i32 m0, s70, 0xe000
	s_nop 0
	global_load_lds_dwordx4 v220, s[100:101]
	s_waitcnt vmcnt(8)
	s_waitcnt lgkmcnt(0)
	s_barrier
	s_setprio 1
	s_waitcnt lgkmcnt(0)
	v_mfma_f32_16x16x32_bf16 v[142:145], v[122:125], v[162:165], v[142:145]
	v_mfma_f32_16x16x32_bf16 v[138:141], v[118:121], v[162:165], v[138:141]
	v_mfma_f32_16x16x32_bf16 v[110:113], v[122:125], v[174:177], v[110:113]
	v_mfma_f32_16x16x32_bf16 v[106:109], v[118:121], v[174:177], v[106:109]
	v_mfma_f32_16x16x32_bf16 v[94:97], v[122:125], v[182:185], v[94:97]
	v_mfma_f32_16x16x32_bf16 v[90:93], v[118:121], v[182:185], v[90:93]
	v_mfma_f32_16x16x32_bf16 v[78:81], v[122:125], v[190:193], v[78:81]
	v_mfma_f32_16x16x32_bf16 v[74:77], v[118:121], v[190:193], v[74:77]
	v_mfma_f32_16x16x32_bf16 v[142:145], v[114:117], v[170:173], v[142:145]
	v_mfma_f32_16x16x32_bf16 v[138:141], v[146:149], v[170:173], v[138:141]
	v_mfma_f32_16x16x32_bf16 v[110:113], v[114:117], v[178:181], v[110:113]
	v_mfma_f32_16x16x32_bf16 v[106:109], v[146:149], v[178:181], v[106:109]
	v_mfma_f32_16x16x32_bf16 v[94:97], v[114:117], v[186:189], v[94:97]
	v_mfma_f32_16x16x32_bf16 v[90:93], v[146:149], v[186:189], v[90:93]
	v_mfma_f32_16x16x32_bf16 v[78:81], v[114:117], v[226:229], v[78:81]
	v_mfma_f32_16x16x32_bf16 v[74:77], v[146:149], v[226:229], v[74:77]
	s_setprio 0
	s_setprio 1
	v_mfma_f32_16x16x32_bf16 v[134:137], v[126:129], v[162:165], v[134:137]
	v_mfma_f32_16x16x32_bf16 v[130:133], v[154:157], v[162:165], v[130:133]
	v_mfma_f32_16x16x32_bf16 v[102:105], v[126:129], v[174:177], v[102:105]
	v_mfma_f32_16x16x32_bf16 v[98:101], v[154:157], v[174:177], v[98:101]
	v_mfma_f32_16x16x32_bf16 v[86:89], v[126:129], v[182:185], v[86:89]
	v_mfma_f32_16x16x32_bf16 v[82:85], v[154:157], v[182:185], v[82:85]
	v_mfma_f32_16x16x32_bf16 v[70:73], v[126:129], v[190:193], v[70:73]
	v_mfma_f32_16x16x32_bf16 v[66:69], v[154:157], v[190:193], v[66:69]
	v_mfma_f32_16x16x32_bf16 v[134:137], v[150:153], v[170:173], v[134:137]
	v_mfma_f32_16x16x32_bf16 v[130:133], v[158:161], v[170:173], v[130:133]
	v_mfma_f32_16x16x32_bf16 v[102:105], v[150:153], v[178:181], v[102:105]
	v_mfma_f32_16x16x32_bf16 v[98:101], v[158:161], v[178:181], v[98:101]
	v_mfma_f32_16x16x32_bf16 v[86:89], v[150:153], v[186:189], v[86:89]
	v_mfma_f32_16x16x32_bf16 v[82:85], v[158:161], v[186:189], v[82:85]
	v_mfma_f32_16x16x32_bf16 v[70:73], v[150:153], v[226:229], v[70:73]
	v_mfma_f32_16x16x32_bf16 v[66:69], v[158:161], v[226:229], v[66:69]
	s_setprio 0
	s_barrier
	s_mov_b32 m0, s71
	s_add_u32 s98, s20, s61
	s_addc_u32 s99, s21, 0
	ds_read_b128 v[162:165], v222 offset:16384
	ds_read_b128 v[170:173], v222 offset:17408
	ds_read_b128 v[174:177], v222 offset:18432
	ds_read_b128 v[178:181], v222 offset:19456
	ds_read_b128 v[182:185], v222 offset:20480
	ds_read_b128 v[186:189], v222 offset:21504
	ds_read_b128 v[190:193], v222 offset:22528
	ds_read_b128 v[226:229], v222 offset:23552
	global_load_lds_dwordx4 v196, s[98:99]
	s_add_u32 s100, s98, s35
	s_addc_u32 s101, s99, 0
	s_mov_b32 m0, s72
	s_nop 0
	global_load_lds_dwordx4 v196, s[100:101]
	s_add_u32 s98, s20, s61
	s_addc_u32 s99, s21, 0
	s_mov_b32 m0, s73
	s_nop 0
	global_load_lds_dwordx4 v197, s[98:99]
	s_add_u32 s100, s98, s35
	s_addc_u32 s101, s99, 0
	s_mov_b32 m0, s76
	s_nop 0
	global_load_lds_dwordx4 v197, s[100:101]
	s_add_u32 s98, s8, s60
	s_addc_u32 s99, s9, 0
	s_mov_b32 m0, s70
	s_nop 0
	global_load_lds_dwordx4 v1, s[98:99]
	s_add_u32 s100, s98, s29
	s_addc_u32 s101, s99, 0
	s_mov_b32 m0, s77
	s_nop 0
	global_load_lds_dwordx4 v1, s[100:101]
	s_waitcnt vmcnt(8)
	s_waitcnt lgkmcnt(0)
	s_barrier
	s_setprio 1
	s_waitcnt lgkmcnt(0)
	v_mfma_f32_16x16x32_bf16 v[62:65], v[122:125], v[162:165], v[62:65]
	v_mfma_f32_16x16x32_bf16 v[58:61], v[118:121], v[162:165], v[58:61]
	v_mfma_f32_16x16x32_bf16 v[46:49], v[122:125], v[174:177], v[46:49]
	v_mfma_f32_16x16x32_bf16 v[42:45], v[118:121], v[174:177], v[42:45]
	v_mfma_f32_16x16x32_bf16 v[30:33], v[122:125], v[182:185], v[30:33]
	v_mfma_f32_16x16x32_bf16 v[26:29], v[118:121], v[182:185], v[26:29]
	v_mfma_f32_16x16x32_bf16 v[14:17], v[122:125], v[190:193], v[14:17]
	v_mfma_f32_16x16x32_bf16 v[10:13], v[118:121], v[190:193], v[10:13]
	v_mfma_f32_16x16x32_bf16 v[62:65], v[114:117], v[170:173], v[62:65]
	v_mfma_f32_16x16x32_bf16 v[58:61], v[146:149], v[170:173], v[58:61]
	v_mfma_f32_16x16x32_bf16 v[46:49], v[114:117], v[178:181], v[46:49]
	v_mfma_f32_16x16x32_bf16 v[42:45], v[146:149], v[178:181], v[42:45]
	v_mfma_f32_16x16x32_bf16 v[30:33], v[114:117], v[186:189], v[30:33]
	v_mfma_f32_16x16x32_bf16 v[26:29], v[146:149], v[186:189], v[26:29]
	v_mfma_f32_16x16x32_bf16 v[14:17], v[114:117], v[226:229], v[14:17]
	v_mfma_f32_16x16x32_bf16 v[10:13], v[146:149], v[226:229], v[10:13]
	s_setprio 0
	s_setprio 1
	v_mfma_f32_16x16x32_bf16 v[54:57], v[126:129], v[162:165], v[54:57]
	v_mfma_f32_16x16x32_bf16 v[50:53], v[154:157], v[162:165], v[50:53]
	v_mfma_f32_16x16x32_bf16 v[38:41], v[126:129], v[174:177], v[38:41]
	v_mfma_f32_16x16x32_bf16 v[34:37], v[154:157], v[174:177], v[34:37]
	v_mfma_f32_16x16x32_bf16 v[22:25], v[126:129], v[182:185], v[22:25]
	v_mfma_f32_16x16x32_bf16 v[18:21], v[154:157], v[182:185], v[18:21]
	v_mfma_f32_16x16x32_bf16 v[6:9], v[126:129], v[190:193], v[6:9]
	v_mfma_f32_16x16x32_bf16 v[2:5], v[154:157], v[190:193], v[2:5]
	v_mfma_f32_16x16x32_bf16 v[54:57], v[150:153], v[170:173], v[54:57]
	v_mfma_f32_16x16x32_bf16 v[50:53], v[158:161], v[170:173], v[50:53]
	v_mfma_f32_16x16x32_bf16 v[38:41], v[150:153], v[178:181], v[38:41]
	v_mfma_f32_16x16x32_bf16 v[34:37], v[158:161], v[178:181], v[34:37]
	v_mfma_f32_16x16x32_bf16 v[22:25], v[150:153], v[186:189], v[22:25]
	v_mfma_f32_16x16x32_bf16 v[18:21], v[158:161], v[186:189], v[18:21]
	v_mfma_f32_16x16x32_bf16 v[6:9], v[150:153], v[226:229], v[6:9]
	v_mfma_f32_16x16x32_bf16 v[2:5], v[158:161], v[226:229], v[2:5]
	s_setprio 0
	s_barrier
	ds_read_b128 v[114:117], v214
	ds_read_b128 v[118:121], v215
	ds_read_b128 v[122:125], v204
	ds_read_b128 v[126:129], v205
	ds_read_b128 v[146:149], v216
	ds_read_b128 v[150:153], v217
	ds_read_b128 v[154:157], v218
	ds_read_b128 v[158:161], v219
	s_mov_b32 m0, s78
	s_add_u32 s98, s8, s60
	s_addc_u32 s99, s9, 0
	ds_read_b128 v[162:165], v222 offset:32768
	ds_read_b128 v[170:173], v222 offset:33792
	ds_read_b128 v[174:177], v222 offset:34816
	ds_read_b128 v[178:181], v222 offset:35840
	ds_read_b128 v[182:185], v222 offset:36864
	ds_read_b128 v[186:189], v222 offset:37888
	ds_read_b128 v[190:193], v222 offset:38912
	ds_read_b128 v[226:229], v222 offset:39936
	global_load_lds_dwordx4 v198, s[98:99]
	s_add_u32 s100, s98, s29
	s_addc_u32 s101, s99, 0
	s_mov_b32 m0, s79
	s_nop 0
	global_load_lds_dwordx4 v198, s[100:101]
	s_waitcnt vmcnt(8)
	s_waitcnt lgkmcnt(0)
	s_barrier
	s_setprio 1
	s_waitcnt lgkmcnt(0)
	v_mfma_f32_16x16x32_bf16 v[142:145], v[122:125], v[162:165], v[142:145]
	v_mfma_f32_16x16x32_bf16 v[138:141], v[118:121], v[162:165], v[138:141]
	v_mfma_f32_16x16x32_bf16 v[110:113], v[122:125], v[174:177], v[110:113]
	v_mfma_f32_16x16x32_bf16 v[106:109], v[118:121], v[174:177], v[106:109]
	v_mfma_f32_16x16x32_bf16 v[94:97], v[122:125], v[182:185], v[94:97]
	v_mfma_f32_16x16x32_bf16 v[90:93], v[118:121], v[182:185], v[90:93]
	v_mfma_f32_16x16x32_bf16 v[78:81], v[122:125], v[190:193], v[78:81]
	v_mfma_f32_16x16x32_bf16 v[74:77], v[118:121], v[190:193], v[74:77]
	v_mfma_f32_16x16x32_bf16 v[142:145], v[114:117], v[170:173], v[142:145]
	v_mfma_f32_16x16x32_bf16 v[138:141], v[146:149], v[170:173], v[138:141]
	v_mfma_f32_16x16x32_bf16 v[110:113], v[114:117], v[178:181], v[110:113]
	v_mfma_f32_16x16x32_bf16 v[106:109], v[146:149], v[178:181], v[106:109]
	v_mfma_f32_16x16x32_bf16 v[94:97], v[114:117], v[186:189], v[94:97]
	v_mfma_f32_16x16x32_bf16 v[90:93], v[146:149], v[186:189], v[90:93]
	v_mfma_f32_16x16x32_bf16 v[78:81], v[114:117], v[226:229], v[78:81]
	v_mfma_f32_16x16x32_bf16 v[74:77], v[146:149], v[226:229], v[74:77]
	s_setprio 0
	s_setprio 1
	v_mfma_f32_16x16x32_bf16 v[134:137], v[126:129], v[162:165], v[134:137]
	v_mfma_f32_16x16x32_bf16 v[130:133], v[154:157], v[162:165], v[130:133]
	v_mfma_f32_16x16x32_bf16 v[102:105], v[126:129], v[174:177], v[102:105]
	v_mfma_f32_16x16x32_bf16 v[98:101], v[154:157], v[174:177], v[98:101]
	v_mfma_f32_16x16x32_bf16 v[86:89], v[126:129], v[182:185], v[86:89]
	v_mfma_f32_16x16x32_bf16 v[82:85], v[154:157], v[182:185], v[82:85]
	v_mfma_f32_16x16x32_bf16 v[70:73], v[126:129], v[190:193], v[70:73]
	v_mfma_f32_16x16x32_bf16 v[66:69], v[154:157], v[190:193], v[66:69]
	v_mfma_f32_16x16x32_bf16 v[134:137], v[150:153], v[170:173], v[134:137]
	v_mfma_f32_16x16x32_bf16 v[130:133], v[158:161], v[170:173], v[130:133]
	v_mfma_f32_16x16x32_bf16 v[102:105], v[150:153], v[178:181], v[102:105]
	v_mfma_f32_16x16x32_bf16 v[98:101], v[158:161], v[178:181], v[98:101]
	v_mfma_f32_16x16x32_bf16 v[86:89], v[150:153], v[186:189], v[86:89]
	v_mfma_f32_16x16x32_bf16 v[82:85], v[158:161], v[186:189], v[82:85]
	v_mfma_f32_16x16x32_bf16 v[70:73], v[150:153], v[226:229], v[70:73]
	v_mfma_f32_16x16x32_bf16 v[66:69], v[158:161], v[226:229], v[66:69]
	s_setprio 0
	s_barrier
	s_addk_i32 s61, 0x80
	s_mov_b32 m0, s81
	s_add_u32 s98, s20, s61
	s_addc_u32 s99, s21, 0
	ds_read_b128 v[162:165], v222 offset:49152
	ds_read_b128 v[170:173], v222 offset:50176
	ds_read_b128 v[174:177], v222 offset:51200
	ds_read_b128 v[178:181], v222 offset:52224
	ds_read_b128 v[182:185], v222 offset:53248
	ds_read_b128 v[186:189], v222 offset:54272
	ds_read_b128 v[190:193], v222 offset:55296
	ds_read_b128 v[226:229], v222 offset:56320
	global_load_lds_dwordx4 v196, s[98:99]
	s_add_u32 s100, s98, s35
	s_addc_u32 s101, s99, 0
	s_mov_b32 m0, s82
	s_nop 0
	global_load_lds_dwordx4 v196, s[100:101]
	s_add_u32 s98, s20, s61
	s_addc_u32 s99, s21, 0
	s_mov_b32 m0, s85
	s_nop 0
	global_load_lds_dwordx4 v197, s[98:99]
	s_add_u32 s100, s98, s35
	s_addc_u32 s101, s99, 0
	s_mov_b32 m0, s86
	s_nop 0
	global_load_lds_dwordx4 v197, s[100:101]
	s_add_u32 s98, s8, s60
	s_addc_u32 s99, s9, 0
	s_mov_b32 m0, s83
	s_nop 0
	global_load_lds_dwordx4 v201, s[98:99]
	s_add_u32 s100, s98, s29
	s_addc_u32 s101, s99, 0
	s_mov_b32 m0, s84
	s_nop 0
	global_load_lds_dwordx4 v201, s[100:101]
	s_waitcnt vmcnt(8)
	s_waitcnt lgkmcnt(0)
	s_barrier
	s_setprio 1
	s_waitcnt lgkmcnt(0)
	v_mfma_f32_16x16x32_bf16 v[62:65], v[122:125], v[162:165], v[62:65]
	v_mfma_f32_16x16x32_bf16 v[58:61], v[118:121], v[162:165], v[58:61]
	v_mfma_f32_16x16x32_bf16 v[46:49], v[122:125], v[174:177], v[46:49]
	v_mfma_f32_16x16x32_bf16 v[42:45], v[118:121], v[174:177], v[42:45]
	v_mfma_f32_16x16x32_bf16 v[30:33], v[122:125], v[182:185], v[30:33]
	v_mfma_f32_16x16x32_bf16 v[26:29], v[118:121], v[182:185], v[26:29]
	v_mfma_f32_16x16x32_bf16 v[14:17], v[122:125], v[190:193], v[14:17]
	v_mfma_f32_16x16x32_bf16 v[10:13], v[118:121], v[190:193], v[10:13]
	v_mfma_f32_16x16x32_bf16 v[62:65], v[114:117], v[170:173], v[62:65]
	v_mfma_f32_16x16x32_bf16 v[58:61], v[146:149], v[170:173], v[58:61]
	v_mfma_f32_16x16x32_bf16 v[46:49], v[114:117], v[178:181], v[46:49]
	v_mfma_f32_16x16x32_bf16 v[42:45], v[146:149], v[178:181], v[42:45]
	v_mfma_f32_16x16x32_bf16 v[30:33], v[114:117], v[186:189], v[30:33]
	v_mfma_f32_16x16x32_bf16 v[26:29], v[146:149], v[186:189], v[26:29]
	v_mfma_f32_16x16x32_bf16 v[14:17], v[114:117], v[226:229], v[14:17]
	v_mfma_f32_16x16x32_bf16 v[10:13], v[146:149], v[226:229], v[10:13]
	s_setprio 0
	s_setprio 1
	v_mfma_f32_16x16x32_bf16 v[54:57], v[126:129], v[162:165], v[54:57]
	v_mfma_f32_16x16x32_bf16 v[50:53], v[154:157], v[162:165], v[50:53]
	v_mfma_f32_16x16x32_bf16 v[38:41], v[126:129], v[174:177], v[38:41]
	v_mfma_f32_16x16x32_bf16 v[34:37], v[154:157], v[174:177], v[34:37]
	v_mfma_f32_16x16x32_bf16 v[22:25], v[126:129], v[182:185], v[22:25]
	v_mfma_f32_16x16x32_bf16 v[18:21], v[154:157], v[182:185], v[18:21]
	v_mfma_f32_16x16x32_bf16 v[6:9], v[126:129], v[190:193], v[6:9]
	v_mfma_f32_16x16x32_bf16 v[2:5], v[154:157], v[190:193], v[2:5]
	v_mfma_f32_16x16x32_bf16 v[54:57], v[150:153], v[170:173], v[54:57]
	v_mfma_f32_16x16x32_bf16 v[50:53], v[158:161], v[170:173], v[50:53]
	v_mfma_f32_16x16x32_bf16 v[38:41], v[150:153], v[178:181], v[38:41]
	v_mfma_f32_16x16x32_bf16 v[34:37], v[158:161], v[178:181], v[34:37]
	v_mfma_f32_16x16x32_bf16 v[22:25], v[150:153], v[186:189], v[22:25]
	v_mfma_f32_16x16x32_bf16 v[18:21], v[158:161], v[186:189], v[18:21]
	v_mfma_f32_16x16x32_bf16 v[6:9], v[150:153], v[226:229], v[6:9]
	v_mfma_f32_16x16x32_bf16 v[2:5], v[158:161], v[226:229], v[2:5]
	s_setprio 0
	s_barrier
	s_add_i32 s59, s59, 2
	s_addk_i32 s6, 0x100
	s_addk_i32 s58, 0x100
	s_cmp_ge_i32 s59, s87
	s_cbranch_scc0 .LBB0_1183

.LBB0_1603:
	ds_read_b128 v[18:21], v235
	ds_read_b128 v[22:25], v236
	ds_read_b128 v[26:29], v243
	ds_read_b128 v[30:33], v244
	s_waitcnt lgkmcnt(0)
	ds_read_b128 v[2:5], v237
	ds_read_b128 v[6:9], v238
	ds_read_b128 v[10:13], v245
	ds_read_b128 v[14:17], v246
	s_add_i32 s63, s6, 0x80
	s_cmp_eq_u32 s89, s62
	s_cselect_b32 s65, s7, s63
	s_cselect_b32 s64, s5, s61
	s_add_i32 s63, s65, 0x80
	ds_read_b128 v[162:165], v251
	ds_read_b128 v[166:169], v251 offset:1024
	ds_read_b128 v[170:173], v251 offset:2048
	ds_read_b128 v[174:177], v251 offset:3072
	ds_read_b128 v[178:181], v251 offset:4096
	ds_read_b128 v[182:185], v251 offset:5120
	ds_read_b128 v[186:189], v251 offset:6144
	ds_read_b128 v[190:193], v251 offset:7168
	s_add_i32 s66, s6, s86
	s_add_u32 s98, s8, s66
	s_addc_u32 s99, s9, 0
	s_add_i32 m0, s70, 0xc000
	s_add_i32 s66, s6, s93
	global_load_lds_dwordx4 v1, s[98:99]
	s_add_i32 m0, s70, 0xe000
	s_add_u32 s100, s8, s66
	s_addc_u32 s101, s9, 0
	global_load_lds_dwordx4 v1, s[100:101]
	s_waitcnt vmcnt(8)
	s_waitcnt lgkmcnt(0)
	s_barrier
	s_setprio 1
	s_waitcnt lgkmcnt(0)
	v_mfma_f32_16x16x128_f8f6f4 v[158:161], v[18:25], v[162:169], v[158:161]
	v_mfma_f32_16x16x128_f8f6f4 v[154:157], v[26:33], v[162:169], v[154:157]
	v_mfma_f32_16x16x128_f8f6f4 v[142:145], v[18:25], v[170:177], v[142:145]
	v_mfma_f32_16x16x128_f8f6f4 v[138:141], v[26:33], v[170:177], v[138:141]
	v_mfma_f32_16x16x128_f8f6f4 v[126:129], v[18:25], v[178:185], v[126:129]
	v_mfma_f32_16x16x128_f8f6f4 v[122:125], v[26:33], v[178:185], v[122:125]
	v_mfma_f32_16x16x128_f8f6f4 v[110:113], v[18:25], v[186:193], v[110:113]
	v_mfma_f32_16x16x128_f8f6f4 v[106:109], v[26:33], v[186:193], v[106:109]
	s_setprio 0
	s_setprio 1
	v_mfma_f32_16x16x128_f8f6f4 v[150:153], v[2:9], v[162:169], v[150:153]
	v_mfma_f32_16x16x128_f8f6f4 v[146:149], v[10:17], v[162:169], v[146:149]
	v_mfma_f32_16x16x128_f8f6f4 v[134:137], v[2:9], v[170:177], v[134:137]
	v_mfma_f32_16x16x128_f8f6f4 v[130:133], v[10:17], v[170:177], v[130:133]
	v_mfma_f32_16x16x128_f8f6f4 v[118:121], v[2:9], v[178:185], v[118:121]
	v_mfma_f32_16x16x128_f8f6f4 v[114:117], v[10:17], v[178:185], v[114:117]
	v_mfma_f32_16x16x128_f8f6f4 v[102:105], v[2:9], v[186:193], v[102:105]
	v_mfma_f32_16x16x128_f8f6f4 v[98:101], v[10:17], v[186:193], v[98:101]
	s_setprio 0
	s_barrier
	ds_read_b128 v[162:165], v251 offset:16384
	ds_read_b128 v[166:169], v251 offset:17408
	ds_read_b128 v[170:173], v251 offset:18432
	ds_read_b128 v[174:177], v251 offset:19456
	ds_read_b128 v[178:181], v251 offset:20480
	ds_read_b128 v[182:185], v251 offset:21504
	ds_read_b128 v[186:189], v251 offset:22528
	ds_read_b128 v[190:193], v251 offset:23552
	s_mov_b32 m0, s71
	s_add_u32 s98, s20, s64
	s_addc_u32 s99, s21, 0
	global_load_lds_dwordx4 v211, s[98:99]
	s_add_i32 s66, s64, s35
	s_add_u32 s100, s20, s66
	s_addc_u32 s101, s21, 0
	s_mov_b32 m0, s72
	s_add_i32 s66, s66, s35
	global_load_lds_dwordx4 v211, s[100:101]
	s_mov_b32 m0, s73
	s_add_u32 s98, s20, s66
	s_addc_u32 s99, s21, 0
	global_load_lds_dwordx4 v211, s[98:99]
	s_add_i32 s66, s66, s35
	s_add_u32 s100, s20, s66
	s_addc_u32 s101, s21, 0
	s_mov_b32 m0, s76
	s_nop 0
	global_load_lds_dwordx4 v211, s[100:101]
	s_mov_b32 m0, s70
	s_add_u32 s98, s8, s65
	s_addc_u32 s99, s9, 0
	global_load_lds_dwordx4 v1, s[98:99]
	s_add_i32 s65, s65, s23
	s_add_u32 s100, s8, s65
	s_addc_u32 s101, s9, 0
	s_mov_b32 m0, s77
	s_nop 0
	global_load_lds_dwordx4 v1, s[100:101]
	s_waitcnt vmcnt(8)
	s_waitcnt lgkmcnt(0)
	s_barrier
	s_setprio 1
	s_waitcnt lgkmcnt(0)
	v_mfma_f32_16x16x128_f8f6f4 v[94:97], v[18:25], v[162:169], v[94:97]
	v_mfma_f32_16x16x128_f8f6f4 v[90:93], v[26:33], v[162:169], v[90:93]
	v_mfma_f32_16x16x128_f8f6f4 v[78:81], v[18:25], v[170:177], v[78:81]
	v_mfma_f32_16x16x128_f8f6f4 v[74:77], v[26:33], v[170:177], v[74:77]
	v_mfma_f32_16x16x128_f8f6f4 v[62:65], v[18:25], v[178:185], v[62:65]
	v_mfma_f32_16x16x128_f8f6f4 v[58:61], v[26:33], v[178:185], v[58:61]
	v_mfma_f32_16x16x128_f8f6f4 v[46:49], v[18:25], v[186:193], v[46:49]
	v_mfma_f32_16x16x128_f8f6f4 v[42:45], v[26:33], v[186:193], v[42:45]
	s_setprio 0
	s_setprio 1
	v_mfma_f32_16x16x128_f8f6f4 v[86:89], v[2:9], v[162:169], v[86:89]
	v_mfma_f32_16x16x128_f8f6f4 v[82:85], v[10:17], v[162:169], v[82:85]
	v_mfma_f32_16x16x128_f8f6f4 v[70:73], v[2:9], v[170:177], v[70:73]
	v_mfma_f32_16x16x128_f8f6f4 v[66:69], v[10:17], v[170:177], v[66:69]
	v_mfma_f32_16x16x128_f8f6f4 v[54:57], v[2:9], v[178:185], v[54:57]
	v_mfma_f32_16x16x128_f8f6f4 v[50:53], v[10:17], v[178:185], v[50:53]
	v_mfma_f32_16x16x128_f8f6f4 v[38:41], v[2:9], v[186:193], v[38:41]
	v_mfma_f32_16x16x128_f8f6f4 v[34:37], v[10:17], v[186:193], v[34:37]
	s_setprio 0
	s_barrier
	ds_read_b128 v[2:5], v239
	ds_read_b128 v[6:9], v240
	ds_read_b128 v[10:13], v247
	ds_read_b128 v[14:17], v248
	ds_read_b128 v[18:21], v241
	ds_read_b128 v[22:25], v242
	ds_read_b128 v[26:29], v249
	ds_read_b128 v[30:33], v250
	ds_read_b128 v[162:165], v251 offset:32768
	ds_read_b128 v[166:169], v251 offset:33792
	ds_read_b128 v[170:173], v251 offset:34816
	ds_read_b128 v[174:177], v251 offset:35840
	ds_read_b128 v[178:181], v251 offset:36864
	ds_read_b128 v[182:185], v251 offset:37888
	ds_read_b128 v[186:189], v251 offset:38912
	ds_read_b128 v[190:193], v251 offset:39936
	s_add_i32 s65, s65, s23
	s_mov_b32 m0, s78
	s_add_u32 s98, s8, s65
	s_addc_u32 s99, s9, 0
	global_load_lds_dwordx4 v1, s[98:99]
	s_add_i32 s65, s65, s23
	s_add_u32 s100, s8, s65
	s_addc_u32 s101, s9, 0
	s_mov_b32 m0, s44
	s_nop 0
	global_load_lds_dwordx4 v1, s[100:101]
	s_waitcnt vmcnt(8)
	s_waitcnt lgkmcnt(0)
	s_barrier
	s_setprio 1
	s_waitcnt lgkmcnt(0)
	v_mfma_f32_16x16x128_f8f6f4 v[158:161], v[2:9], v[162:169], v[158:161]
	v_mfma_f32_16x16x128_f8f6f4 v[154:157], v[10:17], v[162:169], v[154:157]
	v_mfma_f32_16x16x128_f8f6f4 v[142:145], v[2:9], v[170:177], v[142:145]
	v_mfma_f32_16x16x128_f8f6f4 v[138:141], v[10:17], v[170:177], v[138:141]
	v_mfma_f32_16x16x128_f8f6f4 v[126:129], v[2:9], v[178:185], v[126:129]
	v_mfma_f32_16x16x128_f8f6f4 v[122:125], v[10:17], v[178:185], v[122:125]
	v_mfma_f32_16x16x128_f8f6f4 v[110:113], v[2:9], v[186:193], v[110:113]
	v_mfma_f32_16x16x128_f8f6f4 v[106:109], v[10:17], v[186:193], v[106:109]
	s_setprio 0
	s_setprio 1
	v_mfma_f32_16x16x128_f8f6f4 v[150:153], v[18:25], v[162:169], v[150:153]
	v_mfma_f32_16x16x128_f8f6f4 v[146:149], v[26:33], v[162:169], v[146:149]
	v_mfma_f32_16x16x128_f8f6f4 v[134:137], v[18:25], v[170:177], v[134:137]
	v_mfma_f32_16x16x128_f8f6f4 v[130:133], v[26:33], v[170:177], v[130:133]
	v_mfma_f32_16x16x128_f8f6f4 v[118:121], v[18:25], v[178:185], v[118:121]
	v_mfma_f32_16x16x128_f8f6f4 v[114:117], v[26:33], v[178:185], v[114:117]
	v_mfma_f32_16x16x128_f8f6f4 v[102:105], v[18:25], v[186:193], v[102:105]
	v_mfma_f32_16x16x128_f8f6f4 v[98:101], v[26:33], v[186:193], v[98:101]
	s_setprio 0
	s_barrier
	ds_read_b128 v[162:165], v251 offset:49152
	ds_read_b128 v[166:169], v251 offset:50176
	ds_read_b128 v[170:173], v251 offset:51200
	ds_read_b128 v[174:177], v251 offset:52224
	ds_read_b128 v[178:181], v251 offset:53248
	ds_read_b128 v[182:185], v251 offset:54272
	ds_read_b128 v[186:189], v251 offset:55296
	ds_read_b128 v[190:193], v251 offset:56320
	s_addk_i32 s64, 0x80
	s_mov_b32 m0, s79
	s_add_u32 s98, s20, s64
	s_addc_u32 s99, s21, 0
	global_load_lds_dwordx4 v211, s[98:99]
	s_add_i32 s64, s64, s35
	s_add_u32 s100, s20, s64
	s_addc_u32 s101, s21, 0
	s_mov_b32 m0, s80
	s_add_i32 s64, s64, s35
	global_load_lds_dwordx4 v211, s[100:101]
	s_mov_b32 m0, s83
	s_add_u32 s98, s20, s64
	s_addc_u32 s99, s21, 0
	global_load_lds_dwordx4 v211, s[98:99]
	s_add_i32 s64, s64, s35
	s_add_u32 s100, s20, s64
	s_addc_u32 s101, s21, 0
	s_mov_b32 m0, s84
	s_nop 0
	global_load_lds_dwordx4 v211, s[100:101]
	s_mov_b32 m0, s81
	s_add_u32 s98, s8, s63
	s_addc_u32 s99, s9, 0
	global_load_lds_dwordx4 v1, s[98:99]
	s_add_i32 s63, s63, s23
	s_add_u32 s100, s8, s63
	s_addc_u32 s101, s9, 0
	s_mov_b32 m0, s82
	s_nop 0
	global_load_lds_dwordx4 v1, s[100:101]
	s_waitcnt vmcnt(8)
	s_waitcnt lgkmcnt(0)
	s_barrier
	s_setprio 1
	s_waitcnt lgkmcnt(0)
	v_mfma_f32_16x16x128_f8f6f4 v[94:97], v[2:9], v[162:169], v[94:97]
	v_mfma_f32_16x16x128_f8f6f4 v[90:93], v[10:17], v[162:169], v[90:93]
	v_mfma_f32_16x16x128_f8f6f4 v[78:81], v[2:9], v[170:177], v[78:81]
	v_mfma_f32_16x16x128_f8f6f4 v[74:77], v[10:17], v[170:177], v[74:77]
	v_mfma_f32_16x16x128_f8f6f4 v[62:65], v[2:9], v[178:185], v[62:65]
	v_mfma_f32_16x16x128_f8f6f4 v[58:61], v[10:17], v[178:185], v[58:61]
	v_mfma_f32_16x16x128_f8f6f4 v[46:49], v[2:9], v[186:193], v[46:49]
	v_mfma_f32_16x16x128_f8f6f4 v[42:45], v[10:17], v[186:193], v[42:45]
	s_setprio 0
	s_setprio 1
	v_mfma_f32_16x16x128_f8f6f4 v[86:89], v[18:25], v[162:169], v[86:89]
	v_mfma_f32_16x16x128_f8f6f4 v[82:85], v[26:33], v[162:169], v[82:85]
	v_mfma_f32_16x16x128_f8f6f4 v[70:73], v[18:25], v[170:177], v[70:73]
	v_mfma_f32_16x16x128_f8f6f4 v[66:69], v[26:33], v[170:177], v[66:69]
	v_mfma_f32_16x16x128_f8f6f4 v[54:57], v[18:25], v[178:185], v[54:57]
	v_mfma_f32_16x16x128_f8f6f4 v[50:53], v[26:33], v[178:185], v[50:53]
	v_mfma_f32_16x16x128_f8f6f4 v[38:41], v[18:25], v[186:193], v[38:41]
	v_mfma_f32_16x16x128_f8f6f4 v[34:37], v[26:33], v[186:193], v[34:37]
	s_setprio 0
	s_barrier
	s_add_i32 s62, s62, 2
	s_addk_i32 s6, 0x100
	s_addk_i32 s61, 0x100
	s_cmp_ge_i32 s62, s85
	s_cbranch_scc0 .LBB0_1603

.LBB0_2047:
	ds_read_b128 v[138:141], v156
	ds_read_b128 v[142:145], v157
	ds_read_b128 v[168:171], v152
	ds_read_b128 v[172:175], v153
	ds_read_b128 v[176:179], v158
	ds_read_b128 v[180:183], v159
	ds_read_b128 v[184:187], v160
	ds_read_b128 v[188:191], v161
	s_add_i32 s49, s48, 2
	s_add_i32 s50, s73, s46
	s_cmp_eq_u32 s71, s48
	s_cselect_b32 s48, s47, s50
	s_cselect_b32 s51, s31, s30
	s_add_u32 s98, s6, s46
	s_addc_u32 s99, s7, 0
	s_add_i32 m0, s52, 0xc000
	ds_read_b128 v[192:195], v131
	ds_read_b128 v[196:199], v131 offset:1024
	ds_read_b128 v[200:203], v131 offset:2048
	ds_read_b128 v[204:207], v131 offset:3072
	ds_read_b128 v[214:217], v131 offset:4096
	ds_read_b128 v[218:221], v131 offset:5120
	ds_read_b128 v[222:225], v131 offset:6144
	ds_read_b128 v[226:229], v131 offset:7168
	global_load_lds_dwordx4 v132, s[98:99]
	s_add_u32 s100, s6, s46
	s_addc_u32 s101, s7, 0
	s_add_i32 m0, s52, 0xe000
	s_nop 0
	global_load_lds_dwordx4 v130, s[100:101]
	s_waitcnt vmcnt(8)
	s_waitcnt lgkmcnt(0)
	s_barrier
	s_setprio 1
	s_waitcnt lgkmcnt(0)
	v_mfma_f32_16x16x32_bf16 v[122:125], v[168:171], v[192:195], v[122:125]
	v_mfma_f32_16x16x32_bf16 v[126:129], v[142:145], v[192:195], v[126:129]
	v_mfma_f32_16x16x32_bf16 v[110:113], v[168:171], v[200:203], v[110:113]
	v_mfma_f32_16x16x32_bf16 v[106:109], v[142:145], v[200:203], v[106:109]
	v_mfma_f32_16x16x32_bf16 v[94:97], v[168:171], v[214:217], v[94:97]
	v_mfma_f32_16x16x32_bf16 v[90:93], v[142:145], v[214:217], v[90:93]
	v_mfma_f32_16x16x32_bf16 v[78:81], v[168:171], v[222:225], v[78:81]
	v_mfma_f32_16x16x32_bf16 v[74:77], v[142:145], v[222:225], v[74:77]
	v_mfma_f32_16x16x32_bf16 v[122:125], v[138:141], v[196:199], v[122:125]
	v_mfma_f32_16x16x32_bf16 v[126:129], v[176:179], v[196:199], v[126:129]
	v_mfma_f32_16x16x32_bf16 v[110:113], v[138:141], v[204:207], v[110:113]
	v_mfma_f32_16x16x32_bf16 v[106:109], v[176:179], v[204:207], v[106:109]
	v_mfma_f32_16x16x32_bf16 v[94:97], v[138:141], v[218:221], v[94:97]
	v_mfma_f32_16x16x32_bf16 v[90:93], v[176:179], v[218:221], v[90:93]
	v_mfma_f32_16x16x32_bf16 v[78:81], v[138:141], v[226:229], v[78:81]
	v_mfma_f32_16x16x32_bf16 v[74:77], v[176:179], v[226:229], v[74:77]
	s_setprio 0
	s_setprio 1
	v_mfma_f32_16x16x32_bf16 v[118:121], v[172:175], v[192:195], v[118:121]
	v_mfma_f32_16x16x32_bf16 v[114:117], v[184:187], v[192:195], v[114:117]
	v_mfma_f32_16x16x32_bf16 v[102:105], v[172:175], v[200:203], v[102:105]
	v_mfma_f32_16x16x32_bf16 v[98:101], v[184:187], v[200:203], v[98:101]
	v_mfma_f32_16x16x32_bf16 v[86:89], v[172:175], v[214:217], v[86:89]
	v_mfma_f32_16x16x32_bf16 v[82:85], v[184:187], v[214:217], v[82:85]
	v_mfma_f32_16x16x32_bf16 v[70:73], v[172:175], v[222:225], v[70:73]
	v_mfma_f32_16x16x32_bf16 v[66:69], v[184:187], v[222:225], v[66:69]
	v_mfma_f32_16x16x32_bf16 v[118:121], v[180:183], v[196:199], v[118:121]
	v_mfma_f32_16x16x32_bf16 v[114:117], v[188:191], v[196:199], v[114:117]
	v_mfma_f32_16x16x32_bf16 v[102:105], v[180:183], v[204:207], v[102:105]
	v_mfma_f32_16x16x32_bf16 v[98:101], v[188:191], v[204:207], v[98:101]
	v_mfma_f32_16x16x32_bf16 v[86:89], v[180:183], v[218:221], v[86:89]
	v_mfma_f32_16x16x32_bf16 v[82:85], v[188:191], v[218:221], v[82:85]
	v_mfma_f32_16x16x32_bf16 v[70:73], v[180:183], v[226:229], v[70:73]
	v_mfma_f32_16x16x32_bf16 v[66:69], v[188:191], v[226:229], v[66:69]
	s_setprio 0
	s_barrier
	s_mov_b32 m0, s53
	s_add_u32 s98, s8, s51
	s_addc_u32 s99, s9, 0
	ds_read_b128 v[192:195], v131 offset:16384
	ds_read_b128 v[196:199], v131 offset:17408
	ds_read_b128 v[200:203], v131 offset:18432
	ds_read_b128 v[204:207], v131 offset:19456
	ds_read_b128 v[214:217], v131 offset:20480
	ds_read_b128 v[218:221], v131 offset:21504
	ds_read_b128 v[222:225], v131 offset:22528
	ds_read_b128 v[226:229], v131 offset:23552
	global_load_lds_dwordx4 v146, s[98:99]
	s_add_u32 s100, s98, s45
	s_addc_u32 s101, s99, 0
	s_mov_b32 m0, s54
	s_nop 0
	global_load_lds_dwordx4 v146, s[100:101]
	s_add_u32 s98, s8, s51
	s_addc_u32 s99, s9, 0
	s_mov_b32 m0, s55
	s_nop 0
	global_load_lds_dwordx4 v147, s[98:99]
	s_add_u32 s100, s98, s45
	s_addc_u32 s101, s99, 0
	s_mov_b32 m0, s56
	s_nop 0
	global_load_lds_dwordx4 v147, s[100:101]
	s_add_u32 s98, s6, s48
	s_addc_u32 s99, s7, 0
	s_mov_b32 m0, s52
	s_nop 0
	global_load_lds_dwordx4 v1, s[98:99]
	s_add_u32 s100, s98, s44
	s_addc_u32 s101, s99, 0
	s_mov_b32 m0, s57
	s_nop 0
	global_load_lds_dwordx4 v1, s[100:101]
	s_waitcnt vmcnt(8)
	s_waitcnt lgkmcnt(0)
	s_barrier
	s_setprio 1
	s_waitcnt lgkmcnt(0)
	v_mfma_f32_16x16x32_bf16 v[62:65], v[168:171], v[192:195], v[62:65]
	v_mfma_f32_16x16x32_bf16 v[58:61], v[142:145], v[192:195], v[58:61]
	v_mfma_f32_16x16x32_bf16 v[46:49], v[168:171], v[200:203], v[46:49]
	v_mfma_f32_16x16x32_bf16 v[42:45], v[142:145], v[200:203], v[42:45]
	v_mfma_f32_16x16x32_bf16 v[30:33], v[168:171], v[214:217], v[30:33]
	v_mfma_f32_16x16x32_bf16 v[26:29], v[142:145], v[214:217], v[26:29]
	v_mfma_f32_16x16x32_bf16 v[14:17], v[168:171], v[222:225], v[14:17]
	v_mfma_f32_16x16x32_bf16 v[10:13], v[142:145], v[222:225], v[10:13]
	v_mfma_f32_16x16x32_bf16 v[62:65], v[138:141], v[196:199], v[62:65]
	v_mfma_f32_16x16x32_bf16 v[58:61], v[176:179], v[196:199], v[58:61]
	v_mfma_f32_16x16x32_bf16 v[46:49], v[138:141], v[204:207], v[46:49]
	v_mfma_f32_16x16x32_bf16 v[42:45], v[176:179], v[204:207], v[42:45]
	v_mfma_f32_16x16x32_bf16 v[30:33], v[138:141], v[218:221], v[30:33]
	v_mfma_f32_16x16x32_bf16 v[26:29], v[176:179], v[218:221], v[26:29]
	v_mfma_f32_16x16x32_bf16 v[14:17], v[138:141], v[226:229], v[14:17]
	v_mfma_f32_16x16x32_bf16 v[10:13], v[176:179], v[226:229], v[10:13]
	s_setprio 0
	s_setprio 1
	v_mfma_f32_16x16x32_bf16 v[54:57], v[172:175], v[192:195], v[54:57]
	v_mfma_f32_16x16x32_bf16 v[50:53], v[184:187], v[192:195], v[50:53]
	v_mfma_f32_16x16x32_bf16 v[38:41], v[172:175], v[200:203], v[38:41]
	v_mfma_f32_16x16x32_bf16 v[34:37], v[184:187], v[200:203], v[34:37]
	v_mfma_f32_16x16x32_bf16 v[22:25], v[172:175], v[214:217], v[22:25]
	v_mfma_f32_16x16x32_bf16 v[18:21], v[184:187], v[214:217], v[18:21]
	v_mfma_f32_16x16x32_bf16 v[6:9], v[172:175], v[222:225], v[6:9]
	v_mfma_f32_16x16x32_bf16 v[2:5], v[184:187], v[222:225], v[2:5]
	v_mfma_f32_16x16x32_bf16 v[54:57], v[180:183], v[196:199], v[54:57]
	v_mfma_f32_16x16x32_bf16 v[50:53], v[188:191], v[196:199], v[50:53]
	v_mfma_f32_16x16x32_bf16 v[38:41], v[180:183], v[204:207], v[38:41]
	v_mfma_f32_16x16x32_bf16 v[34:37], v[188:191], v[204:207], v[34:37]
	v_mfma_f32_16x16x32_bf16 v[22:25], v[180:183], v[218:221], v[22:25]
	v_mfma_f32_16x16x32_bf16 v[18:21], v[188:191], v[218:221], v[18:21]
	v_mfma_f32_16x16x32_bf16 v[6:9], v[180:183], v[226:229], v[6:9]
	v_mfma_f32_16x16x32_bf16 v[2:5], v[188:191], v[226:229], v[2:5]
	s_setprio 0
	s_barrier
	ds_read_b128 v[138:141], v162
	ds_read_b128 v[142:145], v163
	ds_read_b128 v[168:171], v154
	ds_read_b128 v[172:175], v155
	ds_read_b128 v[176:179], v164
	ds_read_b128 v[180:183], v165
	ds_read_b128 v[184:187], v166
	ds_read_b128 v[188:191], v167
	s_mov_b32 m0, s58
	s_add_u32 s98, s6, s48
	s_addc_u32 s99, s7, 0
	ds_read_b128 v[192:195], v131 offset:32768
	ds_read_b128 v[196:199], v131 offset:33792
	ds_read_b128 v[200:203], v131 offset:34816
	ds_read_b128 v[204:207], v131 offset:35840
	ds_read_b128 v[214:217], v131 offset:36864
	ds_read_b128 v[218:221], v131 offset:37888
	ds_read_b128 v[222:225], v131 offset:38912
	ds_read_b128 v[226:229], v131 offset:39936
	global_load_lds_dwordx4 v148, s[98:99]
	s_add_u32 s100, s98, s44
	s_addc_u32 s101, s99, 0
	s_mov_b32 m0, s59
	s_nop 0
	global_load_lds_dwordx4 v148, s[100:101]
	s_waitcnt vmcnt(8)
	s_waitcnt lgkmcnt(0)
	s_barrier
	s_setprio 1
	s_waitcnt lgkmcnt(0)
	v_mfma_f32_16x16x32_bf16 v[122:125], v[168:171], v[192:195], v[122:125]
	v_mfma_f32_16x16x32_bf16 v[126:129], v[142:145], v[192:195], v[126:129]
	v_mfma_f32_16x16x32_bf16 v[110:113], v[168:171], v[200:203], v[110:113]
	v_mfma_f32_16x16x32_bf16 v[106:109], v[142:145], v[200:203], v[106:109]
	v_mfma_f32_16x16x32_bf16 v[94:97], v[168:171], v[214:217], v[94:97]
	v_mfma_f32_16x16x32_bf16 v[90:93], v[142:145], v[214:217], v[90:93]
	v_mfma_f32_16x16x32_bf16 v[78:81], v[168:171], v[222:225], v[78:81]
	v_mfma_f32_16x16x32_bf16 v[74:77], v[142:145], v[222:225], v[74:77]
	v_mfma_f32_16x16x32_bf16 v[122:125], v[138:141], v[196:199], v[122:125]
	v_mfma_f32_16x16x32_bf16 v[126:129], v[176:179], v[196:199], v[126:129]
	v_mfma_f32_16x16x32_bf16 v[110:113], v[138:141], v[204:207], v[110:113]
	v_mfma_f32_16x16x32_bf16 v[106:109], v[176:179], v[204:207], v[106:109]
	v_mfma_f32_16x16x32_bf16 v[94:97], v[138:141], v[218:221], v[94:97]
	v_mfma_f32_16x16x32_bf16 v[90:93], v[176:179], v[218:221], v[90:93]
	v_mfma_f32_16x16x32_bf16 v[78:81], v[138:141], v[226:229], v[78:81]
	v_mfma_f32_16x16x32_bf16 v[74:77], v[176:179], v[226:229], v[74:77]
	s_setprio 0
	s_setprio 1
	v_mfma_f32_16x16x32_bf16 v[118:121], v[172:175], v[192:195], v[118:121]
	v_mfma_f32_16x16x32_bf16 v[114:117], v[184:187], v[192:195], v[114:117]
	v_mfma_f32_16x16x32_bf16 v[102:105], v[172:175], v[200:203], v[102:105]
	v_mfma_f32_16x16x32_bf16 v[98:101], v[184:187], v[200:203], v[98:101]
	v_mfma_f32_16x16x32_bf16 v[86:89], v[172:175], v[214:217], v[86:89]
	v_mfma_f32_16x16x32_bf16 v[82:85], v[184:187], v[214:217], v[82:85]
	v_mfma_f32_16x16x32_bf16 v[70:73], v[172:175], v[222:225], v[70:73]
	v_mfma_f32_16x16x32_bf16 v[66:69], v[184:187], v[222:225], v[66:69]
	v_mfma_f32_16x16x32_bf16 v[118:121], v[180:183], v[196:199], v[118:121]
	v_mfma_f32_16x16x32_bf16 v[114:117], v[188:191], v[196:199], v[114:117]
	v_mfma_f32_16x16x32_bf16 v[102:105], v[180:183], v[204:207], v[102:105]
	v_mfma_f32_16x16x32_bf16 v[98:101], v[188:191], v[204:207], v[98:101]
	v_mfma_f32_16x16x32_bf16 v[86:89], v[180:183], v[218:221], v[86:89]
	v_mfma_f32_16x16x32_bf16 v[82:85], v[188:191], v[218:221], v[82:85]
	v_mfma_f32_16x16x32_bf16 v[70:73], v[180:183], v[226:229], v[70:73]
	v_mfma_f32_16x16x32_bf16 v[66:69], v[188:191], v[226:229], v[66:69]
	s_setprio 0
	s_barrier
	s_addk_i32 s51, 0x80
	s_mov_b32 m0, s61
	s_add_u32 s98, s8, s51
	s_addc_u32 s99, s9, 0
	ds_read_b128 v[192:195], v131 offset:49152
	ds_read_b128 v[196:199], v131 offset:50176
	ds_read_b128 v[200:203], v131 offset:51200
	ds_read_b128 v[204:207], v131 offset:52224
	ds_read_b128 v[214:217], v131 offset:53248
	ds_read_b128 v[218:221], v131 offset:54272
	ds_read_b128 v[222:225], v131 offset:55296
	ds_read_b128 v[226:229], v131 offset:56320
	global_load_lds_dwordx4 v146, s[98:99]
	s_add_u32 s100, s98, s45
	s_addc_u32 s101, s99, 0
	s_mov_b32 m0, s62
	s_nop 0
	global_load_lds_dwordx4 v146, s[100:101]
	s_add_u32 s98, s8, s51
	s_addc_u32 s99, s9, 0
	s_mov_b32 m0, s65
	s_nop 0
	global_load_lds_dwordx4 v147, s[98:99]
	s_add_u32 s100, s98, s45
	s_addc_u32 s101, s99, 0
	s_mov_b32 m0, s66
	s_nop 0
	global_load_lds_dwordx4 v147, s[100:101]
	s_add_u32 s98, s6, s48
	s_addc_u32 s99, s7, 0
	s_mov_b32 m0, s63
	s_nop 0
	global_load_lds_dwordx4 v149, s[98:99]
	s_add_u32 s100, s98, s44
	s_addc_u32 s101, s99, 0
	s_mov_b32 m0, s64
	s_nop 0
	global_load_lds_dwordx4 v149, s[100:101]
	s_waitcnt vmcnt(8)
	s_waitcnt lgkmcnt(0)
	s_barrier
	s_setprio 1
	s_waitcnt lgkmcnt(0)
	v_mfma_f32_16x16x32_bf16 v[62:65], v[168:171], v[192:195], v[62:65]
	v_mfma_f32_16x16x32_bf16 v[58:61], v[142:145], v[192:195], v[58:61]
	v_mfma_f32_16x16x32_bf16 v[46:49], v[168:171], v[200:203], v[46:49]
	v_mfma_f32_16x16x32_bf16 v[42:45], v[142:145], v[200:203], v[42:45]
	v_mfma_f32_16x16x32_bf16 v[30:33], v[168:171], v[214:217], v[30:33]
	v_mfma_f32_16x16x32_bf16 v[26:29], v[142:145], v[214:217], v[26:29]
	v_mfma_f32_16x16x32_bf16 v[14:17], v[168:171], v[222:225], v[14:17]
	v_mfma_f32_16x16x32_bf16 v[10:13], v[142:145], v[222:225], v[10:13]
	v_mfma_f32_16x16x32_bf16 v[62:65], v[138:141], v[196:199], v[62:65]
	v_mfma_f32_16x16x32_bf16 v[58:61], v[176:179], v[196:199], v[58:61]
	v_mfma_f32_16x16x32_bf16 v[46:49], v[138:141], v[204:207], v[46:49]
	v_mfma_f32_16x16x32_bf16 v[42:45], v[176:179], v[204:207], v[42:45]
	v_mfma_f32_16x16x32_bf16 v[30:33], v[138:141], v[218:221], v[30:33]
	v_mfma_f32_16x16x32_bf16 v[26:29], v[176:179], v[218:221], v[26:29]
	v_mfma_f32_16x16x32_bf16 v[14:17], v[138:141], v[226:229], v[14:17]
	v_mfma_f32_16x16x32_bf16 v[10:13], v[176:179], v[226:229], v[10:13]
	s_setprio 0
	s_setprio 1
	v_mfma_f32_16x16x32_bf16 v[54:57], v[172:175], v[192:195], v[54:57]
	v_mfma_f32_16x16x32_bf16 v[50:53], v[184:187], v[192:195], v[50:53]
	v_mfma_f32_16x16x32_bf16 v[38:41], v[172:175], v[200:203], v[38:41]
	v_mfma_f32_16x16x32_bf16 v[34:37], v[184:187], v[200:203], v[34:37]
	v_mfma_f32_16x16x32_bf16 v[22:25], v[172:175], v[214:217], v[22:25]
	v_mfma_f32_16x16x32_bf16 v[18:21], v[184:187], v[214:217], v[18:21]
	v_mfma_f32_16x16x32_bf16 v[6:9], v[172:175], v[222:225], v[6:9]
	v_mfma_f32_16x16x32_bf16 v[2:5], v[184:187], v[222:225], v[2:5]
	v_mfma_f32_16x16x32_bf16 v[54:57], v[180:183], v[196:199], v[54:57]
	v_mfma_f32_16x16x32_bf16 v[50:53], v[188:191], v[196:199], v[50:53]
	v_mfma_f32_16x16x32_bf16 v[38:41], v[180:183], v[204:207], v[38:41]
	v_mfma_f32_16x16x32_bf16 v[34:37], v[188:191], v[204:207], v[34:37]
	v_mfma_f32_16x16x32_bf16 v[22:25], v[180:183], v[218:221], v[22:25]
	v_mfma_f32_16x16x32_bf16 v[18:21], v[188:191], v[218:221], v[18:21]
	v_mfma_f32_16x16x32_bf16 v[6:9], v[180:183], v[226:229], v[6:9]
	v_mfma_f32_16x16x32_bf16 v[2:5], v[188:191], v[226:229], v[2:5]
	s_setprio 0
	s_barrier
	s_addk_i32 s30, 0x100
	s_cmp_ge_i32 s49, s67
	s_mov_b32 s46, s50
	s_mov_b32 s48, s49
	s_cbranch_scc0 .LBB0_2047

.LBB0_2337:
	ds_read_b128 v[130:133], v194
	ds_read_b128 v[134:137], v195
	ds_read_b128 v[138:141], v190
	ds_read_b128 v[142:145], v191
	ds_read_b128 v[146:149], v196
	ds_read_b128 v[150:153], v197
	ds_read_b128 v[154:157], v198
	ds_read_b128 v[158:161], v199
	s_add_i32 s75, s50, 0x80
	s_cmp_eq_u32 s70, s88
	s_cselect_b32 s89, s51, s87
	s_cselect_b32 s75, s49, s75
	s_add_u32 s98, s4, s50
	s_addc_u32 s99, s5, 0
	s_add_i32 m0, s53, 0xc000
	ds_read_b128 v[162:165], v208
	ds_read_b128 v[166:169], v208 offset:1024
	ds_read_b128 v[170:173], v208 offset:2048
	ds_read_b128 v[180:183], v208 offset:3072
	ds_read_b128 v[214:217], v208 offset:4096
	ds_read_b128 v[218:221], v208 offset:5120
	ds_read_b128 v[222:225], v208 offset:6144
	ds_read_b128 v[226:229], v208 offset:7168
	global_load_lds_dwordx4 v207, s[98:99]
	s_add_u32 s100, s4, s50
	s_addc_u32 s101, s5, 0
	s_add_i32 m0, s53, 0xe000
	s_nop 0
	global_load_lds_dwordx4 v206, s[100:101]
	s_waitcnt vmcnt(8)
	s_waitcnt lgkmcnt(0)
	s_barrier
	s_setprio 1
	s_waitcnt lgkmcnt(0)
	v_mfma_f32_16x16x32_bf16 v[126:129], v[138:141], v[162:165], v[126:129]
	v_mfma_f32_16x16x32_bf16 v[122:125], v[134:137], v[162:165], v[122:125]
	v_mfma_f32_16x16x32_bf16 v[110:113], v[138:141], v[170:173], v[110:113]
	v_mfma_f32_16x16x32_bf16 v[106:109], v[134:137], v[170:173], v[106:109]
	v_mfma_f32_16x16x32_bf16 v[94:97], v[138:141], v[214:217], v[94:97]
	v_mfma_f32_16x16x32_bf16 v[90:93], v[134:137], v[214:217], v[90:93]
	v_mfma_f32_16x16x32_bf16 v[78:81], v[138:141], v[222:225], v[78:81]
	v_mfma_f32_16x16x32_bf16 v[74:77], v[134:137], v[222:225], v[74:77]
	v_mfma_f32_16x16x32_bf16 v[126:129], v[130:133], v[166:169], v[126:129]
	v_mfma_f32_16x16x32_bf16 v[122:125], v[146:149], v[166:169], v[122:125]
	v_mfma_f32_16x16x32_bf16 v[110:113], v[130:133], v[180:183], v[110:113]
	v_mfma_f32_16x16x32_bf16 v[106:109], v[146:149], v[180:183], v[106:109]
	v_mfma_f32_16x16x32_bf16 v[94:97], v[130:133], v[218:221], v[94:97]
	v_mfma_f32_16x16x32_bf16 v[90:93], v[146:149], v[218:221], v[90:93]
	v_mfma_f32_16x16x32_bf16 v[78:81], v[130:133], v[226:229], v[78:81]
	v_mfma_f32_16x16x32_bf16 v[74:77], v[146:149], v[226:229], v[74:77]
	s_setprio 0
	s_setprio 1
	v_mfma_f32_16x16x32_bf16 v[118:121], v[142:145], v[162:165], v[118:121]
	v_mfma_f32_16x16x32_bf16 v[114:117], v[154:157], v[162:165], v[114:117]
	v_mfma_f32_16x16x32_bf16 v[102:105], v[142:145], v[170:173], v[102:105]
	v_mfma_f32_16x16x32_bf16 v[98:101], v[154:157], v[170:173], v[98:101]
	v_mfma_f32_16x16x32_bf16 v[86:89], v[142:145], v[214:217], v[86:89]
	v_mfma_f32_16x16x32_bf16 v[82:85], v[154:157], v[214:217], v[82:85]
	v_mfma_f32_16x16x32_bf16 v[70:73], v[142:145], v[222:225], v[70:73]
	v_mfma_f32_16x16x32_bf16 v[66:69], v[154:157], v[222:225], v[66:69]
	v_mfma_f32_16x16x32_bf16 v[118:121], v[150:153], v[166:169], v[118:121]
	v_mfma_f32_16x16x32_bf16 v[114:117], v[158:161], v[166:169], v[114:117]
	v_mfma_f32_16x16x32_bf16 v[102:105], v[150:153], v[180:183], v[102:105]
	v_mfma_f32_16x16x32_bf16 v[98:101], v[158:161], v[180:183], v[98:101]
	v_mfma_f32_16x16x32_bf16 v[86:89], v[150:153], v[218:221], v[86:89]
	v_mfma_f32_16x16x32_bf16 v[82:85], v[158:161], v[218:221], v[82:85]
	v_mfma_f32_16x16x32_bf16 v[70:73], v[150:153], v[226:229], v[70:73]
	v_mfma_f32_16x16x32_bf16 v[66:69], v[158:161], v[226:229], v[66:69]
	s_setprio 0
	s_barrier
	s_mov_b32 m0, s54
	s_add_u32 s98, s6, s89
	s_addc_u32 s99, s7, 0
	ds_read_b128 v[162:165], v208 offset:16384
	ds_read_b128 v[166:169], v208 offset:17408
	ds_read_b128 v[170:173], v208 offset:18432
	ds_read_b128 v[180:183], v208 offset:19456
	ds_read_b128 v[214:217], v208 offset:20480
	ds_read_b128 v[218:221], v208 offset:21504
	ds_read_b128 v[222:225], v208 offset:22528
	ds_read_b128 v[226:229], v208 offset:23552
	global_load_lds_dwordx4 v184, s[98:99]
	s_add_u32 s100, s98, s52
	s_addc_u32 s101, s99, 0
	s_mov_b32 m0, s55
	s_nop 0
	global_load_lds_dwordx4 v184, s[100:101]
	s_add_u32 s98, s6, s89
	s_addc_u32 s99, s7, 0
	s_mov_b32 m0, s56
	s_nop 0
	global_load_lds_dwordx4 v185, s[98:99]
	s_add_u32 s100, s98, s52
	s_addc_u32 s101, s99, 0
	s_mov_b32 m0, s57
	s_nop 0
	global_load_lds_dwordx4 v185, s[100:101]
	s_add_u32 s98, s4, s75
	s_addc_u32 s99, s5, 0
	s_mov_b32 m0, s53
	s_nop 0
	global_load_lds_dwordx4 v1, s[98:99]
	s_add_u32 s100, s98, s45
	s_addc_u32 s101, s99, 0
	s_mov_b32 m0, s58
	s_nop 0
	global_load_lds_dwordx4 v1, s[100:101]
	s_waitcnt vmcnt(8)
	s_waitcnt lgkmcnt(0)
	s_barrier
	s_setprio 1
	s_waitcnt lgkmcnt(0)
	v_mfma_f32_16x16x32_bf16 v[62:65], v[138:141], v[162:165], v[62:65]
	v_mfma_f32_16x16x32_bf16 v[58:61], v[134:137], v[162:165], v[58:61]
	v_mfma_f32_16x16x32_bf16 v[46:49], v[138:141], v[170:173], v[46:49]
	v_mfma_f32_16x16x32_bf16 v[42:45], v[134:137], v[170:173], v[42:45]
	v_mfma_f32_16x16x32_bf16 v[30:33], v[138:141], v[214:217], v[30:33]
	v_mfma_f32_16x16x32_bf16 v[26:29], v[134:137], v[214:217], v[26:29]
	v_mfma_f32_16x16x32_bf16 v[14:17], v[138:141], v[222:225], v[14:17]
	v_mfma_f32_16x16x32_bf16 v[10:13], v[134:137], v[222:225], v[10:13]
	v_mfma_f32_16x16x32_bf16 v[62:65], v[130:133], v[166:169], v[62:65]
	v_mfma_f32_16x16x32_bf16 v[58:61], v[146:149], v[166:169], v[58:61]
	v_mfma_f32_16x16x32_bf16 v[46:49], v[130:133], v[180:183], v[46:49]
	v_mfma_f32_16x16x32_bf16 v[42:45], v[146:149], v[180:183], v[42:45]
	v_mfma_f32_16x16x32_bf16 v[30:33], v[130:133], v[218:221], v[30:33]
	v_mfma_f32_16x16x32_bf16 v[26:29], v[146:149], v[218:221], v[26:29]
	v_mfma_f32_16x16x32_bf16 v[14:17], v[130:133], v[226:229], v[14:17]
	v_mfma_f32_16x16x32_bf16 v[10:13], v[146:149], v[226:229], v[10:13]
	s_setprio 0
	s_setprio 1
	v_mfma_f32_16x16x32_bf16 v[54:57], v[142:145], v[162:165], v[54:57]
	v_mfma_f32_16x16x32_bf16 v[50:53], v[154:157], v[162:165], v[50:53]
	v_mfma_f32_16x16x32_bf16 v[38:41], v[142:145], v[170:173], v[38:41]
	v_mfma_f32_16x16x32_bf16 v[34:37], v[154:157], v[170:173], v[34:37]
	v_mfma_f32_16x16x32_bf16 v[22:25], v[142:145], v[214:217], v[22:25]
	v_mfma_f32_16x16x32_bf16 v[18:21], v[154:157], v[214:217], v[18:21]
	v_mfma_f32_16x16x32_bf16 v[6:9], v[142:145], v[222:225], v[6:9]
	v_mfma_f32_16x16x32_bf16 v[2:5], v[154:157], v[222:225], v[2:5]
	v_mfma_f32_16x16x32_bf16 v[54:57], v[150:153], v[166:169], v[54:57]
	v_mfma_f32_16x16x32_bf16 v[50:53], v[158:161], v[166:169], v[50:53]
	v_mfma_f32_16x16x32_bf16 v[38:41], v[150:153], v[180:183], v[38:41]
	v_mfma_f32_16x16x32_bf16 v[34:37], v[158:161], v[180:183], v[34:37]
	v_mfma_f32_16x16x32_bf16 v[22:25], v[150:153], v[218:221], v[22:25]
	v_mfma_f32_16x16x32_bf16 v[18:21], v[158:161], v[218:221], v[18:21]
	v_mfma_f32_16x16x32_bf16 v[6:9], v[150:153], v[226:229], v[6:9]
	v_mfma_f32_16x16x32_bf16 v[2:5], v[158:161], v[226:229], v[2:5]
	s_setprio 0
	s_barrier
	ds_read_b128 v[130:133], v200
	ds_read_b128 v[134:137], v201
	ds_read_b128 v[138:141], v192
	ds_read_b128 v[142:145], v193
	ds_read_b128 v[146:149], v202
	ds_read_b128 v[150:153], v203
	ds_read_b128 v[154:157], v204
	ds_read_b128 v[158:161], v205
	s_mov_b32 m0, s59
	s_add_u32 s98, s4, s75
	s_addc_u32 s99, s5, 0
	ds_read_b128 v[162:165], v208 offset:32768
	ds_read_b128 v[166:169], v208 offset:33792
	ds_read_b128 v[170:173], v208 offset:34816
	ds_read_b128 v[180:183], v208 offset:35840
	ds_read_b128 v[214:217], v208 offset:36864
	ds_read_b128 v[218:221], v208 offset:37888
	ds_read_b128 v[222:225], v208 offset:38912
	ds_read_b128 v[226:229], v208 offset:39936
	global_load_lds_dwordx4 v186, s[98:99]
	s_add_u32 s100, s98, s45
	s_addc_u32 s101, s99, 0
	s_mov_b32 m0, s60
	s_nop 0
	global_load_lds_dwordx4 v186, s[100:101]
	s_waitcnt vmcnt(8)
	s_waitcnt lgkmcnt(0)
	s_barrier
	s_setprio 1
	s_waitcnt lgkmcnt(0)
	v_mfma_f32_16x16x32_bf16 v[126:129], v[138:141], v[162:165], v[126:129]
	v_mfma_f32_16x16x32_bf16 v[122:125], v[134:137], v[162:165], v[122:125]
	v_mfma_f32_16x16x32_bf16 v[110:113], v[138:141], v[170:173], v[110:113]
	v_mfma_f32_16x16x32_bf16 v[106:109], v[134:137], v[170:173], v[106:109]
	v_mfma_f32_16x16x32_bf16 v[94:97], v[138:141], v[214:217], v[94:97]
	v_mfma_f32_16x16x32_bf16 v[90:93], v[134:137], v[214:217], v[90:93]
	v_mfma_f32_16x16x32_bf16 v[78:81], v[138:141], v[222:225], v[78:81]
	v_mfma_f32_16x16x32_bf16 v[74:77], v[134:137], v[222:225], v[74:77]
	v_mfma_f32_16x16x32_bf16 v[126:129], v[130:133], v[166:169], v[126:129]
	v_mfma_f32_16x16x32_bf16 v[122:125], v[146:149], v[166:169], v[122:125]
	v_mfma_f32_16x16x32_bf16 v[110:113], v[130:133], v[180:183], v[110:113]
	v_mfma_f32_16x16x32_bf16 v[106:109], v[146:149], v[180:183], v[106:109]
	v_mfma_f32_16x16x32_bf16 v[94:97], v[130:133], v[218:221], v[94:97]
	v_mfma_f32_16x16x32_bf16 v[90:93], v[146:149], v[218:221], v[90:93]
	v_mfma_f32_16x16x32_bf16 v[78:81], v[130:133], v[226:229], v[78:81]
	v_mfma_f32_16x16x32_bf16 v[74:77], v[146:149], v[226:229], v[74:77]
	s_setprio 0
	s_setprio 1
	v_mfma_f32_16x16x32_bf16 v[118:121], v[142:145], v[162:165], v[118:121]
	v_mfma_f32_16x16x32_bf16 v[114:117], v[154:157], v[162:165], v[114:117]
	v_mfma_f32_16x16x32_bf16 v[102:105], v[142:145], v[170:173], v[102:105]
	v_mfma_f32_16x16x32_bf16 v[98:101], v[154:157], v[170:173], v[98:101]
	v_mfma_f32_16x16x32_bf16 v[86:89], v[142:145], v[214:217], v[86:89]
	v_mfma_f32_16x16x32_bf16 v[82:85], v[154:157], v[214:217], v[82:85]
	v_mfma_f32_16x16x32_bf16 v[70:73], v[142:145], v[222:225], v[70:73]
	v_mfma_f32_16x16x32_bf16 v[66:69], v[154:157], v[222:225], v[66:69]
	v_mfma_f32_16x16x32_bf16 v[118:121], v[150:153], v[166:169], v[118:121]
	v_mfma_f32_16x16x32_bf16 v[114:117], v[158:161], v[166:169], v[114:117]
	v_mfma_f32_16x16x32_bf16 v[102:105], v[150:153], v[180:183], v[102:105]
	v_mfma_f32_16x16x32_bf16 v[98:101], v[158:161], v[180:183], v[98:101]
	v_mfma_f32_16x16x32_bf16 v[86:89], v[150:153], v[218:221], v[86:89]
	v_mfma_f32_16x16x32_bf16 v[82:85], v[158:161], v[218:221], v[82:85]
	v_mfma_f32_16x16x32_bf16 v[70:73], v[150:153], v[226:229], v[70:73]
	v_mfma_f32_16x16x32_bf16 v[66:69], v[158:161], v[226:229], v[66:69]
	s_setprio 0
	s_barrier
	s_addk_i32 s89, 0x80
	s_mov_b32 m0, s63
	s_add_u32 s98, s6, s89
	s_addc_u32 s99, s7, 0
	ds_read_b128 v[162:165], v208 offset:49152
	ds_read_b128 v[166:169], v208 offset:50176
	ds_read_b128 v[170:173], v208 offset:51200
	ds_read_b128 v[180:183], v208 offset:52224
	ds_read_b128 v[214:217], v208 offset:53248
	ds_read_b128 v[218:221], v208 offset:54272
	ds_read_b128 v[222:225], v208 offset:55296
	ds_read_b128 v[226:229], v208 offset:56320
	global_load_lds_dwordx4 v184, s[98:99]
	s_add_u32 s100, s98, s52
	s_addc_u32 s101, s99, 0
	s_mov_b32 m0, s64
	s_nop 0
	global_load_lds_dwordx4 v184, s[100:101]
	s_add_u32 s98, s6, s89
	s_addc_u32 s99, s7, 0
	s_mov_b32 m0, s67
	s_nop 0
	global_load_lds_dwordx4 v185, s[98:99]
	s_add_u32 s100, s98, s52
	s_addc_u32 s101, s99, 0
	s_mov_b32 m0, s68
	s_nop 0
	global_load_lds_dwordx4 v185, s[100:101]
	s_add_u32 s98, s4, s75
	s_addc_u32 s99, s5, 0
	s_mov_b32 m0, s65
	s_nop 0
	global_load_lds_dwordx4 v189, s[98:99]
	s_add_u32 s100, s98, s45
	s_addc_u32 s101, s99, 0
	s_mov_b32 m0, s66
	s_nop 0
	global_load_lds_dwordx4 v189, s[100:101]
	s_waitcnt vmcnt(8)
	s_waitcnt lgkmcnt(0)
	s_barrier
	s_setprio 1
	s_waitcnt lgkmcnt(0)
	v_mfma_f32_16x16x32_bf16 v[62:65], v[138:141], v[162:165], v[62:65]
	v_mfma_f32_16x16x32_bf16 v[58:61], v[134:137], v[162:165], v[58:61]
	v_mfma_f32_16x16x32_bf16 v[46:49], v[138:141], v[170:173], v[46:49]
	v_mfma_f32_16x16x32_bf16 v[42:45], v[134:137], v[170:173], v[42:45]
	v_mfma_f32_16x16x32_bf16 v[30:33], v[138:141], v[214:217], v[30:33]
	v_mfma_f32_16x16x32_bf16 v[26:29], v[134:137], v[214:217], v[26:29]
	v_mfma_f32_16x16x32_bf16 v[14:17], v[138:141], v[222:225], v[14:17]
	v_mfma_f32_16x16x32_bf16 v[10:13], v[134:137], v[222:225], v[10:13]
	v_mfma_f32_16x16x32_bf16 v[62:65], v[130:133], v[166:169], v[62:65]
	v_mfma_f32_16x16x32_bf16 v[58:61], v[146:149], v[166:169], v[58:61]
	v_mfma_f32_16x16x32_bf16 v[46:49], v[130:133], v[180:183], v[46:49]
	v_mfma_f32_16x16x32_bf16 v[42:45], v[146:149], v[180:183], v[42:45]
	v_mfma_f32_16x16x32_bf16 v[30:33], v[130:133], v[218:221], v[30:33]
	v_mfma_f32_16x16x32_bf16 v[26:29], v[146:149], v[218:221], v[26:29]
	v_mfma_f32_16x16x32_bf16 v[14:17], v[130:133], v[226:229], v[14:17]
	v_mfma_f32_16x16x32_bf16 v[10:13], v[146:149], v[226:229], v[10:13]
	s_setprio 0
	s_setprio 1
	v_mfma_f32_16x16x32_bf16 v[54:57], v[142:145], v[162:165], v[54:57]
	v_mfma_f32_16x16x32_bf16 v[50:53], v[154:157], v[162:165], v[50:53]
	v_mfma_f32_16x16x32_bf16 v[38:41], v[142:145], v[170:173], v[38:41]
	v_mfma_f32_16x16x32_bf16 v[34:37], v[154:157], v[170:173], v[34:37]
	v_mfma_f32_16x16x32_bf16 v[22:25], v[142:145], v[214:217], v[22:25]
	v_mfma_f32_16x16x32_bf16 v[18:21], v[154:157], v[214:217], v[18:21]
	v_mfma_f32_16x16x32_bf16 v[6:9], v[142:145], v[222:225], v[6:9]
	v_mfma_f32_16x16x32_bf16 v[2:5], v[154:157], v[222:225], v[2:5]
	v_mfma_f32_16x16x32_bf16 v[54:57], v[150:153], v[166:169], v[54:57]
	v_mfma_f32_16x16x32_bf16 v[50:53], v[158:161], v[166:169], v[50:53]
	v_mfma_f32_16x16x32_bf16 v[38:41], v[150:153], v[180:183], v[38:41]
	v_mfma_f32_16x16x32_bf16 v[34:37], v[158:161], v[180:183], v[34:37]
	v_mfma_f32_16x16x32_bf16 v[22:25], v[150:153], v[218:221], v[22:25]
	v_mfma_f32_16x16x32_bf16 v[18:21], v[158:161], v[218:221], v[18:21]
	v_mfma_f32_16x16x32_bf16 v[6:9], v[150:153], v[226:229], v[6:9]
	v_mfma_f32_16x16x32_bf16 v[2:5], v[158:161], v[226:229], v[2:5]
	s_setprio 0
	s_barrier
	s_add_i32 s88, s88, 2
	s_addk_i32 s50, 0x100
	s_addk_i32 s87, 0x100
	s_cmp_ge_i32 s88, s61
	s_cbranch_scc0 .LBB0_2337

.LBB0_2597:
	ds_read_b128 v[130:133], v206
	ds_read_b128 v[134:137], v207
	ds_read_b128 v[138:141], v202
	ds_read_b128 v[142:145], v203
	ds_read_b128 v[146:149], v208
	ds_read_b128 v[150:153], v209
	ds_read_b128 v[154:157], v211
	ds_read_b128 v[158:161], v213
	s_add_i32 s65, s60, 0x80
	s_cmp_eq_u32 s84, s64
	s_cselect_b32 s75, s61, s63
	s_cselect_b32 s65, s5, s65
	s_add_u32 s98, s6, s60
	s_addc_u32 s99, s7, 0
	s_add_i32 m0, s45, 0xc000
	ds_read_b128 v[162:165], v222
	ds_read_b128 v[166:169], v222 offset:1024
	ds_read_b128 v[170:173], v222 offset:2048
	ds_read_b128 v[174:177], v222 offset:3072
	ds_read_b128 v[182:185], v222 offset:4096
	ds_read_b128 v[186:189], v222 offset:5120
	ds_read_b128 v[190:193], v222 offset:6144
	ds_read_b128 v[224:227], v222 offset:7168
	global_load_lds_dwordx4 v221, s[98:99]
	s_add_u32 s100, s6, s60
	s_addc_u32 s101, s7, 0
	s_add_i32 m0, s45, 0xe000
	s_nop 0
	global_load_lds_dwordx4 v220, s[100:101]
	s_waitcnt vmcnt(8)
	s_waitcnt lgkmcnt(0)
	s_barrier
	s_setprio 1
	s_waitcnt lgkmcnt(0)
	v_mfma_f32_16x16x32_bf16 v[126:129], v[138:141], v[162:165], v[126:129]
	v_mfma_f32_16x16x32_bf16 v[122:125], v[134:137], v[162:165], v[122:125]
	v_mfma_f32_16x16x32_bf16 v[110:113], v[138:141], v[170:173], v[110:113]
	v_mfma_f32_16x16x32_bf16 v[106:109], v[134:137], v[170:173], v[106:109]
	v_mfma_f32_16x16x32_bf16 v[94:97], v[138:141], v[182:185], v[94:97]
	v_mfma_f32_16x16x32_bf16 v[90:93], v[134:137], v[182:185], v[90:93]
	v_mfma_f32_16x16x32_bf16 v[78:81], v[138:141], v[190:193], v[78:81]
	v_mfma_f32_16x16x32_bf16 v[74:77], v[134:137], v[190:193], v[74:77]
	v_mfma_f32_16x16x32_bf16 v[126:129], v[130:133], v[166:169], v[126:129]
	v_mfma_f32_16x16x32_bf16 v[122:125], v[146:149], v[166:169], v[122:125]
	v_mfma_f32_16x16x32_bf16 v[110:113], v[130:133], v[174:177], v[110:113]
	v_mfma_f32_16x16x32_bf16 v[106:109], v[146:149], v[174:177], v[106:109]
	v_mfma_f32_16x16x32_bf16 v[94:97], v[130:133], v[186:189], v[94:97]
	v_mfma_f32_16x16x32_bf16 v[90:93], v[146:149], v[186:189], v[90:93]
	v_mfma_f32_16x16x32_bf16 v[78:81], v[130:133], v[224:227], v[78:81]
	v_mfma_f32_16x16x32_bf16 v[74:77], v[146:149], v[224:227], v[74:77]
	s_setprio 0
	s_setprio 1
	v_mfma_f32_16x16x32_bf16 v[118:121], v[142:145], v[162:165], v[118:121]
	v_mfma_f32_16x16x32_bf16 v[114:117], v[154:157], v[162:165], v[114:117]
	v_mfma_f32_16x16x32_bf16 v[102:105], v[142:145], v[170:173], v[102:105]
	v_mfma_f32_16x16x32_bf16 v[98:101], v[154:157], v[170:173], v[98:101]
	v_mfma_f32_16x16x32_bf16 v[86:89], v[142:145], v[182:185], v[86:89]
	v_mfma_f32_16x16x32_bf16 v[82:85], v[154:157], v[182:185], v[82:85]
	v_mfma_f32_16x16x32_bf16 v[70:73], v[142:145], v[190:193], v[70:73]
	v_mfma_f32_16x16x32_bf16 v[66:69], v[154:157], v[190:193], v[66:69]
	v_mfma_f32_16x16x32_bf16 v[118:121], v[150:153], v[166:169], v[118:121]
	v_mfma_f32_16x16x32_bf16 v[114:117], v[158:161], v[166:169], v[114:117]
	v_mfma_f32_16x16x32_bf16 v[102:105], v[150:153], v[174:177], v[102:105]
	v_mfma_f32_16x16x32_bf16 v[98:101], v[158:161], v[174:177], v[98:101]
	v_mfma_f32_16x16x32_bf16 v[86:89], v[150:153], v[186:189], v[86:89]
	v_mfma_f32_16x16x32_bf16 v[82:85], v[158:161], v[186:189], v[82:85]
	v_mfma_f32_16x16x32_bf16 v[70:73], v[150:153], v[224:227], v[70:73]
	v_mfma_f32_16x16x32_bf16 v[66:69], v[158:161], v[224:227], v[66:69]
	s_setprio 0
	s_barrier
	s_mov_b32 m0, s66
	s_add_u32 s98, s8, s75
	s_addc_u32 s99, s9, 0
	ds_read_b128 v[162:165], v222 offset:16384
	ds_read_b128 v[166:169], v222 offset:17408
	ds_read_b128 v[170:173], v222 offset:18432
	ds_read_b128 v[174:177], v222 offset:19456
	ds_read_b128 v[182:185], v222 offset:20480
	ds_read_b128 v[186:189], v222 offset:21504
	ds_read_b128 v[190:193], v222 offset:22528
	ds_read_b128 v[224:227], v222 offset:23552
	global_load_lds_dwordx4 v196, s[98:99]
	s_add_u32 s100, s98, s44
	s_addc_u32 s101, s99, 0
	s_mov_b32 m0, s67
	s_nop 0
	global_load_lds_dwordx4 v196, s[100:101]
	s_add_u32 s98, s8, s75
	s_addc_u32 s99, s9, 0
	s_mov_b32 m0, s68
	s_nop 0
	global_load_lds_dwordx4 v197, s[98:99]
	s_add_u32 s100, s98, s44
	s_addc_u32 s101, s99, 0
	s_mov_b32 m0, s69
	s_nop 0
	global_load_lds_dwordx4 v197, s[100:101]
	s_add_u32 s98, s6, s65
	s_addc_u32 s99, s7, 0
	s_mov_b32 m0, s45
	s_nop 0
	global_load_lds_dwordx4 v1, s[98:99]
	s_add_u32 s100, s98, s35
	s_addc_u32 s101, s99, 0
	s_mov_b32 m0, s70
	s_nop 0
	global_load_lds_dwordx4 v1, s[100:101]
	s_waitcnt vmcnt(8)
	s_waitcnt lgkmcnt(0)
	s_barrier
	s_setprio 1
	s_waitcnt lgkmcnt(0)
	v_mfma_f32_16x16x32_bf16 v[62:65], v[138:141], v[162:165], v[62:65]
	v_mfma_f32_16x16x32_bf16 v[58:61], v[134:137], v[162:165], v[58:61]
	v_mfma_f32_16x16x32_bf16 v[46:49], v[138:141], v[170:173], v[46:49]
	v_mfma_f32_16x16x32_bf16 v[42:45], v[134:137], v[170:173], v[42:45]
	v_mfma_f32_16x16x32_bf16 v[30:33], v[138:141], v[182:185], v[30:33]
	v_mfma_f32_16x16x32_bf16 v[26:29], v[134:137], v[182:185], v[26:29]
	v_mfma_f32_16x16x32_bf16 v[14:17], v[138:141], v[190:193], v[14:17]
	v_mfma_f32_16x16x32_bf16 v[10:13], v[134:137], v[190:193], v[10:13]
	v_mfma_f32_16x16x32_bf16 v[62:65], v[130:133], v[166:169], v[62:65]
	v_mfma_f32_16x16x32_bf16 v[58:61], v[146:149], v[166:169], v[58:61]
	v_mfma_f32_16x16x32_bf16 v[46:49], v[130:133], v[174:177], v[46:49]
	v_mfma_f32_16x16x32_bf16 v[42:45], v[146:149], v[174:177], v[42:45]
	v_mfma_f32_16x16x32_bf16 v[30:33], v[130:133], v[186:189], v[30:33]
	v_mfma_f32_16x16x32_bf16 v[26:29], v[146:149], v[186:189], v[26:29]
	v_mfma_f32_16x16x32_bf16 v[14:17], v[130:133], v[224:227], v[14:17]
	v_mfma_f32_16x16x32_bf16 v[10:13], v[146:149], v[224:227], v[10:13]
	s_setprio 0
	s_setprio 1
	v_mfma_f32_16x16x32_bf16 v[54:57], v[142:145], v[162:165], v[54:57]
	v_mfma_f32_16x16x32_bf16 v[50:53], v[154:157], v[162:165], v[50:53]
	v_mfma_f32_16x16x32_bf16 v[38:41], v[142:145], v[170:173], v[38:41]
	v_mfma_f32_16x16x32_bf16 v[34:37], v[154:157], v[170:173], v[34:37]
	v_mfma_f32_16x16x32_bf16 v[22:25], v[142:145], v[182:185], v[22:25]
	v_mfma_f32_16x16x32_bf16 v[18:21], v[154:157], v[182:185], v[18:21]
	v_mfma_f32_16x16x32_bf16 v[6:9], v[142:145], v[190:193], v[6:9]
	v_mfma_f32_16x16x32_bf16 v[2:5], v[154:157], v[190:193], v[2:5]
	v_mfma_f32_16x16x32_bf16 v[54:57], v[150:153], v[166:169], v[54:57]
	v_mfma_f32_16x16x32_bf16 v[50:53], v[158:161], v[166:169], v[50:53]
	v_mfma_f32_16x16x32_bf16 v[38:41], v[150:153], v[174:177], v[38:41]
	v_mfma_f32_16x16x32_bf16 v[34:37], v[158:161], v[174:177], v[34:37]
	v_mfma_f32_16x16x32_bf16 v[22:25], v[150:153], v[186:189], v[22:25]
	v_mfma_f32_16x16x32_bf16 v[18:21], v[158:161], v[186:189], v[18:21]
	v_mfma_f32_16x16x32_bf16 v[6:9], v[150:153], v[224:227], v[6:9]
	v_mfma_f32_16x16x32_bf16 v[2:5], v[158:161], v[224:227], v[2:5]
	s_setprio 0
	s_barrier
	ds_read_b128 v[130:133], v214
	ds_read_b128 v[134:137], v215
	ds_read_b128 v[138:141], v204
	ds_read_b128 v[142:145], v205
	ds_read_b128 v[146:149], v216
	ds_read_b128 v[150:153], v217
	ds_read_b128 v[154:157], v218
	ds_read_b128 v[158:161], v219
	s_mov_b32 m0, s71
	s_add_u32 s98, s6, s65
	s_addc_u32 s99, s7, 0
	ds_read_b128 v[162:165], v222 offset:32768
	ds_read_b128 v[166:169], v222 offset:33792
	ds_read_b128 v[170:173], v222 offset:34816
	ds_read_b128 v[174:177], v222 offset:35840
	ds_read_b128 v[182:185], v222 offset:36864
	ds_read_b128 v[186:189], v222 offset:37888
	ds_read_b128 v[190:193], v222 offset:38912
	ds_read_b128 v[224:227], v222 offset:39936
	global_load_lds_dwordx4 v198, s[98:99]
	s_add_u32 s100, s98, s35
	s_addc_u32 s101, s99, 0
	s_mov_b32 m0, s72
	s_nop 0
	global_load_lds_dwordx4 v198, s[100:101]
	s_waitcnt vmcnt(8)
	s_waitcnt lgkmcnt(0)
	s_barrier
	s_setprio 1
	s_waitcnt lgkmcnt(0)
	v_mfma_f32_16x16x32_bf16 v[126:129], v[138:141], v[162:165], v[126:129]
	v_mfma_f32_16x16x32_bf16 v[122:125], v[134:137], v[162:165], v[122:125]
	v_mfma_f32_16x16x32_bf16 v[110:113], v[138:141], v[170:173], v[110:113]
	v_mfma_f32_16x16x32_bf16 v[106:109], v[134:137], v[170:173], v[106:109]
	v_mfma_f32_16x16x32_bf16 v[94:97], v[138:141], v[182:185], v[94:97]
	v_mfma_f32_16x16x32_bf16 v[90:93], v[134:137], v[182:185], v[90:93]
	v_mfma_f32_16x16x32_bf16 v[78:81], v[138:141], v[190:193], v[78:81]
	v_mfma_f32_16x16x32_bf16 v[74:77], v[134:137], v[190:193], v[74:77]
	v_mfma_f32_16x16x32_bf16 v[126:129], v[130:133], v[166:169], v[126:129]
	v_mfma_f32_16x16x32_bf16 v[122:125], v[146:149], v[166:169], v[122:125]
	v_mfma_f32_16x16x32_bf16 v[110:113], v[130:133], v[174:177], v[110:113]
	v_mfma_f32_16x16x32_bf16 v[106:109], v[146:149], v[174:177], v[106:109]
	v_mfma_f32_16x16x32_bf16 v[94:97], v[130:133], v[186:189], v[94:97]
	v_mfma_f32_16x16x32_bf16 v[90:93], v[146:149], v[186:189], v[90:93]
	v_mfma_f32_16x16x32_bf16 v[78:81], v[130:133], v[224:227], v[78:81]
	v_mfma_f32_16x16x32_bf16 v[74:77], v[146:149], v[224:227], v[74:77]
	s_setprio 0
	s_setprio 1
	v_mfma_f32_16x16x32_bf16 v[118:121], v[142:145], v[162:165], v[118:121]
	v_mfma_f32_16x16x32_bf16 v[114:117], v[154:157], v[162:165], v[114:117]
	v_mfma_f32_16x16x32_bf16 v[102:105], v[142:145], v[170:173], v[102:105]
	v_mfma_f32_16x16x32_bf16 v[98:101], v[154:157], v[170:173], v[98:101]
	v_mfma_f32_16x16x32_bf16 v[86:89], v[142:145], v[182:185], v[86:89]
	v_mfma_f32_16x16x32_bf16 v[82:85], v[154:157], v[182:185], v[82:85]
	v_mfma_f32_16x16x32_bf16 v[70:73], v[142:145], v[190:193], v[70:73]
	v_mfma_f32_16x16x32_bf16 v[66:69], v[154:157], v[190:193], v[66:69]
	v_mfma_f32_16x16x32_bf16 v[118:121], v[150:153], v[166:169], v[118:121]
	v_mfma_f32_16x16x32_bf16 v[114:117], v[158:161], v[166:169], v[114:117]
	v_mfma_f32_16x16x32_bf16 v[102:105], v[150:153], v[174:177], v[102:105]
	v_mfma_f32_16x16x32_bf16 v[98:101], v[158:161], v[174:177], v[98:101]
	v_mfma_f32_16x16x32_bf16 v[86:89], v[150:153], v[186:189], v[86:89]
	v_mfma_f32_16x16x32_bf16 v[82:85], v[158:161], v[186:189], v[82:85]
	v_mfma_f32_16x16x32_bf16 v[70:73], v[150:153], v[224:227], v[70:73]
	v_mfma_f32_16x16x32_bf16 v[66:69], v[158:161], v[224:227], v[66:69]
	s_setprio 0
	s_barrier
	s_addk_i32 s75, 0x80
	s_mov_b32 m0, s77
	s_add_u32 s98, s8, s75
	s_addc_u32 s99, s9, 0
	ds_read_b128 v[162:165], v222 offset:49152
	ds_read_b128 v[166:169], v222 offset:50176
	ds_read_b128 v[170:173], v222 offset:51200
	ds_read_b128 v[174:177], v222 offset:52224
	ds_read_b128 v[182:185], v222 offset:53248
	ds_read_b128 v[186:189], v222 offset:54272
	ds_read_b128 v[190:193], v222 offset:55296
	ds_read_b128 v[224:227], v222 offset:56320
	global_load_lds_dwordx4 v196, s[98:99]
	s_add_u32 s100, s98, s44
	s_addc_u32 s101, s99, 0
	s_mov_b32 m0, s78
	s_nop 0
	global_load_lds_dwordx4 v196, s[100:101]
	s_add_u32 s98, s8, s75
	s_addc_u32 s99, s9, 0
	s_mov_b32 m0, s81
	s_nop 0
	global_load_lds_dwordx4 v197, s[98:99]
	s_add_u32 s100, s98, s44
	s_addc_u32 s101, s99, 0
	s_mov_b32 m0, s82
	s_nop 0
	global_load_lds_dwordx4 v197, s[100:101]
	s_add_u32 s98, s6, s65
	s_addc_u32 s99, s7, 0
	s_mov_b32 m0, s79
	s_nop 0
	global_load_lds_dwordx4 v201, s[98:99]
	s_add_u32 s100, s98, s35
	s_addc_u32 s101, s99, 0
	s_mov_b32 m0, s80
	s_nop 0
	global_load_lds_dwordx4 v201, s[100:101]
	s_waitcnt vmcnt(8)
	s_waitcnt lgkmcnt(0)
	s_barrier
	s_setprio 1
	s_waitcnt lgkmcnt(0)
	v_mfma_f32_16x16x32_bf16 v[62:65], v[138:141], v[162:165], v[62:65]
	v_mfma_f32_16x16x32_bf16 v[58:61], v[134:137], v[162:165], v[58:61]
	v_mfma_f32_16x16x32_bf16 v[46:49], v[138:141], v[170:173], v[46:49]
	v_mfma_f32_16x16x32_bf16 v[42:45], v[134:137], v[170:173], v[42:45]
	v_mfma_f32_16x16x32_bf16 v[30:33], v[138:141], v[182:185], v[30:33]
	v_mfma_f32_16x16x32_bf16 v[26:29], v[134:137], v[182:185], v[26:29]
	v_mfma_f32_16x16x32_bf16 v[14:17], v[138:141], v[190:193], v[14:17]
	v_mfma_f32_16x16x32_bf16 v[10:13], v[134:137], v[190:193], v[10:13]
	v_mfma_f32_16x16x32_bf16 v[62:65], v[130:133], v[166:169], v[62:65]
	v_mfma_f32_16x16x32_bf16 v[58:61], v[146:149], v[166:169], v[58:61]
	v_mfma_f32_16x16x32_bf16 v[46:49], v[130:133], v[174:177], v[46:49]
	v_mfma_f32_16x16x32_bf16 v[42:45], v[146:149], v[174:177], v[42:45]
	v_mfma_f32_16x16x32_bf16 v[30:33], v[130:133], v[186:189], v[30:33]
	v_mfma_f32_16x16x32_bf16 v[26:29], v[146:149], v[186:189], v[26:29]
	v_mfma_f32_16x16x32_bf16 v[14:17], v[130:133], v[224:227], v[14:17]
	v_mfma_f32_16x16x32_bf16 v[10:13], v[146:149], v[224:227], v[10:13]
	s_setprio 0
	s_setprio 1
	v_mfma_f32_16x16x32_bf16 v[54:57], v[142:145], v[162:165], v[54:57]
	v_mfma_f32_16x16x32_bf16 v[50:53], v[154:157], v[162:165], v[50:53]
	v_mfma_f32_16x16x32_bf16 v[38:41], v[142:145], v[170:173], v[38:41]
	v_mfma_f32_16x16x32_bf16 v[34:37], v[154:157], v[170:173], v[34:37]
	v_mfma_f32_16x16x32_bf16 v[22:25], v[142:145], v[182:185], v[22:25]
	v_mfma_f32_16x16x32_bf16 v[18:21], v[154:157], v[182:185], v[18:21]
	v_mfma_f32_16x16x32_bf16 v[6:9], v[142:145], v[190:193], v[6:9]
	v_mfma_f32_16x16x32_bf16 v[2:5], v[154:157], v[190:193], v[2:5]
	v_mfma_f32_16x16x32_bf16 v[54:57], v[150:153], v[166:169], v[54:57]
	v_mfma_f32_16x16x32_bf16 v[50:53], v[158:161], v[166:169], v[50:53]
	v_mfma_f32_16x16x32_bf16 v[38:41], v[150:153], v[174:177], v[38:41]
	v_mfma_f32_16x16x32_bf16 v[34:37], v[158:161], v[174:177], v[34:37]
	v_mfma_f32_16x16x32_bf16 v[22:25], v[150:153], v[186:189], v[22:25]
	v_mfma_f32_16x16x32_bf16 v[18:21], v[158:161], v[186:189], v[18:21]
	v_mfma_f32_16x16x32_bf16 v[6:9], v[150:153], v[224:227], v[6:9]
	v_mfma_f32_16x16x32_bf16 v[2:5], v[158:161], v[224:227], v[2:5]
	s_setprio 0
	s_barrier
	s_add_i32 s64, s64, 2
	s_addk_i32 s60, 0x100
	s_addk_i32 s63, 0x100
	s_cmp_ge_i32 s64, s74
	s_cbranch_scc0 .LBB0_2597

.LBB0_2937:
	ds_read_b128 v[18:21], v180
	ds_read_b128 v[22:25], v181
	ds_read_b128 v[26:29], v188
	ds_read_b128 v[30:33], v189
	ds_read_b128 v[2:5], v182
	ds_read_b128 v[6:9], v183
	ds_read_b128 v[10:13], v190
	ds_read_b128 v[14:17], v191
	s_add_i32 s84, s28, 0x80
	s_cmp_eq_u32 s67, s83
	s_cselect_b32 s86, s25, s84
	s_cselect_b32 s87, s29, s82
	s_add_i32 s84, s86, 0x80
	s_add_i32 s85, s87, 0x80
	ds_read_b128 v[164:167], v196
	ds_read_b128 v[168:171], v196 offset:1024
	ds_read_b128 v[198:201], v196 offset:2048
	ds_read_b128 v[202:205], v196 offset:3072
	ds_read_b128 v[214:217], v196 offset:4096
	ds_read_b128 v[218:221], v196 offset:5120
	ds_read_b128 v[222:225], v196 offset:6144
	ds_read_b128 v[226:229], v196 offset:7168
	s_add_i32 s88, s28, s65
	s_add_u32 s98, s4, s88
	s_addc_u32 s99, s5, 0
	s_add_i32 m0, s49, 0xc000
	s_add_i32 s88, s28, s70
	global_load_lds_dwordx4 v176, s[98:99]
	s_add_i32 m0, s49, 0xe000
	s_add_u32 s100, s4, s88
	s_addc_u32 s101, s5, 0
	global_load_lds_dwordx4 v176, s[100:101]
	s_waitcnt vmcnt(8)
	s_waitcnt lgkmcnt(0)
	s_barrier
	s_setprio 1
	s_waitcnt lgkmcnt(0)
	v_mfma_f32_16x16x128_f8f6f4 v[158:161], v[18:25], v[164:171], v[158:161]
	v_mfma_f32_16x16x128_f8f6f4 v[154:157], v[26:33], v[164:171], v[154:157]
	v_mfma_f32_16x16x128_f8f6f4 v[150:153], v[18:25], v[198:205], v[150:153]
	v_mfma_f32_16x16x128_f8f6f4 v[146:149], v[26:33], v[198:205], v[146:149]
	v_mfma_f32_16x16x128_f8f6f4 v[138:141], v[18:25], v[214:221], v[138:141]
	v_mfma_f32_16x16x128_f8f6f4 v[130:133], v[26:33], v[214:221], v[130:133]
	v_mfma_f32_16x16x128_f8f6f4 v[122:125], v[18:25], v[222:229], v[122:125]
	v_mfma_f32_16x16x128_f8f6f4 v[114:117], v[26:33], v[222:229], v[114:117]
	s_setprio 0
	s_setprio 1
	v_mfma_f32_16x16x128_f8f6f4 v[142:145], v[2:9], v[164:171], v[142:145]
	v_mfma_f32_16x16x128_f8f6f4 v[134:137], v[10:17], v[164:171], v[134:137]
	v_mfma_f32_16x16x128_f8f6f4 v[126:129], v[2:9], v[198:205], v[126:129]
	v_mfma_f32_16x16x128_f8f6f4 v[118:121], v[10:17], v[198:205], v[118:121]
	v_mfma_f32_16x16x128_f8f6f4 v[110:113], v[2:9], v[214:221], v[110:113]
	v_mfma_f32_16x16x128_f8f6f4 v[106:109], v[10:17], v[214:221], v[106:109]
	v_mfma_f32_16x16x128_f8f6f4 v[102:105], v[2:9], v[222:229], v[102:105]
	v_mfma_f32_16x16x128_f8f6f4 v[98:101], v[10:17], v[222:229], v[98:101]
	s_setprio 0
	s_barrier
	ds_read_b128 v[164:167], v196 offset:16384
	ds_read_b128 v[168:171], v196 offset:17408
	ds_read_b128 v[198:201], v196 offset:18432
	ds_read_b128 v[202:205], v196 offset:19456
	ds_read_b128 v[214:217], v196 offset:20480
	ds_read_b128 v[218:221], v196 offset:21504
	ds_read_b128 v[222:225], v196 offset:22528
	ds_read_b128 v[226:229], v196 offset:23552
	s_mov_b32 m0, s50
	s_add_u32 s98, s6, s87
	s_addc_u32 s99, s7, 0
	global_load_lds_dwordx4 v177, s[98:99]
	s_add_i32 s87, s87, s48
	s_add_u32 s100, s6, s87
	s_addc_u32 s101, s7, 0
	s_mov_b32 m0, s51
	s_add_i32 s87, s87, s48
	global_load_lds_dwordx4 v177, s[100:101]
	s_mov_b32 m0, s52
	s_add_u32 s98, s6, s87
	s_addc_u32 s99, s7, 0
	global_load_lds_dwordx4 v177, s[98:99]
	s_add_i32 s87, s87, s48
	s_add_u32 s100, s6, s87
	s_addc_u32 s101, s7, 0
	s_mov_b32 m0, s53
	s_nop 0
	global_load_lds_dwordx4 v177, s[100:101]
	s_mov_b32 m0, s49
	s_add_u32 s98, s4, s86
	s_addc_u32 s99, s5, 0
	global_load_lds_dwordx4 v176, s[98:99]
	s_add_i32 s86, s86, s47
	s_add_u32 s100, s4, s86
	s_addc_u32 s101, s5, 0
	s_mov_b32 m0, s54
	s_nop 0
	global_load_lds_dwordx4 v176, s[100:101]
	s_waitcnt vmcnt(8)
	s_waitcnt lgkmcnt(0)
	s_barrier
	s_setprio 1
	s_waitcnt lgkmcnt(0)
	v_mfma_f32_16x16x128_f8f6f4 v[94:97], v[18:25], v[164:171], v[94:97]
	v_mfma_f32_16x16x128_f8f6f4 v[90:93], v[26:33], v[164:171], v[90:93]
	v_mfma_f32_16x16x128_f8f6f4 v[86:89], v[18:25], v[198:205], v[86:89]
	v_mfma_f32_16x16x128_f8f6f4 v[82:85], v[26:33], v[198:205], v[82:85]
	v_mfma_f32_16x16x128_f8f6f4 v[74:77], v[18:25], v[214:221], v[74:77]
	v_mfma_f32_16x16x128_f8f6f4 v[66:69], v[26:33], v[214:221], v[66:69]
	v_mfma_f32_16x16x128_f8f6f4 v[58:61], v[18:25], v[222:229], v[58:61]
	v_mfma_f32_16x16x128_f8f6f4 v[50:53], v[26:33], v[222:229], v[50:53]
	s_setprio 0
	s_setprio 1
	v_mfma_f32_16x16x128_f8f6f4 v[78:81], v[2:9], v[164:171], v[78:81]
	v_mfma_f32_16x16x128_f8f6f4 v[70:73], v[10:17], v[164:171], v[70:73]
	v_mfma_f32_16x16x128_f8f6f4 v[62:65], v[2:9], v[198:205], v[62:65]
	v_mfma_f32_16x16x128_f8f6f4 v[54:57], v[10:17], v[198:205], v[54:57]
	v_mfma_f32_16x16x128_f8f6f4 v[46:49], v[2:9], v[214:221], v[46:49]
	v_mfma_f32_16x16x128_f8f6f4 v[42:45], v[10:17], v[214:221], v[42:45]
	v_mfma_f32_16x16x128_f8f6f4 v[38:41], v[2:9], v[222:229], v[38:41]
	v_mfma_f32_16x16x128_f8f6f4 v[34:37], v[10:17], v[222:229], v[34:37]
	s_setprio 0
	s_barrier
	ds_read_b128 v[2:5], v184
	ds_read_b128 v[6:9], v185
	ds_read_b128 v[10:13], v192
	ds_read_b128 v[14:17], v193
	ds_read_b128 v[18:21], v186
	ds_read_b128 v[22:25], v187
	ds_read_b128 v[26:29], v194
	ds_read_b128 v[30:33], v195
	ds_read_b128 v[164:167], v196 offset:32768
	ds_read_b128 v[168:171], v196 offset:33792
	ds_read_b128 v[198:201], v196 offset:34816
	ds_read_b128 v[202:205], v196 offset:35840
	ds_read_b128 v[214:217], v196 offset:36864
	ds_read_b128 v[218:221], v196 offset:37888
	ds_read_b128 v[222:225], v196 offset:38912
	ds_read_b128 v[226:229], v196 offset:39936
	s_add_i32 s86, s86, s47
	s_mov_b32 m0, s55
	s_add_u32 s98, s4, s86
	s_addc_u32 s99, s5, 0
	global_load_lds_dwordx4 v176, s[98:99]
	s_add_i32 s86, s86, s47
	s_add_u32 s100, s4, s86
	s_addc_u32 s101, s5, 0
	s_mov_b32 m0, s56
	s_nop 0
	global_load_lds_dwordx4 v176, s[100:101]
	s_waitcnt vmcnt(8)
	s_waitcnt lgkmcnt(0)
	s_barrier
	s_setprio 1
	s_waitcnt lgkmcnt(0)
	v_mfma_f32_16x16x128_f8f6f4 v[158:161], v[2:9], v[164:171], v[158:161]
	v_mfma_f32_16x16x128_f8f6f4 v[154:157], v[10:17], v[164:171], v[154:157]
	v_mfma_f32_16x16x128_f8f6f4 v[150:153], v[2:9], v[198:205], v[150:153]
	v_mfma_f32_16x16x128_f8f6f4 v[146:149], v[10:17], v[198:205], v[146:149]
	v_mfma_f32_16x16x128_f8f6f4 v[138:141], v[2:9], v[214:221], v[138:141]
	v_mfma_f32_16x16x128_f8f6f4 v[130:133], v[10:17], v[214:221], v[130:133]
	v_mfma_f32_16x16x128_f8f6f4 v[122:125], v[2:9], v[222:229], v[122:125]
	v_mfma_f32_16x16x128_f8f6f4 v[114:117], v[10:17], v[222:229], v[114:117]
	s_setprio 0
	s_setprio 1
	v_mfma_f32_16x16x128_f8f6f4 v[142:145], v[18:25], v[164:171], v[142:145]
	v_mfma_f32_16x16x128_f8f6f4 v[134:137], v[26:33], v[164:171], v[134:137]
	v_mfma_f32_16x16x128_f8f6f4 v[126:129], v[18:25], v[198:205], v[126:129]
	v_mfma_f32_16x16x128_f8f6f4 v[118:121], v[26:33], v[198:205], v[118:121]
	v_mfma_f32_16x16x128_f8f6f4 v[110:113], v[18:25], v[214:221], v[110:113]
	v_mfma_f32_16x16x128_f8f6f4 v[106:109], v[26:33], v[214:221], v[106:109]
	v_mfma_f32_16x16x128_f8f6f4 v[102:105], v[18:25], v[222:229], v[102:105]
	v_mfma_f32_16x16x128_f8f6f4 v[98:101], v[26:33], v[222:229], v[98:101]
	s_setprio 0
	s_barrier
	ds_read_b128 v[164:167], v196 offset:49152
	ds_read_b128 v[168:171], v196 offset:50176
	ds_read_b128 v[198:201], v196 offset:51200
	ds_read_b128 v[202:205], v196 offset:52224
	ds_read_b128 v[214:217], v196 offset:53248
	ds_read_b128 v[218:221], v196 offset:54272
	ds_read_b128 v[222:225], v196 offset:55296
	ds_read_b128 v[226:229], v196 offset:56320
	s_mov_b32 m0, s58
	s_add_u32 s98, s6, s85
	s_addc_u32 s99, s7, 0
	global_load_lds_dwordx4 v177, s[98:99]
	s_add_i32 s85, s85, s48
	s_add_u32 s100, s6, s85
	s_addc_u32 s101, s7, 0
	s_mov_b32 m0, s59
	s_add_i32 s85, s85, s48
	global_load_lds_dwordx4 v177, s[100:101]
	s_mov_b32 m0, s62
	s_add_u32 s98, s6, s85
	s_addc_u32 s99, s7, 0
	global_load_lds_dwordx4 v177, s[98:99]
	s_add_i32 s85, s85, s48
	s_add_u32 s100, s6, s85
	s_addc_u32 s101, s7, 0
	s_mov_b32 m0, s63
	s_nop 0
	global_load_lds_dwordx4 v177, s[100:101]
	s_mov_b32 m0, s60
	s_add_u32 s98, s4, s84
	s_addc_u32 s99, s5, 0
	global_load_lds_dwordx4 v176, s[98:99]
	s_add_i32 s84, s84, s47
	s_add_u32 s100, s4, s84
	s_addc_u32 s101, s5, 0
	s_mov_b32 m0, s61
	s_nop 0
	global_load_lds_dwordx4 v176, s[100:101]
	s_waitcnt vmcnt(8)
	s_waitcnt lgkmcnt(0)
	s_barrier
	s_setprio 1
	s_waitcnt lgkmcnt(0)
	v_mfma_f32_16x16x128_f8f6f4 v[94:97], v[2:9], v[164:171], v[94:97]
	v_mfma_f32_16x16x128_f8f6f4 v[90:93], v[10:17], v[164:171], v[90:93]
	v_mfma_f32_16x16x128_f8f6f4 v[86:89], v[2:9], v[198:205], v[86:89]
	v_mfma_f32_16x16x128_f8f6f4 v[82:85], v[10:17], v[198:205], v[82:85]
	v_mfma_f32_16x16x128_f8f6f4 v[74:77], v[2:9], v[214:221], v[74:77]
	v_mfma_f32_16x16x128_f8f6f4 v[66:69], v[10:17], v[214:221], v[66:69]
	v_mfma_f32_16x16x128_f8f6f4 v[58:61], v[2:9], v[222:229], v[58:61]
	v_mfma_f32_16x16x128_f8f6f4 v[50:53], v[10:17], v[222:229], v[50:53]
	s_setprio 0
	s_setprio 1
	v_mfma_f32_16x16x128_f8f6f4 v[78:81], v[18:25], v[164:171], v[78:81]
	v_mfma_f32_16x16x128_f8f6f4 v[70:73], v[26:33], v[164:171], v[70:73]
	v_mfma_f32_16x16x128_f8f6f4 v[62:65], v[18:25], v[198:205], v[62:65]
	v_mfma_f32_16x16x128_f8f6f4 v[54:57], v[26:33], v[198:205], v[54:57]
	v_mfma_f32_16x16x128_f8f6f4 v[46:49], v[18:25], v[214:221], v[46:49]
	v_mfma_f32_16x16x128_f8f6f4 v[42:45], v[26:33], v[214:221], v[42:45]
	v_mfma_f32_16x16x128_f8f6f4 v[38:41], v[18:25], v[222:229], v[38:41]
	v_mfma_f32_16x16x128_f8f6f4 v[34:37], v[26:33], v[222:229], v[34:37]
	s_setprio 0
	s_barrier
	s_add_i32 s83, s83, 2
	s_addk_i32 s28, 0x100
	s_addk_i32 s82, 0x100
	s_cmp_ge_i32 s83, s64
	s_cbranch_scc0 .LBB0_2937
	v_pk_fma_f32 v[164:165], v[160:161], s[18:19], 0 op_sel_hi:[1,0,0]
	v_pk_fma_f32 v[168:169], v[158:159], s[18:19], 0 op_sel_hi:[1,0,0]
	v_pk_fma_f32 v[172:173], v[144:145], s[20:21], 0 op_sel_hi:[1,0,0]
	v_pk_fma_f32 v[174:175], v[142:143], s[20:21], 0 op_sel_hi:[1,0,0]
	v_pk_fma_f32 v[156:157], v[156:157], s[18:19], 0 op_sel_hi:[1,0,0]
	v_pk_fma_f32 v[160:161], v[154:155], s[18:19], 0 op_sel_hi:[1,0,0]
	v_pk_fma_f32 v[166:167], v[136:137], s[20:21], 0 op_sel_hi:[1,0,0]
	v_pk_fma_f32 v[170:171], v[134:135], s[20:21], 0 op_sel_hi:[1,0,0]
	v_pk_fma_f32 v[152:153], v[152:153], s[18:19], 0 op_sel_hi:[1,0,0]
	v_pk_fma_f32 v[150:151], v[150:151], s[18:19], 0 op_sel_hi:[1,0,0]
	v_pk_fma_f32 v[154:155], v[128:129], s[20:21], 0 op_sel_hi:[1,0,0]
	v_pk_fma_f32 v[158:159], v[126:127], s[20:21], 0 op_sel_hi:[1,0,0]
	v_pk_fma_f32 v[142:143], v[148:149], s[18:19], 0 op_sel_hi:[1,0,0]
	v_pk_fma_f32 v[144:145], v[146:147], s[18:19], 0 op_sel_hi:[1,0,0]
	v_pk_fma_f32 v[146:147], v[120:121], s[20:21], 0 op_sel_hi:[1,0,0]
	v_pk_fma_f32 v[148:149], v[118:119], s[20:21], 0 op_sel_hi:[1,0,0]
	v_pk_fma_f32 v[134:135], v[140:141], s[18:19], 0 op_sel_hi:[1,0,0]
	v_pk_fma_f32 v[136:137], v[138:139], s[18:19], 0 op_sel_hi:[1,0,0]
	v_pk_fma_f32 v[138:139], v[112:113], s[20:21], 0 op_sel_hi:[1,0,0]
	v_pk_fma_f32 v[140:141], v[110:111], s[20:21], 0 op_sel_hi:[1,0,0]
	v_pk_fma_f32 v[126:127], v[132:133], s[18:19], 0 op_sel_hi:[1,0,0]
	v_pk_fma_f32 v[128:129], v[130:131], s[18:19], 0 op_sel_hi:[1,0,0]
	v_pk_fma_f32 v[130:131], v[108:109], s[20:21], 0 op_sel_hi:[1,0,0]
	v_pk_fma_f32 v[132:133], v[106:107], s[20:21], 0 op_sel_hi:[1,0,0]
	v_pk_fma_f32 v[108:109], v[124:125], s[18:19], 0 op_sel_hi:[1,0,0]
	v_pk_fma_f32 v[118:119], v[122:123], s[18:19], 0 op_sel_hi:[1,0,0]
	v_pk_fma_f32 v[120:121], v[104:105], s[20:21], 0 op_sel_hi:[1,0,0]
	v_pk_fma_f32 v[122:123], v[102:103], s[20:21], 0 op_sel_hi:[1,0,0]
	v_pk_fma_f32 v[102:103], v[116:117], s[18:19], 0 op_sel_hi:[1,0,0]
	v_pk_fma_f32 v[104:105], v[114:115], s[18:19], 0 op_sel_hi:[1,0,0]
	v_pk_fma_f32 v[106:107], v[100:101], s[20:21], 0 op_sel_hi:[1,0,0]
	v_pk_fma_f32 v[112:113], v[98:99], s[20:21], 0 op_sel_hi:[1,0,0]
	v_pk_fma_f32 v[96:97], v[96:97], s[18:19], 0 op_sel_hi:[1,0,0]
	v_pk_fma_f32 v[98:99], v[94:95], s[18:19], 0 op_sel_hi:[1,0,0]
	v_pk_fma_f32 v[100:101], v[80:81], s[20:21], 0 op_sel_hi:[1,0,0]
	v_pk_fma_f32 v[110:111], v[78:79], s[20:21], 0 op_sel_hi:[1,0,0]
	v_pk_fma_f32 v[78:79], v[92:93], s[18:19], 0 op_sel_hi:[1,0,0]
	v_pk_fma_f32 v[90:91], v[90:91], s[18:19], 0 op_sel_hi:[1,0,0]
	v_pk_fma_f32 v[92:93], v[72:73], s[20:21], 0 op_sel_hi:[1,0,0]
	v_pk_fma_f32 v[94:95], v[70:71], s[20:21], 0 op_sel_hi:[1,0,0]
	v_pk_fma_f32 v[70:71], v[88:89], s[18:19], 0 op_sel_hi:[1,0,0]
	v_pk_fma_f32 v[72:73], v[86:87], s[18:19], 0 op_sel_hi:[1,0,0]
	v_pk_fma_f32 v[64:65], v[64:65], s[20:21], 0 op_sel_hi:[1,0,0]
	v_pk_fma_f32 v[80:81], v[62:63], s[20:21], 0 op_sel_hi:[1,0,0]
	v_pk_fma_f32 v[32:33], v[84:85], s[18:19], 0 op_sel_hi:[1,0,0]
	v_pk_fma_f32 v[62:63], v[82:83], s[18:19], 0 op_sel_hi:[1,0,0]
	v_pk_fma_f32 v[56:57], v[56:57], s[20:21], 0 op_sel_hi:[1,0,0]
	v_pk_fma_f32 v[54:55], v[54:55], s[20:21], 0 op_sel_hi:[1,0,0]
	v_pk_fma_f32 v[24:25], v[76:77], s[18:19], 0 op_sel_hi:[1,0,0]
	v_pk_fma_f32 v[28:29], v[74:75], s[18:19], 0 op_sel_hi:[1,0,0]
	v_pk_fma_f32 v[30:31], v[48:49], s[20:21], 0 op_sel_hi:[1,0,0]
	v_pk_fma_f32 v[46:47], v[46:47], s[20:21], 0 op_sel_hi:[1,0,0]
	v_pk_fma_f32 v[16:17], v[68:69], s[18:19], 0 op_sel_hi:[1,0,0]
	v_pk_fma_f32 v[20:21], v[66:67], s[18:19], 0 op_sel_hi:[1,0,0]
	v_pk_fma_f32 v[22:23], v[44:45], s[20:21], 0 op_sel_hi:[1,0,0]
	v_pk_fma_f32 v[26:27], v[42:43], s[20:21], 0 op_sel_hi:[1,0,0]
	v_pk_fma_f32 v[8:9], v[60:61], s[18:19], 0 op_sel_hi:[1,0,0]
	v_pk_fma_f32 v[12:13], v[58:59], s[18:19], 0 op_sel_hi:[1,0,0]
	v_pk_fma_f32 v[14:15], v[40:41], s[20:21], 0 op_sel_hi:[1,0,0]
	v_pk_fma_f32 v[18:19], v[38:39], s[20:21], 0 op_sel_hi:[1,0,0]
	v_pk_fma_f32 v[2:3], v[52:53], s[18:19], 0 op_sel_hi:[1,0,0]
	v_pk_fma_f32 v[4:5], v[50:51], s[18:19], 0 op_sel_hi:[1,0,0]
	v_pk_fma_f32 v[6:7], v[36:37], s[20:21], 0 op_sel_hi:[1,0,0]
	v_pk_fma_f32 v[10:11], v[34:35], s[20:21], 0 op_sel_hi:[1,0,0]

.LBB0_3007:
	ds_read_b128 v[18:21], v168
	ds_read_b128 v[22:25], v169
	ds_read_b128 v[26:29], v176
	ds_read_b128 v[30:33], v177
	ds_read_b128 v[2:5], v170
	ds_read_b128 v[6:9], v171
	ds_read_b128 v[10:13], v178
	ds_read_b128 v[14:17], v179
	s_add_i32 s76, s20, 0x80
	s_cmp_eq_u32 s61, s75
	s_cselect_b32 s78, s11, s76
	s_cselect_b32 s77, s21, s74
	s_add_i32 s76, s78, 0x80
	ds_read_b128 v[186:189], v184
	ds_read_b128 v[190:193], v184 offset:1024
	ds_read_b128 v[194:197], v184 offset:2048
	ds_read_b128 v[198:201], v184 offset:3072
	ds_read_b128 v[202:205], v184 offset:4096
	ds_read_b128 v[206:209], v184 offset:5120
	ds_read_b128 v[214:217], v184 offset:6144
	ds_read_b128 v[218:221], v184 offset:7168
	s_add_i32 s79, s20, s59
	s_add_u32 s98, s4, s79
	s_addc_u32 s99, s5, 0
	s_add_i32 m0, s30, 0xc000
	s_add_i32 s79, s20, s66
	global_load_lds_dwordx4 v164, s[98:99]
	s_add_i32 m0, s30, 0xe000
	s_add_u32 s100, s4, s79
	s_addc_u32 s101, s5, 0
	global_load_lds_dwordx4 v164, s[100:101]
	s_waitcnt vmcnt(8)
	s_waitcnt lgkmcnt(0)
	s_barrier
	s_setprio 1
	s_waitcnt lgkmcnt(0)
	v_mfma_f32_16x16x128_f8f6f4 v[158:161], v[18:25], v[186:193], v[158:161]
	v_mfma_f32_16x16x128_f8f6f4 v[154:157], v[26:33], v[186:193], v[154:157]
	v_mfma_f32_16x16x128_f8f6f4 v[150:153], v[18:25], v[194:201], v[150:153]
	v_mfma_f32_16x16x128_f8f6f4 v[146:149], v[26:33], v[194:201], v[146:149]
	v_mfma_f32_16x16x128_f8f6f4 v[138:141], v[18:25], v[202:209], v[138:141]
	v_mfma_f32_16x16x128_f8f6f4 v[130:133], v[26:33], v[202:209], v[130:133]
	v_mfma_f32_16x16x128_f8f6f4 v[122:125], v[18:25], v[214:221], v[122:125]
	v_mfma_f32_16x16x128_f8f6f4 v[114:117], v[26:33], v[214:221], v[114:117]
	s_setprio 0
	s_setprio 1
	v_mfma_f32_16x16x128_f8f6f4 v[142:145], v[2:9], v[186:193], v[142:145]
	v_mfma_f32_16x16x128_f8f6f4 v[134:137], v[10:17], v[186:193], v[134:137]
	v_mfma_f32_16x16x128_f8f6f4 v[126:129], v[2:9], v[194:201], v[126:129]
	v_mfma_f32_16x16x128_f8f6f4 v[118:121], v[10:17], v[194:201], v[118:121]
	v_mfma_f32_16x16x128_f8f6f4 v[110:113], v[2:9], v[202:209], v[110:113]
	v_mfma_f32_16x16x128_f8f6f4 v[106:109], v[10:17], v[202:209], v[106:109]
	v_mfma_f32_16x16x128_f8f6f4 v[102:105], v[2:9], v[214:221], v[102:105]
	v_mfma_f32_16x16x128_f8f6f4 v[98:101], v[10:17], v[214:221], v[98:101]
	s_setprio 0
	s_barrier
	ds_read_b128 v[186:189], v184 offset:16384
	ds_read_b128 v[190:193], v184 offset:17408
	ds_read_b128 v[194:197], v184 offset:18432
	ds_read_b128 v[198:201], v184 offset:19456
	ds_read_b128 v[202:205], v184 offset:20480
	ds_read_b128 v[206:209], v184 offset:21504
	ds_read_b128 v[214:217], v184 offset:22528
	ds_read_b128 v[218:221], v184 offset:23552
	s_mov_b32 m0, s31
	s_add_u32 s98, s6, s77
	s_addc_u32 s99, s7, 0
	global_load_lds_dwordx4 v165, s[98:99]
	s_add_i32 s79, s77, s25
	s_add_u32 s100, s6, s79
	s_addc_u32 s101, s7, 0
	s_mov_b32 m0, s35
	s_add_i32 s79, s79, s25
	global_load_lds_dwordx4 v165, s[100:101]
	s_mov_b32 m0, s44
	s_add_u32 s98, s6, s79
	s_addc_u32 s99, s7, 0
	global_load_lds_dwordx4 v165, s[98:99]
	s_add_i32 s79, s79, s25
	s_add_u32 s100, s6, s79
	s_addc_u32 s101, s7, 0
	s_mov_b32 m0, s45
	s_nop 0
	global_load_lds_dwordx4 v165, s[100:101]
	s_mov_b32 m0, s30
	s_add_u32 s98, s4, s78
	s_addc_u32 s99, s5, 0
	global_load_lds_dwordx4 v164, s[98:99]
	s_add_i32 s78, s78, s24
	s_add_u32 s100, s4, s78
	s_addc_u32 s101, s5, 0
	s_mov_b32 m0, s46
	s_nop 0
	global_load_lds_dwordx4 v164, s[100:101]
	s_waitcnt vmcnt(8)
	s_waitcnt lgkmcnt(0)
	s_barrier
	s_setprio 1
	s_waitcnt lgkmcnt(0)
	v_mfma_f32_16x16x128_f8f6f4 v[94:97], v[18:25], v[186:193], v[94:97]
	v_mfma_f32_16x16x128_f8f6f4 v[90:93], v[26:33], v[186:193], v[90:93]
	v_mfma_f32_16x16x128_f8f6f4 v[86:89], v[18:25], v[194:201], v[86:89]
	v_mfma_f32_16x16x128_f8f6f4 v[82:85], v[26:33], v[194:201], v[82:85]
	v_mfma_f32_16x16x128_f8f6f4 v[74:77], v[18:25], v[202:209], v[74:77]
	v_mfma_f32_16x16x128_f8f6f4 v[66:69], v[26:33], v[202:209], v[66:69]
	v_mfma_f32_16x16x128_f8f6f4 v[58:61], v[18:25], v[214:221], v[58:61]
	v_mfma_f32_16x16x128_f8f6f4 v[50:53], v[26:33], v[214:221], v[50:53]
	s_setprio 0
	s_setprio 1
	v_mfma_f32_16x16x128_f8f6f4 v[78:81], v[2:9], v[186:193], v[78:81]
	v_mfma_f32_16x16x128_f8f6f4 v[70:73], v[10:17], v[186:193], v[70:73]
	v_mfma_f32_16x16x128_f8f6f4 v[62:65], v[2:9], v[194:201], v[62:65]
	v_mfma_f32_16x16x128_f8f6f4 v[54:57], v[10:17], v[194:201], v[54:57]
	v_mfma_f32_16x16x128_f8f6f4 v[46:49], v[2:9], v[202:209], v[46:49]
	v_mfma_f32_16x16x128_f8f6f4 v[42:45], v[10:17], v[202:209], v[42:45]
	v_mfma_f32_16x16x128_f8f6f4 v[38:41], v[2:9], v[214:221], v[38:41]
	v_mfma_f32_16x16x128_f8f6f4 v[34:37], v[10:17], v[214:221], v[34:37]
	s_setprio 0
	s_barrier
	ds_read_b128 v[2:5], v172
	ds_read_b128 v[6:9], v173
	ds_read_b128 v[10:13], v180
	ds_read_b128 v[14:17], v181
	ds_read_b128 v[18:21], v174
	ds_read_b128 v[22:25], v175
	ds_read_b128 v[26:29], v182
	ds_read_b128 v[30:33], v183
	ds_read_b128 v[186:189], v184 offset:32768
	ds_read_b128 v[190:193], v184 offset:33792
	ds_read_b128 v[194:197], v184 offset:34816
	ds_read_b128 v[198:201], v184 offset:35840
	ds_read_b128 v[202:205], v184 offset:36864
	ds_read_b128 v[206:209], v184 offset:37888
	ds_read_b128 v[214:217], v184 offset:38912
	ds_read_b128 v[218:221], v184 offset:39936
	s_add_i32 s78, s78, s24
	s_mov_b32 m0, s47
	s_add_u32 s98, s4, s78
	s_addc_u32 s99, s5, 0
	global_load_lds_dwordx4 v164, s[98:99]
	s_add_i32 s78, s78, s24
	s_add_u32 s100, s4, s78
	s_addc_u32 s101, s5, 0
	s_mov_b32 m0, s48
	s_nop 0
	global_load_lds_dwordx4 v164, s[100:101]
	s_waitcnt vmcnt(8)
	s_waitcnt lgkmcnt(0)
	s_barrier
	s_setprio 1
	s_waitcnt lgkmcnt(0)
	v_mfma_f32_16x16x128_f8f6f4 v[158:161], v[2:9], v[186:193], v[158:161]
	v_mfma_f32_16x16x128_f8f6f4 v[154:157], v[10:17], v[186:193], v[154:157]
	v_mfma_f32_16x16x128_f8f6f4 v[150:153], v[2:9], v[194:201], v[150:153]
	v_mfma_f32_16x16x128_f8f6f4 v[146:149], v[10:17], v[194:201], v[146:149]
	v_mfma_f32_16x16x128_f8f6f4 v[138:141], v[2:9], v[202:209], v[138:141]
	v_mfma_f32_16x16x128_f8f6f4 v[130:133], v[10:17], v[202:209], v[130:133]
	v_mfma_f32_16x16x128_f8f6f4 v[122:125], v[2:9], v[214:221], v[122:125]
	v_mfma_f32_16x16x128_f8f6f4 v[114:117], v[10:17], v[214:221], v[114:117]
	s_setprio 0
	s_setprio 1
	v_mfma_f32_16x16x128_f8f6f4 v[142:145], v[18:25], v[186:193], v[142:145]
	v_mfma_f32_16x16x128_f8f6f4 v[134:137], v[26:33], v[186:193], v[134:137]
	v_mfma_f32_16x16x128_f8f6f4 v[126:129], v[18:25], v[194:201], v[126:129]
	v_mfma_f32_16x16x128_f8f6f4 v[118:121], v[26:33], v[194:201], v[118:121]
	v_mfma_f32_16x16x128_f8f6f4 v[110:113], v[18:25], v[202:209], v[110:113]
	v_mfma_f32_16x16x128_f8f6f4 v[106:109], v[26:33], v[202:209], v[106:109]
	v_mfma_f32_16x16x128_f8f6f4 v[102:105], v[18:25], v[214:221], v[102:105]
	v_mfma_f32_16x16x128_f8f6f4 v[98:101], v[26:33], v[214:221], v[98:101]
	s_setprio 0
	s_barrier
	ds_read_b128 v[186:189], v184 offset:49152
	ds_read_b128 v[190:193], v184 offset:50176
	ds_read_b128 v[194:197], v184 offset:51200
	ds_read_b128 v[198:201], v184 offset:52224
	ds_read_b128 v[202:205], v184 offset:53248
	ds_read_b128 v[206:209], v184 offset:54272
	ds_read_b128 v[214:217], v184 offset:55296
	ds_read_b128 v[218:221], v184 offset:56320
	s_addk_i32 s77, 0x80
	s_mov_b32 m0, s51
	s_add_u32 s98, s6, s77
	s_addc_u32 s99, s7, 0
	global_load_lds_dwordx4 v165, s[98:99]
	s_add_i32 s77, s77, s25
	s_add_u32 s100, s6, s77
	s_addc_u32 s101, s7, 0
	s_mov_b32 m0, s52
	s_add_i32 s77, s77, s25
	global_load_lds_dwordx4 v165, s[100:101]
	s_mov_b32 m0, s55
	s_add_u32 s98, s6, s77
	s_addc_u32 s99, s7, 0
	global_load_lds_dwordx4 v165, s[98:99]
	s_add_i32 s77, s77, s25
	s_add_u32 s100, s6, s77
	s_addc_u32 s101, s7, 0
	s_mov_b32 m0, s57
	s_nop 0
	global_load_lds_dwordx4 v165, s[100:101]
	s_mov_b32 m0, s53
	s_add_u32 s98, s4, s76
	s_addc_u32 s99, s5, 0
	global_load_lds_dwordx4 v164, s[98:99]
	s_add_i32 s76, s76, s24
	s_add_u32 s100, s4, s76
	s_addc_u32 s101, s5, 0
	s_mov_b32 m0, s54
	s_nop 0
	global_load_lds_dwordx4 v164, s[100:101]
	s_waitcnt vmcnt(8)
	s_waitcnt lgkmcnt(0)
	s_barrier
	s_setprio 1
	s_waitcnt lgkmcnt(0)
	v_mfma_f32_16x16x128_f8f6f4 v[94:97], v[2:9], v[186:193], v[94:97]
	v_mfma_f32_16x16x128_f8f6f4 v[90:93], v[10:17], v[186:193], v[90:93]
	v_mfma_f32_16x16x128_f8f6f4 v[86:89], v[2:9], v[194:201], v[86:89]
	v_mfma_f32_16x16x128_f8f6f4 v[82:85], v[10:17], v[194:201], v[82:85]
	v_mfma_f32_16x16x128_f8f6f4 v[74:77], v[2:9], v[202:209], v[74:77]
	v_mfma_f32_16x16x128_f8f6f4 v[66:69], v[10:17], v[202:209], v[66:69]
	v_mfma_f32_16x16x128_f8f6f4 v[58:61], v[2:9], v[214:221], v[58:61]
	v_mfma_f32_16x16x128_f8f6f4 v[50:53], v[10:17], v[214:221], v[50:53]
	s_setprio 0
	s_setprio 1
	v_mfma_f32_16x16x128_f8f6f4 v[78:81], v[18:25], v[186:193], v[78:81]
	v_mfma_f32_16x16x128_f8f6f4 v[70:73], v[26:33], v[186:193], v[70:73]
	v_mfma_f32_16x16x128_f8f6f4 v[62:65], v[18:25], v[194:201], v[62:65]
	v_mfma_f32_16x16x128_f8f6f4 v[54:57], v[26:33], v[194:201], v[54:57]
	v_mfma_f32_16x16x128_f8f6f4 v[46:49], v[18:25], v[202:209], v[46:49]
	v_mfma_f32_16x16x128_f8f6f4 v[42:45], v[26:33], v[202:209], v[42:45]
	v_mfma_f32_16x16x128_f8f6f4 v[38:41], v[18:25], v[214:221], v[38:41]
	v_mfma_f32_16x16x128_f8f6f4 v[34:37], v[26:33], v[214:221], v[34:37]
	s_setprio 0
	s_barrier
	s_add_i32 s75, s75, 2
	s_addk_i32 s20, 0x100
	s_addk_i32 s74, 0x100
	s_cmp_ge_i32 s75, s58
	s_cbranch_scc0 .LBB0_3007
	v_pk_mul_f32 v[2:3], v[160:161], s[16:17] op_sel_hi:[1,0]
	v_pk_mul_f32 v[4:5], v[158:159], s[16:17] op_sel_hi:[1,0]
	v_pk_mul_f32 v[6:7], v[156:157], s[16:17] op_sel_hi:[1,0]
	v_pk_mul_f32 v[12:13], v[154:155], s[16:17] op_sel_hi:[1,0]
	v_pk_mul_f32 v[144:145], v[144:145], s[16:17] op_sel_hi:[1,0]
	v_pk_mul_f32 v[142:143], v[142:143], s[16:17] op_sel_hi:[1,0]
	v_pk_mul_f32 v[136:137], v[136:137], s[16:17] op_sel_hi:[1,0]
	v_pk_mul_f32 v[134:135], v[134:135], s[16:17] op_sel_hi:[1,0]
	v_pk_mul_f32 v[8:9], v[152:153], s[16:17] op_sel_hi:[1,0]
	v_pk_mul_f32 v[14:15], v[150:151], s[16:17] op_sel_hi:[1,0]
	v_pk_mul_f32 v[18:19], v[148:149], s[16:17] op_sel_hi:[1,0]
	v_pk_mul_f32 v[26:27], v[146:147], s[16:17] op_sel_hi:[1,0]
	v_pk_mul_f32 v[128:129], v[128:129], s[16:17] op_sel_hi:[1,0]
	v_pk_mul_f32 v[126:127], v[126:127], s[16:17] op_sel_hi:[1,0]
	v_pk_mul_f32 v[120:121], v[120:121], s[16:17] op_sel_hi:[1,0]
	v_pk_mul_f32 v[118:119], v[118:119], s[16:17] op_sel_hi:[1,0]
	v_pk_mul_f32 v[10:11], v[140:141], s[16:17] op_sel_hi:[1,0]
	v_pk_mul_f32 v[20:21], v[138:139], s[16:17] op_sel_hi:[1,0]
	v_pk_mul_f32 v[22:23], v[132:133], s[16:17] op_sel_hi:[1,0]
	v_pk_mul_f32 v[30:31], v[130:131], s[16:17] op_sel_hi:[1,0]
	v_pk_mul_f32 v[112:113], v[112:113], s[16:17] op_sel_hi:[1,0]
	v_pk_mul_f32 v[110:111], v[110:111], s[16:17] op_sel_hi:[1,0]
	v_pk_mul_f32 v[108:109], v[108:109], s[16:17] op_sel_hi:[1,0]
	v_pk_mul_f32 v[106:107], v[106:107], s[16:17] op_sel_hi:[1,0]
	v_pk_mul_f32 v[16:17], v[124:125], s[16:17] op_sel_hi:[1,0]
	v_pk_mul_f32 v[24:25], v[122:123], s[16:17] op_sel_hi:[1,0]
	v_pk_mul_f32 v[28:29], v[116:117], s[16:17] op_sel_hi:[1,0]
	v_pk_mul_f32 v[32:33], v[114:115], s[16:17] op_sel_hi:[1,0]
	v_pk_mul_f32 v[104:105], v[104:105], s[16:17] op_sel_hi:[1,0]
	v_pk_mul_f32 v[102:103], v[102:103], s[16:17] op_sel_hi:[1,0]
	v_pk_mul_f32 v[100:101], v[100:101], s[16:17] op_sel_hi:[1,0]
	v_pk_mul_f32 v[98:99], v[98:99], s[16:17] op_sel_hi:[1,0]
	v_pk_mul_f32 v[96:97], v[96:97], s[16:17] op_sel_hi:[1,0]
	v_pk_mul_f32 v[94:95], v[94:95], s[16:17] op_sel_hi:[1,0]
	v_pk_mul_f32 v[92:93], v[92:93], s[16:17] op_sel_hi:[1,0]
	v_pk_mul_f32 v[90:91], v[90:91], s[16:17] op_sel_hi:[1,0]
	v_pk_mul_f32 v[114:115], v[80:81], s[16:17] op_sel_hi:[1,0]
	v_pk_mul_f32 v[116:117], v[78:79], s[16:17] op_sel_hi:[1,0]
	v_pk_mul_f32 v[122:123], v[72:73], s[16:17] op_sel_hi:[1,0]
	v_pk_mul_f32 v[124:125], v[70:71], s[16:17] op_sel_hi:[1,0]
	v_pk_mul_f32 v[70:71], v[88:89], s[16:17] op_sel_hi:[1,0]
	v_pk_mul_f32 v[72:73], v[86:87], s[16:17] op_sel_hi:[1,0]
	v_pk_mul_f32 v[78:79], v[84:85], s[16:17] op_sel_hi:[1,0]
	v_pk_mul_f32 v[80:81], v[82:83], s[16:17] op_sel_hi:[1,0]
	v_pk_mul_f32 v[82:83], v[64:65], s[16:17] op_sel_hi:[1,0]
	v_pk_mul_f32 v[84:85], v[62:63], s[16:17] op_sel_hi:[1,0]
	v_pk_mul_f32 v[86:87], v[56:57], s[16:17] op_sel_hi:[1,0]
	v_pk_mul_f32 v[88:89], v[54:55], s[16:17] op_sel_hi:[1,0]
	v_pk_mul_f32 v[54:55], v[76:77], s[16:17] op_sel_hi:[1,0]
	v_pk_mul_f32 v[56:57], v[74:75], s[16:17] op_sel_hi:[1,0]
	v_pk_mul_f32 v[62:63], v[68:69], s[16:17] op_sel_hi:[1,0]
	v_pk_mul_f32 v[64:65], v[66:67], s[16:17] op_sel_hi:[1,0]
	v_pk_mul_f32 v[66:67], v[48:49], s[16:17] op_sel_hi:[1,0]
	v_pk_mul_f32 v[68:69], v[46:47], s[16:17] op_sel_hi:[1,0]
	v_pk_mul_f32 v[74:75], v[44:45], s[16:17] op_sel_hi:[1,0]
	v_pk_mul_f32 v[76:77], v[42:43], s[16:17] op_sel_hi:[1,0]
	v_pk_mul_f32 v[42:43], v[60:61], s[16:17] op_sel_hi:[1,0]
	v_pk_mul_f32 v[44:45], v[58:59], s[16:17] op_sel_hi:[1,0]
	v_pk_mul_f32 v[46:47], v[52:53], s[16:17] op_sel_hi:[1,0]
	v_pk_mul_f32 v[48:49], v[50:51], s[16:17] op_sel_hi:[1,0]
	v_pk_mul_f32 v[40:41], v[40:41], s[16:17] op_sel_hi:[1,0]
	v_pk_mul_f32 v[38:39], v[38:39], s[16:17] op_sel_hi:[1,0]
	v_pk_mul_f32 v[36:37], v[36:37], s[16:17] op_sel_hi:[1,0]
	v_pk_mul_f32 v[34:35], v[34:35], s[16:17] op_sel_hi:[1,0]
